# GEMM3 routing epilogue VALU trims: canonicalising v_max x,x removed or folded into the first compare-exchange, column-index packing done with one v_and_or_b32 per element (same values)
# baseline (speedup 1.0000x reference)
; #define PG8_LAS __attribute__((address_space(3)))
; #define RT_BAR() do { asm volatile("s_waitcnt lgkmcnt(0)" ::: "memory"); __builtin_amdgcn_s_barrier(); asm volatile("" ::: "memory"); } while (0)
;     __device__ __forceinline__ void fused(f32x4 (&acc)[2][2][4][2], const Unit& u, int wr, int wc, int fr, int fq, PG8_LAS unsigned char* lds, int wid, int lane) const {
;     ...
;         for (int bj = 0; bj < 2; ++bj) {
; #pragma unroll
;             for (int ai = 0; ai < 2; ++ai)
; #pragma unroll
;                 for (int m = 0; m < 4; ++m)
; #pragma unroll
;                     for (int n = 0; n < 2; ++n) {
;                         const int rw = ai * HALF + wr * 64 + m * 16 + fr, g = 8 * wc + 4 * n + fq, col = 32 * wc + 16 * n + 4 * fq;
;                         const f32x4 v = acc[ai][bj][m][n]; f32x4 p;
; #pragma unroll
;                         for (int e = 0; e < 4; ++e) p[e] = __uint_as_float((__float_as_uint(v[e]) & ~127u) | (unsigned)(col + e));
;                         *(PG8_LAS f32x4*)(tile + rw * 128 + ((g ^ fr) << 2)) = p;
;                     }
;             RT_BAR();
.LBB0_580:
	v_and_b32_e32 v128, 63, v139
	v_bfe_u32 v139, v139, 4, 2
	v_lshlrev_b32_e32 v129, 2, v139
	s_lshl_b32 s5, s52, 15
	v_lshl_or_b32 v129, s57, 5, v129
	s_movk_i32 s98, 0xff80
	v_or_b32_e32 v218, 1, v129
	v_or_b32_e32 v219, 2, v129
	v_or_b32_e32 v220, 3, v129
	v_or_b32_e32 v221, 17, v129
	v_or_b32_e32 v222, 18, v129
	v_or_b32_e32 v223, 19, v129
	s_add_i32 s22, s5, 0
	s_movk_i32 s5, 0xff80
	v_and_or_b32 v132, v124, s5, v129
	v_and_or_b32 v133, v125, s98, v218
	s_lshl_b32 s19, s57, 3
	v_and_or_b32 v134, v126, s98, v219
	v_lshlrev_b32_e32 v141, 9, v138
	v_and_or_b32 v135, v127, s98, v220
	v_bitop3_b32 v124, s19, v138, v139 bitop3:0x36
	v_add_u32_e32 v142, s22, v141
	v_lshlrev_b32_e32 v126, 4, v124
	v_add_u32_e32 v125, v142, v126
	v_or_b32_e32 v124, 16, v129
	s_barrier
	ds_write_b128 v125, v[132:135]
	v_and_or_b32 v132, v120, s5, v124
	v_and_or_b32 v133, v121, s98, v221
	v_or_b32_e32 v140, s19, v139
	v_and_or_b32 v134, v122, s98, v222
	v_and_or_b32 v135, v123, s98, v223
	v_bitop3_b32 v120, v140, v138, 4 bitop3:0x36
	v_lshlrev_b32_e32 v121, 4, v120
	v_add_u32_e32 v120, v142, v121
	v_and_or_b32 v96, v96, s5, v124
	v_and_or_b32 v97, v97, s98, v221
	v_and_or_b32 v98, v98, s98, v222
	v_and_or_b32 v99, v99, s98, v223
	ds_write_b128 v120, v[96:99] offset:24576
	v_and_or_b32 v96, v92, s5, v129
	v_and_or_b32 v100, v100, s5, v129
	v_and_or_b32 v101, v101, s98, v218
	v_and_or_b32 v102, v102, s98, v219
	v_and_or_b32 v103, v103, s98, v220
	s_add_i32 s19, s22, 0x10000
	v_and_or_b32 v97, v93, s98, v218
	ds_write_b128 v125, v[100:103] offset:24576
	v_add_u32_e32 v100, s19, v141
	v_and_or_b32 v98, v94, s98, v219
	v_and_or_b32 v94, v88, s5, v124
	v_and_or_b32 v99, v95, s98, v220
	v_add_u32_e32 v92, v100, v126
	v_and_or_b32 v95, v89, s98, v221
	ds_write_b128 v92, v[96:99]
	v_and_or_b32 v96, v90, s98, v222
	v_and_or_b32 v97, v91, s98, v223
	v_add_u32_e32 v88, v100, v121
	ds_write_b128 v88, v[94:97]
	v_and_or_b32 v94, v84, s5, v129
	s_add_i32 s19, s22, 0x12000
	v_and_or_b32 v95, v85, s98, v218
	v_add_u32_e32 v89, s19, v141
	v_and_or_b32 v96, v86, s98, v219
	v_and_or_b32 v97, v87, s98, v220
	v_add_u32_e32 v84, v89, v126
	ds_write_b128 v84, v[94:97]
	v_and_or_b32 v94, v80, s5, v124
	v_and_or_b32 v95, v81, s98, v221
	v_and_or_b32 v96, v82, s98, v222
	s_add_i32 s19, s22, 0x14000
	v_and_or_b32 v97, v83, s98, v223
	v_add_u32_e32 v80, s19, v141
	v_and_or_b32 v72, v72, s5, v124
	v_and_or_b32 v73, v73, s98, v221
	v_and_or_b32 v74, v74, s98, v222
	v_and_or_b32 v75, v75, s98, v223
	v_add_u32_e32 v86, v80, v121
	s_add_i32 s22, s22, 0x16000
	s_and_b32 s4, s53, 0xc0
	ds_write_b128 v86, v[72:75]
	v_add_u32_e32 v72, s22, v141
	v_or_b32_e32 v128, s4, v128
	s_lshl_b32 s4, s52, 4
	v_and_or_b32 v64, v64, s5, v124
	v_and_or_b32 v65, v65, s98, v221
	v_and_or_b32 v66, v66, s98, v222
	v_and_or_b32 v67, v67, s98, v223
	v_add_u32_e32 v91, v72, v121
	ds_write_b128 v91, v[64:67]
	v_or_b32_e32 v64, s4, v138
	v_lshl_add_u32 v130, v128, 9, 0
	v_lshlrev_b32_e32 v64, 4, v64
	v_add_u32_e32 v93, v130, v64
	v_bitop3_b32 v64, s4, v138, 1 bitop3:0x36
	v_and_or_b32 v116, v116, s5, v129
	v_and_or_b32 v117, v117, s98, v218
	v_and_or_b32 v118, v118, s98, v219
	v_and_or_b32 v119, v119, s98, v220
	v_and_or_b32 v112, v112, s5, v124
	v_and_or_b32 v113, v113, s98, v221
	v_and_or_b32 v114, v114, s98, v222
	v_and_or_b32 v115, v115, s98, v223
	v_and_or_b32 v108, v108, s5, v129
	v_and_or_b32 v109, v109, s98, v218
	v_and_or_b32 v110, v110, s98, v219
	v_and_or_b32 v111, v111, s98, v220
	v_and_or_b32 v104, v104, s5, v124
	v_and_or_b32 v105, v105, s98, v221
	v_and_or_b32 v106, v106, s98, v222
	v_and_or_b32 v107, v107, s98, v223
	v_add_u32_e32 v82, v89, v121
	v_and_or_b32 v76, v76, s5, v129
	v_and_or_b32 v77, v77, s98, v218
	v_and_or_b32 v78, v78, s98, v219
	v_and_or_b32 v79, v79, s98, v220
	v_add_u32_e32 v85, v80, v126
	v_and_or_b32 v68, v68, s5, v129
	v_and_or_b32 v69, v69, s98, v218
	v_and_or_b32 v70, v70, s98, v219
	v_and_or_b32 v71, v71, s98, v220
	v_add_u32_e32 v90, v72, v126
	v_lshlrev_b32_e32 v64, 4, v64
	ds_write_b128 v120, v[132:135]
	ds_write_b128 v125, v[116:119] offset:8192
	ds_write_b128 v120, v[112:115] offset:8192
	ds_write_b128 v125, v[108:111] offset:16384
	ds_write_b128 v120, v[104:107] offset:16384
	ds_write_b128 v82, v[94:97]
	ds_write_b128 v85, v[76:79]
	ds_write_b128 v90, v[68:71]
	v_add_u32_e32 v89, v130, v64
	v_bitop3_b32 v64, s4, v138, 2 bitop3:0x36
	v_bitop3_b32 v68, s4, v138, 3 bitop3:0x36
	s_waitcnt lgkmcnt(0)
	s_barrier
; #define PG8_LAS __attribute__((address_space(3)))
; #define CE(a, b) do { const float hi_ = fmaxf(a, b), lo_ = fminf(a, b); a = hi_; b = lo_; } while (0)
; __device__ __forceinline__ void sort16_desc(float (&v)[16]) {
;     CE(v[0], v[1]); CE(v[2], v[3]); CE(v[0], v[2]); CE(v[1], v[3]);
;     CE(v[1], v[2]); CE(v[4], v[5]); CE(v[6], v[7]); CE(v[4], v[6]);
;     CE(v[5], v[7]); CE(v[5], v[6]); CE(v[0], v[4]); CE(v[2], v[6]);
;     CE(v[2], v[4]); CE(v[1], v[5]); CE(v[3], v[7]); CE(v[3], v[5]);
;     __device__ __forceinline__ void fused(f32x4 (&acc)[2][2][4][2], const Unit& u, int wr, int wc, int fr, int fq, PG8_LAS unsigned char* lds, int wid, int lane) const {
;     ...
;             for (int grp = 0; grp < 4; ++grp) {
;                 float nw[16];
; #pragma unroll
;                 for (int i = 0; i < 4; ++i) { const int g = half * 16 + grp * 4 + i; const f32x4 v = *(const PG8_LAS f32x4*)(tile + row * 128 + ((g ^ (row & 15)) << 2));
;                     nw[4 * i] = v[0]; nw[4 * i + 1] = v[1]; nw[4 * i + 2] = v[2]; nw[4 * i + 3] = v[3]; }
;                 sort16_desc(nw);
;                 if (grp == 0) {
; #pragma unroll
;                     for (int q = 0; q < 16; ++q) run[q] = nw[q];
;                 } else merge_top16(run, nw);
	v_lshlrev_b32_e32 v64, 4, v64
	v_lshlrev_b32_e32 v68, 4, v68
	v_add_u32_e32 v81, v130, v64
	ds_read_b128 v[64:67], v93
	v_add_u32_e32 v80, v130, v68
	ds_read_b128 v[68:71], v89
	v_mul_i32_i24_e32 v131, 0xfffffe40, v128
	s_andn2_b64 vcc, exec, s[20:21]
	s_waitcnt lgkmcnt(0)
	v_min_f32_e32 v74, v64, v65
	v_max_f32_e32 v72, v64, v65
	v_min_f32_e32 v77, v66, v67
	v_max_f32_e32 v73, v66, v67
	v_min_f32_e32 v87, v68, v69
	v_max_f32_e32 v79, v68, v69
	v_min_f32_e32 v96, v70, v71
	v_max_f32_e32 v83, v70, v71
	ds_read_b128 v[64:67], v81
	ds_read_b128 v[68:71], v80
	s_waitcnt lgkmcnt(0)
	v_min_f32_e32 v99, v64, v65
	v_min_f32_e32 v100, v66, v67
	v_min_f32_e32 v102, v68, v69
	v_min_f32_e32 v103, v70, v71
	v_max_f32_e32 v64, v64, v65
	v_max_f32_e32 v65, v66, v67
	v_max_f32_e32 v68, v68, v69
	v_max_f32_e32 v69, v70, v71
	v_min_f32_e32 v78, v74, v77
	v_min_f32_e32 v97, v87, v96
	v_min_f32_e32 v101, v99, v100
	v_max_f32_e32 v74, v74, v77
	v_min_f32_e32 v75, v72, v73
	v_max_f32_e32 v77, v87, v96
	v_min_f32_e32 v87, v79, v83
	v_max_f32_e32 v99, v99, v100
	v_min_f32_e32 v66, v64, v65
	v_max_f32_e32 v100, v102, v103
	v_min_f32_e32 v70, v68, v69
	v_min_f32_e32 v104, v102, v103
	v_max_f32_e32 v76, v74, v75
	v_max_f32_e32 v94, v77, v87
	v_max_f32_e32 v67, v99, v66
	v_max_f32_e32 v71, v100, v70
	v_min_f32_e32 v98, v78, v97
	v_min_f32_e32 v105, v101, v104
	v_max_f32_e32 v78, v78, v97
	v_min_f32_e32 v95, v76, v94
	v_min_f32_e32 v74, v74, v75
	v_min_f32_e32 v75, v77, v87
	v_max_f32_e32 v97, v101, v104
	v_min_f32_e32 v101, v67, v71
	v_min_f32_e32 v66, v99, v66
	v_min_f32_e32 v70, v100, v70
	v_max_f32_e32 v96, v78, v95
	v_max_f32_e32 v77, v74, v75
	v_max_f32_e32 v72, v72, v73
	v_max_f32_e32 v73, v79, v83
	v_max_f32_e32 v99, v66, v70
	v_max_f32_e32 v64, v64, v65
	v_max_f32_e32 v65, v68, v69
	v_min_f32_e32 v78, v78, v95
	v_min_f32_e32 v74, v74, v75
	v_min_f32_e32 v95, v97, v101
	v_min_f32_e32 v66, v66, v70
	v_min_f32_e32 v79, v72, v73
	v_min_f32_e32 v68, v64, v65
	v_max_f32_e32 v75, v78, v74
	v_max_f32_e32 v70, v95, v66
	v_min_f32_e32 v74, v78, v74
	v_min_f32_e32 v66, v95, v66
	v_min_f32_e32 v83, v77, v79
	v_max_f32_e32 v102, v97, v101
	v_min_f32_e32 v69, v99, v68
	v_min_f32_e32 v78, v74, v66
	v_max_f32_e32 v66, v74, v66
	v_max_f32_e32 v74, v76, v94
	v_max_f32_e32 v76, v77, v79
	v_max_f32_e32 v67, v67, v71
	v_max_f32_e32 v68, v99, v68
	v_max_f32_e32 v87, v96, v83
	v_max_f32_e32 v100, v102, v69
	v_min_f32_e32 v77, v74, v76
	v_min_f32_e32 v71, v67, v68
	v_min_f32_e32 v83, v96, v83
	v_min_f32_e32 v69, v102, v69
	v_max_f32_e32 v72, v72, v73
	v_max_f32_e32 v73, v64, v65
	v_min_f32_e32 v79, v77, v71
	v_min_f32_e32 v96, v83, v69
	v_max_f32_e32 v69, v83, v69
	v_min_f32_e32 v64, v72, v73
	v_min_f32_e32 v94, v66, v79
	v_max_f32_e32 v66, v66, v79
	v_min_f32_e32 v65, v69, v64
	v_max_f32_e32 v74, v74, v76
	v_max_f32_e32 v67, v67, v68
	v_min_f32_e32 v79, v66, v65
	v_max_f32_e32 v107, v66, v65
	v_max_f32_e32 v65, v77, v71
	v_max_f32_e32 v64, v69, v64
	v_max_f32_e32 v106, v98, v105
	v_min_f32_e32 v103, v87, v100
	v_min_f32_e32 v97, v75, v70
	v_max_f32_e32 v70, v75, v70
	v_min_f32_e32 v68, v74, v67
	v_min_f32_e32 v77, v65, v64
	v_max_f32_e32 v111, v65, v64
	v_bitop3_b32 v64, s4, v138, 4 bitop3:0x36
	v_max_f32_e32 v99, v106, v103
	v_min_f32_e32 v75, v70, v68
	v_lshlrev_b32_e32 v64, 4, v64
	v_min_f32_e32 v76, v99, v75
	v_max_f32_e32 v75, v99, v75
	v_add_u32_e32 v99, v130, v64
	v_bitop3_b32 v64, s4, v138, 5 bitop3:0x36
	v_max_f32_e32 v83, v87, v100
	v_max_f32_e32 v68, v70, v68
	v_lshlrev_b32_e32 v64, 4, v64
	v_min_f32_e32 v102, v94, v96
	v_max_f32_e32 v94, v94, v96
	v_min_f32_e32 v100, v83, v68
	v_max_f32_e32 v109, v83, v68
	v_add_u32_e32 v96, v130, v64
	v_bitop3_b32 v64, s4, v138, 6 bitop3:0x36
	v_bitop3_b32 v68, s4, v138, 7 bitop3:0x36
	v_lshlrev_b32_e32 v64, 4, v64
	v_lshlrev_b32_e32 v68, 4, v68
	v_max_f32_e32 v74, v74, v67
	v_add_u32_e32 v87, v130, v64
	ds_read_b128 v[64:67], v99
	v_add_u32_e32 v83, v130, v68
	ds_read_b128 v[68:71], v96
	v_min_f32_e32 v98, v98, v105
	v_min_f32_e32 v104, v106, v103
	s_waitcnt lgkmcnt(0)
	v_min_f32_e32 v114, v64, v65
	v_max_f32_e32 v105, v64, v65
	v_min_f32_e32 v117, v66, v67
	v_max_f32_e32 v113, v66, v67
	v_min_f32_e32 v122, v68, v69
	v_max_f32_e32 v119, v68, v69
	v_min_f32_e32 v127, v70, v71
	v_max_f32_e32 v121, v70, v71
	ds_read_b128 v[64:67], v87
	ds_read_b128 v[68:71], v83
	s_waitcnt lgkmcnt(0)
; #define PG8_LAS __attribute__((address_space(3)))
;     __device__ __forceinline__ void fused(f32x4 (&acc)[2][2][4][2], const Unit& u, int wr, int wc, int fr, int fq, PG8_LAS unsigned char* lds, int wid, int lane) const {
;     ...
;             for (int grp = 0; grp < 4; ++grp) {
;                 float nw[16];
; #pragma unroll
;                 for (int i = 0; i < 4; ++i) { const int g = half * 16 + grp * 4 + i; const f32x4 v = *(const PG8_LAS f32x4*)(tile + row * 128 + ((g ^ (row & 15)) << 2));
;                     nw[4 * i] = v[0]; nw[4 * i + 1] = v[1]; nw[4 * i + 2] = v[2]; nw[4 * i + 3] = v[3]; }
;                 sort16_desc(nw);
;                 if (grp == 0) {
; #pragma unroll
;                     for (int q = 0; q < 16; ++q) run[q] = nw[q];
;                 } else merge_top16(run, nw);
	v_min_f32_e32 v134, v64, v65
	v_min_f32_e32 v135, v66, v67
	v_min_f32_e32 v140, v68, v69
	v_min_f32_e32 v141, v70, v71
	v_max_f32_e32 v64, v64, v65
	v_max_f32_e32 v65, v66, v67
	v_max_f32_e32 v68, v68, v69
	v_max_f32_e32 v69, v70, v71
	v_min_f32_e32 v118, v114, v117
	v_min_f32_e32 v132, v122, v127
	v_min_f32_e32 v139, v134, v135
	v_max_f32_e32 v114, v114, v117
	v_min_f32_e32 v115, v105, v113
	v_max_f32_e32 v117, v122, v127
	v_min_f32_e32 v122, v119, v121
	v_max_f32_e32 v134, v134, v135
	v_min_f32_e32 v66, v64, v65
	v_max_f32_e32 v135, v140, v141
	v_min_f32_e32 v70, v68, v69
	v_min_f32_e32 v142, v140, v141
	v_max_f32_e32 v116, v114, v115
	v_max_f32_e32 v123, v117, v122
	v_max_f32_e32 v67, v134, v66
	v_max_f32_e32 v71, v135, v70
	v_min_f32_e32 v133, v118, v132
	v_min_f32_e32 v143, v139, v142
	v_max_f32_e32 v118, v118, v132
	v_min_f32_e32 v126, v116, v123
	v_min_f32_e32 v114, v114, v115
	v_min_f32_e32 v115, v117, v122
	v_max_f32_e32 v132, v139, v142
	v_min_f32_e32 v139, v67, v71
	v_min_f32_e32 v66, v134, v66
	v_min_f32_e32 v70, v135, v70
	v_max_f32_e32 v127, v118, v126
	v_max_f32_e32 v117, v114, v115
	v_max_f32_e32 v105, v105, v113
	v_max_f32_e32 v113, v119, v121
	v_max_f32_e32 v134, v66, v70
	v_max_f32_e32 v64, v64, v65
	v_max_f32_e32 v65, v68, v69
	v_min_f32_e32 v118, v118, v126
	v_min_f32_e32 v114, v114, v115
	v_min_f32_e32 v126, v132, v139
	v_min_f32_e32 v66, v66, v70
	v_min_f32_e32 v119, v105, v113
	v_min_f32_e32 v68, v64, v65
	v_max_f32_e32 v115, v118, v114
	v_max_f32_e32 v70, v126, v66
	v_min_f32_e32 v114, v118, v114
	v_min_f32_e32 v66, v126, v66
	v_min_f32_e32 v121, v117, v119
	v_max_f32_e32 v140, v132, v139
	v_min_f32_e32 v69, v134, v68
	v_min_f32_e32 v118, v114, v66
	v_max_f32_e32 v66, v114, v66
	v_max_f32_e32 v114, v116, v123
	v_max_f32_e32 v116, v117, v119
	v_max_f32_e32 v67, v67, v71
	v_max_f32_e32 v68, v134, v68
	v_max_f32_e32 v122, v127, v121
	v_max_f32_e32 v135, v140, v69
	v_min_f32_e32 v117, v114, v116
	v_min_f32_e32 v71, v67, v68
	v_min_f32_e32 v121, v127, v121
	v_min_f32_e32 v69, v140, v69
	v_max_f32_e32 v114, v114, v116
	v_max_f32_e32 v67, v67, v68
	v_max_f32_e32 v105, v105, v113
	v_max_f32_e32 v64, v64, v65
	v_max_f32_e32 v144, v133, v143
	v_min_f32_e32 v141, v122, v135
	v_min_f32_e32 v132, v115, v70
	v_min_f32_e32 v119, v117, v71
	v_min_f32_e32 v127, v121, v69
	v_max_f32_e32 v70, v115, v70
	v_min_f32_e32 v68, v114, v67
	v_max_f32_e32 v69, v121, v69
	v_min_f32_e32 v65, v105, v64
	v_min_f32_e32 v142, v144, v141
	v_min_f32_e32 v123, v66, v119
	v_max_f32_e32 v141, v144, v141
	v_min_f32_e32 v115, v70, v68
	v_max_f32_e32 v66, v66, v119
	v_min_f32_e32 v113, v69, v65
	v_max_f32_e32 v122, v122, v135
	v_max_f32_e32 v68, v70, v68
	v_max_f32_e32 v71, v117, v71
	v_max_f32_e32 v65, v69, v65
	v_min_f32_e32 v101, v104, v97
	v_max_f32_e32 v97, v104, v97
	v_min_f32_e32 v139, v142, v132
	v_max_f32_e32 v132, v142, v132
	v_min_f32_e32 v134, v123, v127
	v_min_f32_e32 v116, v141, v115
	v_max_f32_e32 v123, v123, v127
	v_max_f32_e32 v115, v141, v115
	v_min_f32_e32 v119, v66, v113
	v_min_f32_e32 v70, v122, v68
	v_max_f32_e32 v66, v66, v113
	v_max_f32_e32 v68, v122, v68
	v_min_f32_e32 v69, v71, v65
	v_max_f32_e32 v67, v114, v67
	v_max_f32_e32 v65, v71, v65
	v_min_f32_e32 v95, v101, v78
	v_min_f32_e32 v104, v97, v102
	v_min_f32_e32 v103, v76, v94
	v_min_f32_e32 v106, v75, v79
	v_min_f32_e32 v108, v100, v107
	v_min_f32_e32 v110, v109, v77
	v_min_f32_e32 v112, v74, v111
	v_min_f32_e32 v126, v139, v118
	v_min_f32_e32 v140, v132, v134
	v_min_f32_e32 v127, v116, v123
	v_min_f32_e32 v121, v115, v119
	v_min_f32_e32 v113, v70, v66
	v_min_f32_e32 v117, v68, v69
	v_min_f32_e32 v71, v67, v65
	v_min_f32_e32 v114, v133, v143
	v_max3_f32 v72, v72, v73, v114
	v_max3_f32 v73, v74, v111, v126
	v_max3_f32 v74, v112, v139, v118
	v_max3_f32 v77, v109, v77, v140
	v_max3_f32 v109, v110, v132, v134
	v_max3_f32 v100, v100, v107, v127
	v_max3_f32 v107, v108, v116, v123
	v_max3_f32 v75, v75, v79, v121
	v_max3_f32 v79, v106, v115, v119
	v_max3_f32 v76, v76, v94, v113
	v_max3_f32 v66, v103, v70, v66
	v_max3_f32 v70, v97, v102, v117
	v_max3_f32 v68, v104, v68, v69
	v_max3_f32 v69, v101, v78, v71
	v_max3_f32 v65, v95, v67, v65
	v_max3_f32 v64, v98, v105, v64
	v_max_f32_e32 v67, v72, v79
	v_min_f32_e32 v71, v72, v79
	v_max_f32_e32 v72, v73, v76
	v_min_f32_e32 v73, v73, v76
	v_max_f32_e32 v76, v74, v66
	v_min_f32_e32 v66, v74, v66
	v_max_f32_e32 v74, v77, v70
	v_min_f32_e32 v70, v77, v70
	v_max_f32_e32 v77, v109, v68
	v_min_f32_e32 v68, v109, v68
	v_max_f32_e32 v78, v100, v69
	v_min_f32_e32 v69, v100, v69
	v_max_f32_e32 v79, v107, v65
	v_min_f32_e32 v65, v107, v65
	v_max_f32_e32 v94, v75, v64
	v_min_f32_e32 v64, v75, v64
	v_max_f32_e32 v75, v67, v77
	v_min_f32_e32 v67, v67, v77
	v_max_f32_e32 v77, v72, v78
	v_min_f32_e32 v72, v72, v78
	v_max_f32_e32 v78, v76, v79
	v_min_f32_e32 v76, v76, v79
	v_max_f32_e32 v79, v74, v94
	v_min_f32_e32 v74, v74, v94
	v_max_f32_e32 v94, v71, v68
	v_min_f32_e32 v68, v71, v68
	v_max_f32_e32 v71, v73, v69
	v_min_f32_e32 v69, v73, v69
	v_max_f32_e32 v73, v66, v65
	v_min_f32_e32 v65, v66, v65
	v_max_f32_e32 v66, v70, v64
	v_min_f32_e32 v64, v70, v64
	v_max_f32_e32 v106, v69, v64
	v_min_f32_e32 v107, v69, v64
	v_bitop3_b32 v64, s4, v138, 8 bitop3:0x36
	v_lshlrev_b32_e32 v64, 4, v64
	v_add_u32_e32 v102, v130, v64
	v_bitop3_b32 v64, s4, v138, 9 bitop3:0x36
	v_lshlrev_b32_e32 v64, 4, v64
	v_max_f32_e32 v104, v68, v65
	v_min_f32_e32 v105, v68, v65
	v_add_u32_e32 v101, v130, v64
	v_bitop3_b32 v64, s4, v138, 10 bitop3:0x36
	v_bitop3_b32 v68, s4, v138, 11 bitop3:0x36
	v_lshlrev_b32_e32 v64, 4, v64
	v_lshlrev_b32_e32 v68, 4, v68
	v_max_f32_e32 v97, v75, v78
	v_min_f32_e32 v75, v75, v78
	v_max_f32_e32 v78, v77, v79
	v_min_f32_e32 v77, v77, v79
	v_max_f32_e32 v79, v67, v76
	v_min_f32_e32 v76, v67, v76
	v_max_f32_e32 v98, v72, v74
	v_min_f32_e32 v72, v72, v74
	v_max_f32_e32 v74, v94, v73
	v_min_f32_e32 v73, v94, v73
	v_max_f32_e32 v100, v71, v66
	v_min_f32_e32 v103, v71, v66
	v_add_u32_e32 v95, v130, v64
	ds_read_b128 v[64:67], v102
	v_add_u32_e32 v94, v130, v68
	ds_read_b128 v[68:71], v101
	v_min_f32_e32 v108, v97, v78
	v_min_f32_e32 v109, v75, v77
	s_waitcnt lgkmcnt(0)
; #define PG8_LAS __attribute__((address_space(3)))
;     __device__ __forceinline__ void fused(f32x4 (&acc)[2][2][4][2], const Unit& u, int wr, int wc, int fr, int fq, PG8_LAS unsigned char* lds, int wid, int lane) const {
;     ...
;             for (int grp = 0; grp < 4; ++grp) {
;                 float nw[16];
; #pragma unroll
;                 for (int i = 0; i < 4; ++i) { const int g = half * 16 + grp * 4 + i; const f32x4 v = *(const PG8_LAS f32x4*)(tile + row * 128 + ((g ^ (row & 15)) << 2));
;                     nw[4 * i] = v[0]; nw[4 * i + 1] = v[1]; nw[4 * i + 2] = v[2]; nw[4 * i + 3] = v[3]; }
;                 sort16_desc(nw);
;                 if (grp == 0) {
; #pragma unroll
;                     for (int q = 0; q < 16; ++q) run[q] = nw[q];
;                 } else merge_top16(run, nw);
	v_min_f32_e32 v118, v64, v65
	v_max_f32_e32 v116, v64, v65
	v_min_f32_e32 v122, v66, v67
	v_max_f32_e32 v117, v66, v67
	v_min_f32_e32 v132, v68, v69
	v_max_f32_e32 v126, v68, v69
	v_min_f32_e32 v135, v70, v71
	v_max_f32_e32 v127, v70, v71
	ds_read_b128 v[64:67], v95
	ds_read_b128 v[68:71], v94
	s_waitcnt lgkmcnt(0)
	v_min_f32_e32 v141, v64, v65
	v_min_f32_e32 v142, v66, v67
	v_min_f32_e32 v144, v68, v69
	v_min_f32_e32 v145, v70, v71
	v_max_f32_e32 v64, v64, v65
	v_max_f32_e32 v65, v66, v67
	v_max_f32_e32 v68, v68, v69
	v_max_f32_e32 v69, v70, v71
	v_min_f32_e32 v123, v118, v122
	v_min_f32_e32 v139, v132, v135
	v_min_f32_e32 v143, v141, v142
	v_max_f32_e32 v118, v118, v122
	v_min_f32_e32 v119, v116, v117
	v_max_f32_e32 v122, v132, v135
	v_min_f32_e32 v132, v126, v127
	v_max_f32_e32 v141, v141, v142
	v_min_f32_e32 v66, v64, v65
	v_max_f32_e32 v142, v144, v145
	v_min_f32_e32 v70, v68, v69
	v_min_f32_e32 v146, v144, v145
	v_max_f32_e32 v121, v118, v119
	v_max_f32_e32 v133, v122, v132
	v_max_f32_e32 v67, v141, v66
	v_max_f32_e32 v71, v142, v70
	v_min_f32_e32 v140, v123, v139
	v_min_f32_e32 v147, v143, v146
	v_max_f32_e32 v123, v123, v139
	v_min_f32_e32 v134, v121, v133
	v_min_f32_e32 v118, v118, v119
	v_min_f32_e32 v119, v122, v132
	v_max_f32_e32 v139, v143, v146
	v_min_f32_e32 v143, v67, v71
	v_min_f32_e32 v66, v141, v66
	v_min_f32_e32 v70, v142, v70
	v_max_f32_e32 v135, v123, v134
	v_max_f32_e32 v122, v118, v119
	v_max_f32_e32 v116, v116, v117
	v_max_f32_e32 v117, v126, v127
	v_max_f32_e32 v141, v66, v70
	v_max_f32_e32 v64, v64, v65
	v_max_f32_e32 v65, v68, v69
	v_min_f32_e32 v123, v123, v134
	v_min_f32_e32 v118, v118, v119
	v_min_f32_e32 v134, v139, v143
	v_min_f32_e32 v66, v66, v70
	v_min_f32_e32 v126, v116, v117
	v_min_f32_e32 v68, v64, v65
	v_max_f32_e32 v119, v123, v118
	v_max_f32_e32 v70, v134, v66
	v_min_f32_e32 v118, v123, v118
	v_min_f32_e32 v66, v134, v66
	v_min_f32_e32 v127, v122, v126
	v_max_f32_e32 v144, v139, v143
	v_min_f32_e32 v69, v141, v68
	v_min_f32_e32 v123, v118, v66
	v_max_f32_e32 v66, v118, v66
	v_max_f32_e32 v118, v121, v133
	v_max_f32_e32 v121, v122, v126
	v_max_f32_e32 v67, v67, v71
	v_max_f32_e32 v68, v141, v68
	v_max_f32_e32 v132, v135, v127
	v_max_f32_e32 v142, v144, v69
	v_min_f32_e32 v122, v118, v121
	v_min_f32_e32 v71, v67, v68
	v_max_f32_e32 v148, v140, v147
	v_min_f32_e32 v145, v132, v142
	v_min_f32_e32 v126, v122, v71
	v_min_f32_e32 v127, v135, v127
	v_min_f32_e32 v69, v144, v69
	v_min_f32_e32 v146, v148, v145
	v_min_f32_e32 v139, v119, v70
	v_min_f32_e32 v133, v66, v126
	v_min_f32_e32 v135, v127, v69
	v_max_f32_e32 v118, v118, v121
	v_max_f32_e32 v67, v67, v68
	v_max_f32_e32 v116, v116, v117
	v_max_f32_e32 v64, v64, v65
	v_min_f32_e32 v143, v146, v139
	v_max_f32_e32 v139, v146, v139
	v_min_f32_e32 v141, v133, v135
	v_max_f32_e32 v70, v119, v70
	v_min_f32_e32 v68, v118, v67
	v_max_f32_e32 v69, v127, v69
	v_min_f32_e32 v65, v116, v64
	v_min_f32_e32 v134, v143, v123
	v_max_f32_e32 v123, v143, v123
	v_min_f32_e32 v143, v139, v141
	v_max_f32_e32 v139, v139, v141
	v_max_f32_e32 v141, v148, v145
	v_min_f32_e32 v119, v70, v68
	v_max_f32_e32 v66, v66, v126
	v_min_f32_e32 v117, v69, v65
	v_min_f32_e32 v121, v141, v119
	v_max_f32_e32 v119, v141, v119
	v_min_f32_e32 v126, v66, v117
	v_min_f32_e32 v127, v119, v126
	v_max_f32_e32 v119, v119, v126
	v_max_f32_e32 v126, v132, v142
	v_max_f32_e32 v68, v70, v68
	v_min_f32_e32 v70, v126, v68
	v_max_f32_e32 v66, v66, v117
	v_min_f32_e32 v117, v70, v66
	v_max_f32_e32 v66, v70, v66
	v_max_f32_e32 v70, v122, v71
	v_max_f32_e32 v65, v69, v65
	v_max_f32_e32 v133, v133, v135
	v_max_f32_e32 v68, v126, v68
	v_min_f32_e32 v69, v70, v65
	v_max_f32_e32 v67, v118, v67
	v_max_f32_e32 v65, v70, v65
	v_min_f32_e32 v110, v79, v98
	v_min_f32_e32 v111, v76, v72
	v_min_f32_e32 v112, v74, v100
	v_min_f32_e32 v113, v73, v103
	v_min_f32_e32 v114, v104, v106
	v_min_f32_e32 v115, v105, v107
	v_min_f32_e32 v135, v121, v133
	v_max_f32_e32 v121, v121, v133
	v_min_f32_e32 v71, v68, v69
	v_max_f32_e32 v68, v68, v69
	v_min_f32_e32 v69, v67, v65
	v_max_f32_e32 v65, v67, v65
	v_min_f32_e32 v67, v140, v147
	v_max3_f32 v67, v97, v78, v67
	v_max_f32_e32 v70, v108, v134
	v_max3_f32 v75, v75, v77, v123
	v_max_f32_e32 v77, v109, v143
	v_max3_f32 v78, v79, v98, v139
	v_max_f32_e32 v79, v110, v135
	v_max3_f32 v72, v76, v72, v121
	v_max_f32_e32 v76, v111, v127
	v_max3_f32 v74, v74, v100, v119
	v_max_f32_e32 v97, v112, v117
	v_max3_f32 v66, v73, v103, v66
	v_max_f32_e32 v71, v113, v71
	v_max3_f32 v68, v104, v106, v68
	v_max_f32_e32 v69, v114, v69
	v_max3_f32 v65, v105, v107, v65
	v_max3_f32 v64, v115, v116, v64
	v_max_f32_e32 v73, v67, v74
	v_min_f32_e32 v67, v67, v74
	v_max_f32_e32 v74, v70, v97
	v_min_f32_e32 v70, v70, v97
	v_max_f32_e32 v97, v75, v66
	v_min_f32_e32 v66, v75, v66
	v_max_f32_e32 v75, v77, v71
	v_min_f32_e32 v71, v77, v71
	v_max_f32_e32 v77, v78, v68
	v_min_f32_e32 v68, v78, v68
	v_max_f32_e32 v78, v79, v69
	v_min_f32_e32 v69, v79, v69
	v_max_f32_e32 v79, v72, v65
	v_min_f32_e32 v65, v72, v65
	v_max_f32_e32 v72, v76, v64
	v_min_f32_e32 v64, v76, v64
	v_max_f32_e32 v76, v73, v77
	v_min_f32_e32 v73, v73, v77
	v_max_f32_e32 v77, v74, v78
	v_min_f32_e32 v74, v74, v78
	v_max_f32_e32 v78, v97, v79
	v_min_f32_e32 v79, v97, v79
	v_max_f32_e32 v97, v75, v72
	v_min_f32_e32 v72, v75, v72
	v_max_f32_e32 v75, v67, v68
	v_min_f32_e32 v67, v67, v68
	v_max_f32_e32 v68, v70, v69
	v_min_f32_e32 v69, v70, v69
	v_max_f32_e32 v70, v66, v65
	v_min_f32_e32 v65, v66, v65
	v_max_f32_e32 v66, v71, v64
	v_min_f32_e32 v64, v71, v64
	v_max_f32_e32 v110, v69, v64
	v_min_f32_e32 v111, v69, v64
	v_bitop3_b32 v64, s4, v138, 12 bitop3:0x36
	v_lshlrev_b32_e32 v64, 4, v64
	v_add_u32_e32 v104, v130, v64
	v_bitop3_b32 v64, s4, v138, 13 bitop3:0x36
	v_lshlrev_b32_e32 v64, 4, v64
	v_max_f32_e32 v106, v68, v66
	v_min_f32_e32 v107, v68, v66
	v_add_u32_e32 v103, v130, v64
	v_bitop3_b32 v64, s4, v138, 14 bitop3:0x36
	v_bitop3_b32 v68, s4, v138, 15 bitop3:0x36
	v_lshlrev_b32_e32 v64, 4, v64
	v_lshlrev_b32_e32 v68, 4, v68
	v_max_f32_e32 v105, v76, v78
	v_min_f32_e32 v76, v76, v78
	v_max_f32_e32 v78, v77, v97
	v_min_f32_e32 v77, v77, v97
	v_max_f32_e32 v97, v73, v79
	v_min_f32_e32 v73, v73, v79
	v_max_f32_e32 v79, v74, v72
	v_min_f32_e32 v72, v74, v72
	v_max_f32_e32 v74, v75, v70
	v_min_f32_e32 v75, v75, v70
	v_max_f32_e32 v108, v67, v65
	v_min_f32_e32 v109, v67, v65
	v_add_u32_e32 v100, v130, v64
	ds_read_b128 v[64:67], v104
	v_add_u32_e32 v98, v130, v68
	ds_read_b128 v[68:71], v103
	v_min_f32_e32 v112, v105, v78
	v_min_f32_e32 v113, v76, v77
	s_waitcnt lgkmcnt(0)
; #define PG8_LAS __attribute__((address_space(3)))
; #define RT_BAR() do { asm volatile("s_waitcnt lgkmcnt(0)" ::: "memory"); __builtin_amdgcn_s_barrier(); asm volatile("" ::: "memory"); } while (0)
;     __device__ __forceinline__ void fused(f32x4 (&acc)[2][2][4][2], const Unit& u, int wr, int wc, int fr, int fq, PG8_LAS unsigned char* lds, int wid, int lane) const {
;     ...
;             for (int grp = 0; grp < 4; ++grp) {
;                 float nw[16];
; #pragma unroll
;                 for (int i = 0; i < 4; ++i) { const int g = half * 16 + grp * 4 + i; const f32x4 v = *(const PG8_LAS f32x4*)(tile + row * 128 + ((g ^ (row & 15)) << 2));
;                     nw[4 * i] = v[0]; nw[4 * i + 1] = v[1]; nw[4 * i + 2] = v[2]; nw[4 * i + 3] = v[3]; }
;                 sort16_desc(nw);
;                 if (grp == 0) {
; #pragma unroll
;                     for (int q = 0; q < 16; ++q) run[q] = nw[q];
;                 } else merge_top16(run, nw);
;             }
;             RT_BAR();
;             if (half == 1) {
; #pragma unroll
;                 for (int i = 0; i < 4; ++i) *(PG8_LAS f32x4*)(tile + row * 16 + 4 * i) = (f32x4){run[4 * i], run[4 * i + 1], run[4 * i + 2], run[4 * i + 3]};
;             }
	v_min_f32_e32 v123, v64, v65
	v_max_f32_e32 v121, v64, v65
	v_min_f32_e32 v132, v66, v67
	v_max_f32_e32 v122, v66, v67
	v_min_f32_e32 v138, v68, v69
	v_max_f32_e32 v134, v68, v69
	v_min_f32_e32 v141, v70, v71
	v_max_f32_e32 v135, v70, v71
	ds_read_b128 v[64:67], v100
	ds_read_b128 v[68:71], v98
	s_waitcnt lgkmcnt(0)
	v_min_f32_e32 v144, v64, v65
	v_min_f32_e32 v145, v66, v67
	v_min_f32_e32 v147, v68, v69
	v_min_f32_e32 v148, v70, v71
	v_max_f32_e32 v64, v64, v65
	v_max_f32_e32 v65, v66, v67
	v_max_f32_e32 v68, v68, v69
	v_max_f32_e32 v69, v70, v71
	v_min_f32_e32 v133, v123, v132
	v_min_f32_e32 v142, v138, v141
	v_min_f32_e32 v146, v144, v145
	v_max_f32_e32 v123, v123, v132
	v_min_f32_e32 v126, v121, v122
	v_max_f32_e32 v132, v138, v141
	v_min_f32_e32 v138, v134, v135
	v_max_f32_e32 v144, v144, v145
	v_min_f32_e32 v66, v64, v65
	v_max_f32_e32 v145, v147, v148
	v_min_f32_e32 v70, v68, v69
	v_min_f32_e32 v149, v147, v148
	v_max_f32_e32 v127, v123, v126
	v_max_f32_e32 v139, v132, v138
	v_max_f32_e32 v67, v144, v66
	v_max_f32_e32 v71, v145, v70
	v_min_f32_e32 v143, v133, v142
	v_min_f32_e32 v150, v146, v149
	v_max_f32_e32 v133, v133, v142
	v_min_f32_e32 v140, v127, v139
	v_min_f32_e32 v123, v123, v126
	v_min_f32_e32 v126, v132, v138
	v_max_f32_e32 v142, v146, v149
	v_min_f32_e32 v146, v67, v71
	v_min_f32_e32 v66, v144, v66
	v_min_f32_e32 v70, v145, v70
	v_max_f32_e32 v141, v133, v140
	v_max_f32_e32 v132, v123, v126
	v_max_f32_e32 v121, v121, v122
	v_max_f32_e32 v122, v134, v135
	v_max_f32_e32 v144, v66, v70
	v_max_f32_e32 v64, v64, v65
	v_max_f32_e32 v65, v68, v69
	v_min_f32_e32 v133, v133, v140
	v_min_f32_e32 v123, v123, v126
	v_min_f32_e32 v140, v142, v146
	v_min_f32_e32 v66, v66, v70
	v_min_f32_e32 v134, v121, v122
	v_min_f32_e32 v68, v64, v65
	v_max_f32_e32 v126, v133, v123
	v_max_f32_e32 v70, v140, v66
	v_min_f32_e32 v123, v133, v123
	v_min_f32_e32 v66, v140, v66
	v_min_f32_e32 v135, v132, v134
	v_max_f32_e32 v147, v142, v146
	v_min_f32_e32 v69, v144, v68
	v_min_f32_e32 v133, v123, v66
	v_max_f32_e32 v66, v123, v66
	v_max_f32_e32 v123, v127, v139
	v_max_f32_e32 v127, v132, v134
	v_max_f32_e32 v67, v67, v71
	v_max_f32_e32 v68, v144, v68
	v_max_f32_e32 v138, v141, v135
	v_max_f32_e32 v145, v147, v69
	v_min_f32_e32 v132, v123, v127
	v_min_f32_e32 v71, v67, v68
	v_max_f32_e32 v151, v143, v150
	v_min_f32_e32 v148, v138, v145
	v_min_f32_e32 v134, v132, v71
	v_min_f32_e32 v135, v141, v135
	v_min_f32_e32 v69, v147, v69
	v_min_f32_e32 v149, v151, v148
	v_min_f32_e32 v142, v126, v70
	v_min_f32_e32 v139, v66, v134
	v_min_f32_e32 v141, v135, v69
	v_max_f32_e32 v123, v123, v127
	v_max_f32_e32 v67, v67, v68
	v_max_f32_e32 v121, v121, v122
	v_max_f32_e32 v64, v64, v65
	v_min_f32_e32 v146, v149, v142
	v_max_f32_e32 v142, v149, v142
	v_min_f32_e32 v144, v139, v141
	v_max_f32_e32 v70, v126, v70
	v_min_f32_e32 v68, v123, v67
	v_max_f32_e32 v69, v135, v69
	v_min_f32_e32 v65, v121, v64
	v_min_f32_e32 v140, v146, v133
	v_max_f32_e32 v133, v146, v133
	v_min_f32_e32 v146, v142, v144
	v_max_f32_e32 v142, v142, v144
	v_max_f32_e32 v144, v151, v148
	v_min_f32_e32 v126, v70, v68
	v_max_f32_e32 v66, v66, v134
	v_min_f32_e32 v122, v69, v65
	v_min_f32_e32 v127, v144, v126
	v_max_f32_e32 v126, v144, v126
	v_min_f32_e32 v134, v66, v122
	v_min_f32_e32 v135, v126, v134
	v_max_f32_e32 v126, v126, v134
	v_max_f32_e32 v134, v138, v145
	v_max_f32_e32 v68, v70, v68
	v_min_f32_e32 v70, v134, v68
	v_max_f32_e32 v66, v66, v122
	v_min_f32_e32 v122, v70, v66
	v_max_f32_e32 v66, v70, v66
	v_max_f32_e32 v70, v132, v71
	v_max_f32_e32 v65, v69, v65
	v_max_f32_e32 v139, v139, v141
	v_max_f32_e32 v68, v134, v68
	v_min_f32_e32 v69, v70, v65
	v_max_f32_e32 v67, v123, v67
	v_max_f32_e32 v65, v70, v65
	v_min_f32_e32 v114, v97, v79
	v_min_f32_e32 v115, v73, v72
	v_min_f32_e32 v116, v74, v106
	v_min_f32_e32 v117, v75, v107
	v_min_f32_e32 v118, v108, v110
	v_min_f32_e32 v119, v109, v111
	v_min_f32_e32 v141, v127, v139
	v_max_f32_e32 v127, v127, v139
	v_min_f32_e32 v71, v68, v69
	v_max_f32_e32 v68, v68, v69
	v_min_f32_e32 v69, v67, v65
	v_max_f32_e32 v65, v67, v65
	v_min_f32_e32 v67, v143, v150
	v_max3_f32 v67, v105, v78, v67
	v_max_f32_e32 v70, v112, v140
	v_max3_f32 v76, v76, v77, v133
	v_max_f32_e32 v77, v113, v146
	v_max3_f32 v78, v97, v79, v142
	v_max_f32_e32 v79, v114, v141
	v_max3_f32 v72, v73, v72, v127
	v_max_f32_e32 v73, v115, v135
	v_max3_f32 v74, v74, v106, v126
	v_max_f32_e32 v97, v116, v122
	v_max3_f32 v66, v75, v107, v66
	v_max_f32_e32 v71, v117, v71
	v_max3_f32 v68, v108, v110, v68
	v_max_f32_e32 v69, v118, v69
	v_max3_f32 v65, v109, v111, v65
	v_max3_f32 v64, v119, v121, v64
	v_max_f32_e32 v75, v67, v74
	v_min_f32_e32 v67, v67, v74
	v_max_f32_e32 v74, v70, v97
	v_min_f32_e32 v70, v70, v97
	v_max_f32_e32 v97, v76, v66
	v_min_f32_e32 v66, v76, v66
	v_max_f32_e32 v76, v77, v71
	v_min_f32_e32 v71, v77, v71
	v_max_f32_e32 v77, v78, v68
	v_min_f32_e32 v68, v78, v68
	v_max_f32_e32 v78, v79, v69
	v_min_f32_e32 v69, v79, v69
	v_max_f32_e32 v79, v72, v65
	v_min_f32_e32 v65, v72, v65
	v_max_f32_e32 v72, v73, v64
	v_min_f32_e32 v64, v73, v64
	v_max_f32_e32 v73, v75, v77
	v_min_f32_e32 v75, v75, v77
	v_max_f32_e32 v77, v74, v78
	v_min_f32_e32 v74, v74, v78
	v_max_f32_e32 v78, v97, v79
	v_min_f32_e32 v79, v97, v79
	v_max_f32_e32 v97, v76, v72
	v_min_f32_e32 v72, v76, v72
	v_max_f32_e32 v76, v67, v68
	v_min_f32_e32 v67, v67, v68
	v_max_f32_e32 v68, v70, v69
	v_min_f32_e32 v69, v70, v69
	v_max_f32_e32 v70, v66, v65
	v_min_f32_e32 v65, v66, v65
	v_max_f32_e32 v66, v71, v64
	v_min_f32_e32 v64, v71, v64
	v_max_f32_e32 v71, v73, v78
	v_min_f32_e32 v73, v73, v78
	v_max_f32_e32 v78, v77, v97
	v_min_f32_e32 v97, v77, v97
	s_waitcnt lgkmcnt(0)
	s_barrier
	v_max_f32_e32 v105, v75, v79
	v_min_f32_e32 v75, v75, v79
	v_max_f32_e32 v106, v74, v72
	v_min_f32_e32 v107, v74, v72
	v_max_f32_e32 v108, v76, v70
	v_min_f32_e32 v109, v76, v70
	v_max_f32_e32 v70, v68, v66
	v_min_f32_e32 v66, v68, v66
	v_max_f32_e32 v110, v67, v65
	v_min_f32_e32 v67, v67, v65
	v_max_f32_e32 v65, v69, v64
	v_min_f32_e32 v111, v69, v64
	v_max_f32_e32 v76, v71, v78
	v_min_f32_e32 v77, v71, v78
	v_max_f32_e32 v78, v73, v97
	v_min_f32_e32 v79, v73, v97
	v_cndmask_b32_e64 v97, 0, 1, s[20:21]
	v_max_f32_e32 v72, v105, v106
	v_min_f32_e32 v73, v105, v106
	v_max_f32_e32 v74, v75, v107
	v_min_f32_e32 v75, v75, v107
	v_max_f32_e32 v68, v108, v70
	v_min_f32_e32 v69, v108, v70
	v_max_f32_e32 v70, v109, v66
	v_min_f32_e32 v71, v109, v66
	v_max_f32_e32 v64, v110, v65
	v_min_f32_e32 v65, v110, v65
	v_max_f32_e32 v66, v67, v111
	v_min_f32_e32 v67, v67, v111
	v_cmp_ne_u32_e64 s[4:5], 1, v97
	v_add_u32_e32 v97, v130, v131
	s_cbranch_vccnz .LBB0_582
	ds_write_b128 v97, v[76:79]
	ds_write_b128 v97, v[72:75] offset:16
	ds_write_b128 v97, v[68:71] offset:32
	ds_write_b128 v97, v[64:67] offset:48
; #define PG8_LAS __attribute__((address_space(3)))
; #define RT_BAR() do { asm volatile("s_waitcnt lgkmcnt(0)" ::: "memory"); __builtin_amdgcn_s_barrier(); asm volatile("" ::: "memory"); } while (0)
;     __device__ __forceinline__ void fused(f32x4 (&acc)[2][2][4][2], const Unit& u, int wr, int wc, int fr, int fq, PG8_LAS unsigned char* lds, int wid, int lane) const {
;     ...
;                     for (int n = 0; n < 2; ++n) {
;                         const int rw = ai * HALF + wr * 64 + m * 16 + fr, g = 8 * wc + 4 * n + fq, col = 32 * wc + 16 * n + 4 * fq;
;                         const f32x4 v = acc[ai][bj][m][n]; f32x4 p;
; #pragma unroll
;                         for (int e = 0; e < 4; ++e) p[e] = __uint_as_float((__float_as_uint(v[e]) & ~127u) | (unsigned)(col + e));
;                         *(PG8_LAS f32x4*)(tile + rw * 128 + ((g ^ fr) << 2)) = p;
;                     }
;             RT_BAR();
;     ...
;             if (half == 0) {
;                 float nw[16];
; #pragma unroll
;                 for (int i = 0; i < 4; ++i) { const f32x4 v = *(const PG8_LAS f32x4*)(tile + row * 16 + 4 * i); nw[4 * i] = v[0]; nw[4 * i + 1] = v[1]; nw[4 * i + 2] = v[2]; nw[4 * i + 3] = v[3]; }
;                 merge_top16(run, nw);
;             }
; #pragma unroll
;             for (int q = 0; q < 16; ++q) { if (bj == 0) top0[q] = run[q]; else top1[q] = run[q]; }
.LBB0_582:
	s_waitcnt lgkmcnt(0)
	s_barrier
	s_cmp_lt_u32 s51, 4
	s_cselect_b64 s[20:21], -1, 0
	s_cmp_gt_u32 s51, 3
	s_cbranch_scc1 .LBB0_584
	ds_read_b128 v[106:109], v97 offset:48
	ds_read_b128 v[110:113], v97 offset:32
	ds_read_b128 v[114:117], v97
	ds_read_b128 v[130:133], v97 offset:16
	s_waitcnt lgkmcnt(0)
	v_max_f32_e32 v105, v109, v109
	v_max_f32_e32 v76, v76, v105
	v_max_f32_e32 v105, v108, v108
	v_max_f32_e32 v77, v77, v105
	v_max_f32_e32 v105, v107, v107
	v_max_f32_e32 v78, v78, v105
	v_max_f32_e32 v105, v106, v106
	v_max_f32_e32 v79, v79, v105
	v_max_f32_e32 v105, v113, v113
	v_max_f32_e32 v72, v72, v105
	v_max_f32_e32 v105, v112, v112
	v_max_f32_e32 v73, v73, v105
	v_max_f32_e32 v105, v111, v111
	v_max_f32_e32 v74, v74, v105
	v_max_f32_e32 v105, v110, v110
	v_max_f32_e32 v75, v75, v105
	v_max_f32_e32 v105, v133, v133
	v_max_f32_e32 v68, v68, v105
	v_max_f32_e32 v105, v132, v132
	v_max_f32_e32 v69, v69, v105
	v_max_f32_e32 v105, v131, v131
	v_max_f32_e32 v70, v70, v105
	v_max_f32_e32 v105, v130, v130
	v_max_f32_e32 v71, v71, v105
	v_max_f32_e32 v105, v117, v117
	v_max_f32_e32 v64, v64, v105
	v_max_f32_e32 v105, v116, v116
	v_max_f32_e32 v65, v65, v105
	v_max_f32_e32 v105, v115, v115
	v_max_f32_e32 v66, v66, v105
	v_max_f32_e32 v105, v114, v114
	v_max_f32_e32 v67, v67, v105
	v_max_f32_e32 v105, v76, v68
	v_min_f32_e32 v68, v76, v68
	v_max_f32_e32 v76, v77, v69
	v_min_f32_e32 v69, v77, v69
	v_max_f32_e32 v77, v78, v70
	v_min_f32_e32 v70, v78, v70
	v_max_f32_e32 v78, v79, v71
	v_min_f32_e32 v71, v79, v71
	v_max_f32_e32 v79, v72, v64
	v_min_f32_e32 v64, v72, v64
	v_max_f32_e32 v72, v73, v65
	v_min_f32_e32 v65, v73, v65
	v_max_f32_e32 v73, v74, v66
	v_min_f32_e32 v66, v74, v66
	v_max_f32_e32 v74, v75, v67
	v_min_f32_e32 v67, v75, v67
	v_max_f32_e32 v75, v105, v79
	v_min_f32_e32 v79, v105, v79
	v_max_f32_e32 v105, v76, v72
	v_min_f32_e32 v72, v76, v72
	v_max_f32_e32 v76, v77, v73
	v_min_f32_e32 v73, v77, v73
	v_max_f32_e32 v77, v78, v74
	v_min_f32_e32 v74, v78, v74
	v_max_f32_e32 v78, v68, v64
	v_min_f32_e32 v64, v68, v64
	v_max_f32_e32 v68, v69, v65
	v_min_f32_e32 v65, v69, v65
	v_max_f32_e32 v69, v70, v66
	v_min_f32_e32 v66, v70, v66
	v_max_f32_e32 v70, v71, v67
	v_min_f32_e32 v67, v71, v67
	v_max_f32_e32 v71, v75, v76
	v_min_f32_e32 v75, v75, v76
	v_max_f32_e32 v106, v105, v77
	v_min_f32_e32 v105, v105, v77
	v_max_f32_e32 v107, v79, v73
	v_min_f32_e32 v108, v79, v73
	v_max_f32_e32 v73, v72, v74
	v_min_f32_e32 v109, v72, v74
	v_max_f32_e32 v110, v78, v69
	v_min_f32_e32 v111, v78, v69
	v_max_f32_e32 v69, v68, v70
	v_min_f32_e32 v112, v68, v70
	v_max_f32_e32 v113, v64, v66
	v_min_f32_e32 v114, v64, v66
	v_max_f32_e32 v66, v65, v67
	v_min_f32_e32 v67, v65, v67
	v_max_f32_e32 v76, v71, v106
	v_min_f32_e32 v77, v71, v106
	v_max_f32_e32 v78, v75, v105
	v_min_f32_e32 v79, v75, v105
	v_max_f32_e32 v72, v107, v73
	v_min_f32_e32 v73, v107, v73
	v_max_f32_e32 v74, v108, v109
	v_min_f32_e32 v75, v108, v109
	v_max_f32_e32 v68, v110, v69
	v_min_f32_e32 v69, v110, v69
	v_max_f32_e32 v70, v111, v112
	v_min_f32_e32 v71, v111, v112
	v_max_f32_e32 v64, v113, v66
	v_min_f32_e32 v65, v113, v66
	v_max_f32_e32 v66, v114, v67
	v_min_f32_e32 v67, v114, v67
.LBB0_584:
	s_movk_i32 s19, 0xff80
	v_and_or_b32 v60, v60, s19, v129
	v_and_or_b32 v61, v61, s98, v218
	v_and_or_b32 v62, v62, s98, v219
	v_and_or_b32 v63, v63, s98, v220
	v_and_or_b32 v56, v56, s19, v124
	v_and_or_b32 v57, v57, s98, v221
	v_and_or_b32 v58, v58, s98, v222
	v_and_or_b32 v59, v59, s98, v223
	v_and_or_b32 v52, v52, s19, v129
	v_and_or_b32 v53, v53, s98, v218
	v_and_or_b32 v54, v54, s98, v219
	v_and_or_b32 v55, v55, s98, v220
	v_and_or_b32 v48, v48, s19, v124
	v_and_or_b32 v49, v49, s98, v221
	v_and_or_b32 v50, v50, s98, v222
	v_and_or_b32 v51, v51, s98, v223
	v_and_or_b32 v44, v44, s19, v129
	v_and_or_b32 v45, v45, s98, v218
	v_and_or_b32 v46, v46, s98, v219
	v_and_or_b32 v47, v47, s98, v220
	v_and_or_b32 v40, v40, s19, v124
	v_and_or_b32 v41, v41, s98, v221
	v_and_or_b32 v42, v42, s98, v222
	v_and_or_b32 v43, v43, s98, v223
	v_and_or_b32 v36, v36, s19, v129
	v_and_or_b32 v37, v37, s98, v218
	v_and_or_b32 v38, v38, s98, v219
	v_and_or_b32 v39, v39, s98, v220
	v_and_or_b32 v32, v32, s19, v124
	v_and_or_b32 v33, v33, s98, v221
	v_and_or_b32 v34, v34, s98, v222
	v_and_or_b32 v35, v35, s98, v223
	v_and_or_b32 v28, v28, s19, v129
	v_and_or_b32 v29, v29, s98, v218
	v_and_or_b32 v30, v30, s98, v219
	v_and_or_b32 v31, v31, s98, v220
	v_and_or_b32 v24, v24, s19, v124
	v_and_or_b32 v25, v25, s98, v221
	v_and_or_b32 v26, v26, s98, v222
	v_and_or_b32 v27, v27, s98, v223
	v_and_or_b32 v20, v20, s19, v129
	v_and_or_b32 v21, v21, s98, v218
	v_and_or_b32 v22, v22, s98, v219
	v_and_or_b32 v23, v23, s98, v220
	v_and_or_b32 v16, v16, s19, v124
	v_and_or_b32 v17, v17, s98, v221
	v_and_or_b32 v18, v18, s98, v222
	v_and_or_b32 v19, v19, s98, v223
	v_and_or_b32 v12, v12, s19, v129
	v_and_or_b32 v13, v13, s98, v218
	v_and_or_b32 v14, v14, s98, v219
	v_and_or_b32 v15, v15, s98, v220
	v_and_or_b32 v8, v8, s19, v124
	v_and_or_b32 v9, v9, s98, v221
	v_and_or_b32 v10, v10, s98, v222
	v_and_or_b32 v11, v11, s98, v223
	v_and_or_b32 v4, v4, s19, v129
	v_and_or_b32 v5, v5, s98, v218
	v_and_or_b32 v6, v6, s98, v219
	v_and_or_b32 v7, v7, s98, v220
	v_and_or_b32 v0, v0, s19, v124
	v_and_or_b32 v1, v1, s98, v221
	v_and_or_b32 v2, v2, s98, v222
	v_and_or_b32 v3, v3, s98, v223
	s_waitcnt lgkmcnt(0)
	s_barrier
; #define PG8_LAS __attribute__((address_space(3)))
; #define RT_BAR() do { asm volatile("s_waitcnt lgkmcnt(0)" ::: "memory"); __builtin_amdgcn_s_barrier(); asm volatile("" ::: "memory"); } while (0)
;     __device__ __forceinline__ void fused(f32x4 (&acc)[2][2][4][2], const Unit& u, int wr, int wc, int fr, int fq, PG8_LAS unsigned char* lds, int wid, int lane) const {
;     ...
;                     for (int n = 0; n < 2; ++n) {
;                         const int rw = ai * HALF + wr * 64 + m * 16 + fr, g = 8 * wc + 4 * n + fq, col = 32 * wc + 16 * n + 4 * fq;
;                         const f32x4 v = acc[ai][bj][m][n]; f32x4 p;
; #pragma unroll
;                         for (int e = 0; e < 4; ++e) p[e] = __uint_as_float((__float_as_uint(v[e]) & ~127u) | (unsigned)(col + e));
;                         *(PG8_LAS f32x4*)(tile + rw * 128 + ((g ^ fr) << 2)) = p;
;                     }
;             RT_BAR();
;             float run[16];
; #pragma unroll
;             for (int grp = 0; grp < 4; ++grp) {
;                 float nw[16];
; #pragma unroll
;                 for (int i = 0; i < 4; ++i) { const int g = half * 16 + grp * 4 + i; const f32x4 v = *(const PG8_LAS f32x4*)(tile + row * 128 + ((g ^ (row & 15)) << 2));
;                     nw[4 * i] = v[0]; nw[4 * i + 1] = v[1]; nw[4 * i + 2] = v[2]; nw[4 * i + 3] = v[3]; }
;                 sort16_desc(nw);
	ds_write_b128 v125, v[60:63]
	ds_write_b128 v120, v[56:59]
	ds_write_b128 v125, v[52:55] offset:8192
	ds_write_b128 v120, v[48:51] offset:8192
	ds_write_b128 v125, v[44:47] offset:16384
	ds_write_b128 v120, v[40:43] offset:16384
	ds_write_b128 v125, v[36:39] offset:24576
	ds_write_b128 v120, v[32:35] offset:24576
	ds_write_b128 v92, v[28:31]
	ds_write_b128 v88, v[24:27]
	ds_write_b128 v84, v[20:23]
	ds_write_b128 v82, v[16:19]
	ds_write_b128 v85, v[12:15]
	ds_write_b128 v86, v[8:11]
	ds_write_b128 v90, v[4:7]
	ds_write_b128 v91, v[0:3]
	s_waitcnt lgkmcnt(0)
	s_barrier
	ds_read_b128 v[0:3], v93
	ds_read_b128 v[4:7], v89
	s_and_b64 vcc, exec, s[4:5]
	s_waitcnt lgkmcnt(0)
	v_min_f32_e32 v10, v0, v1
	v_max_f32_e32 v8, v0, v1
	v_min_f32_e32 v13, v2, v3
	v_max_f32_e32 v9, v2, v3
	v_min_f32_e32 v17, v4, v5
	v_max_f32_e32 v15, v4, v5
	v_min_f32_e32 v20, v6, v7
	v_max_f32_e32 v16, v6, v7
	ds_read_b128 v[0:3], v81
	ds_read_b128 v[4:7], v80
	s_waitcnt lgkmcnt(0)
	v_min_f32_e32 v23, v0, v1
	v_min_f32_e32 v24, v2, v3
	v_min_f32_e32 v26, v4, v5
	v_min_f32_e32 v27, v6, v7
	v_max_f32_e32 v0, v0, v1
	v_max_f32_e32 v1, v2, v3
	v_max_f32_e32 v4, v4, v5
	v_max_f32_e32 v5, v6, v7
	v_min_f32_e32 v14, v10, v13
	v_min_f32_e32 v21, v17, v20
	v_min_f32_e32 v25, v23, v24
	v_max_f32_e32 v10, v10, v13
	v_min_f32_e32 v11, v8, v9
	v_max_f32_e32 v13, v17, v20
	v_min_f32_e32 v17, v15, v16
	v_max_f32_e32 v23, v23, v24
	v_min_f32_e32 v2, v0, v1
	v_max_f32_e32 v24, v26, v27
	v_min_f32_e32 v6, v4, v5
	v_min_f32_e32 v28, v26, v27
	v_max_f32_e32 v12, v10, v11
	v_max_f32_e32 v18, v13, v17
	v_max_f32_e32 v3, v23, v2
	v_max_f32_e32 v7, v24, v6
	v_min_f32_e32 v22, v14, v21
	v_min_f32_e32 v29, v25, v28
	v_max_f32_e32 v14, v14, v21
	v_min_f32_e32 v19, v12, v18
	v_min_f32_e32 v10, v10, v11
	v_min_f32_e32 v11, v13, v17
	v_max_f32_e32 v21, v25, v28
	v_min_f32_e32 v25, v3, v7
	v_min_f32_e32 v2, v23, v2
	v_min_f32_e32 v6, v24, v6
	v_max_f32_e32 v20, v14, v19
	v_max_f32_e32 v13, v10, v11
	v_max_f32_e32 v8, v8, v9
	v_max_f32_e32 v9, v15, v16
	v_max_f32_e32 v23, v2, v6
	v_max_f32_e32 v0, v0, v1
	v_max_f32_e32 v1, v4, v5
	v_min_f32_e32 v14, v14, v19
	v_min_f32_e32 v10, v10, v11
	v_min_f32_e32 v19, v21, v25
	v_min_f32_e32 v2, v2, v6
	v_min_f32_e32 v15, v8, v9
	v_min_f32_e32 v4, v0, v1
	v_max_f32_e32 v11, v14, v10
	v_max_f32_e32 v6, v19, v2
	v_min_f32_e32 v10, v14, v10
	v_min_f32_e32 v2, v19, v2
	v_min_f32_e32 v5, v23, v4
	v_min_f32_e32 v14, v10, v2
	v_max_f32_e32 v2, v10, v2
	v_max_f32_e32 v10, v12, v18
	v_max_f32_e32 v12, v13, v15
	v_max_f32_e32 v3, v3, v7
	v_max_f32_e32 v4, v23, v4
	v_min_f32_e32 v16, v13, v15
	v_max_f32_e32 v26, v21, v25
	v_min_f32_e32 v13, v10, v12
	v_min_f32_e32 v7, v3, v4
	v_max_f32_e32 v10, v10, v12
	v_max_f32_e32 v3, v3, v4
	v_max_f32_e32 v17, v20, v16
	v_max_f32_e32 v24, v26, v5
	v_min_f32_e32 v21, v11, v6
	v_min_f32_e32 v16, v20, v16
	v_min_f32_e32 v5, v26, v5
	v_max_f32_e32 v6, v11, v6
	v_min_f32_e32 v4, v10, v3
	v_max_f32_e32 v8, v8, v9
	v_max_f32_e32 v9, v0, v1
	v_max_f32_e32 v30, v22, v29
	v_min_f32_e32 v27, v17, v24
	v_min_f32_e32 v15, v13, v7
	v_min_f32_e32 v20, v16, v5
	v_min_f32_e32 v11, v6, v4
	v_max_f32_e32 v5, v16, v5
	v_min_f32_e32 v0, v8, v9
	v_max_f32_e32 v17, v17, v24
	v_max_f32_e32 v4, v6, v4
	v_min_f32_e32 v28, v30, v27
	v_min_f32_e32 v18, v2, v15
	v_max_f32_e32 v27, v30, v27
	v_max_f32_e32 v2, v2, v15
	v_min_f32_e32 v1, v5, v0
	v_min_f32_e32 v24, v17, v4
	v_max_f32_e32 v17, v17, v4
	v_max_f32_e32 v4, v13, v7
	v_max_f32_e32 v5, v5, v0
	v_min_f32_e32 v12, v27, v11
	v_max_f32_e32 v11, v27, v11
	v_min_f32_e32 v15, v2, v1
	v_max_f32_e32 v27, v2, v1
	v_min_f32_e32 v13, v4, v5
	v_max_f32_e32 v10, v10, v3
	ds_read_b128 v[0:3], v99
	v_max_f32_e32 v31, v4, v5
	ds_read_b128 v[4:7], v96
	v_min_f32_e32 v22, v22, v29
	v_min_f32_e32 v25, v28, v21
	s_waitcnt lgkmcnt(0)
	v_min_f32_e32 v34, v0, v1
	v_max_f32_e32 v29, v0, v1
	v_min_f32_e32 v37, v2, v3
	v_max_f32_e32 v33, v2, v3
	v_min_f32_e32 v41, v4, v5
	v_max_f32_e32 v39, v4, v5
	v_min_f32_e32 v44, v6, v7
	v_max_f32_e32 v40, v6, v7
	ds_read_b128 v[0:3], v87
	ds_read_b128 v[4:7], v83
	s_waitcnt lgkmcnt(0)
	v_min_f32_e32 v47, v0, v1
	v_min_f32_e32 v48, v2, v3
	v_min_f32_e32 v50, v4, v5
	v_min_f32_e32 v51, v6, v7
	v_max_f32_e32 v0, v0, v1
	v_max_f32_e32 v1, v2, v3
	v_max_f32_e32 v4, v4, v5
	v_max_f32_e32 v5, v6, v7
	v_min_f32_e32 v38, v34, v37
	v_min_f32_e32 v45, v41, v44
	v_min_f32_e32 v49, v47, v48
	v_max_f32_e32 v34, v34, v37
	v_min_f32_e32 v35, v29, v33
	v_max_f32_e32 v37, v41, v44
	v_min_f32_e32 v41, v39, v40
	v_max_f32_e32 v47, v47, v48
	v_min_f32_e32 v2, v0, v1
	v_max_f32_e32 v48, v50, v51
	v_min_f32_e32 v6, v4, v5
	v_min_f32_e32 v52, v50, v51
	v_max_f32_e32 v36, v34, v35
	v_max_f32_e32 v42, v37, v41
	v_max_f32_e32 v3, v47, v2
	v_max_f32_e32 v7, v48, v6
	v_min_f32_e32 v46, v38, v45
	v_min_f32_e32 v53, v49, v52
	v_max_f32_e32 v38, v38, v45
	v_min_f32_e32 v43, v36, v42
	v_min_f32_e32 v34, v34, v35
	v_min_f32_e32 v35, v37, v41
	v_max_f32_e32 v45, v49, v52
	v_min_f32_e32 v49, v3, v7
	v_min_f32_e32 v2, v47, v2
	v_min_f32_e32 v6, v48, v6
	v_max_f32_e32 v44, v38, v43
	v_max_f32_e32 v37, v34, v35
	v_max_f32_e32 v29, v29, v33
	v_max_f32_e32 v33, v39, v40
	v_max_f32_e32 v47, v2, v6
	v_max_f32_e32 v0, v0, v1
	v_max_f32_e32 v1, v4, v5
	v_min_f32_e32 v38, v38, v43
	v_min_f32_e32 v34, v34, v35
	v_min_f32_e32 v43, v45, v49
	v_min_f32_e32 v2, v2, v6
	v_min_f32_e32 v39, v29, v33
	v_min_f32_e32 v4, v0, v1
	v_max_f32_e32 v35, v38, v34
	v_max_f32_e32 v6, v43, v2
	v_min_f32_e32 v34, v38, v34
	v_min_f32_e32 v2, v43, v2
	v_min_f32_e32 v40, v37, v39
	v_max_f32_e32 v50, v45, v49
	v_min_f32_e32 v5, v47, v4
	v_min_f32_e32 v38, v34, v2
; #define PG8_LAS __attribute__((address_space(3)))
;     __device__ __forceinline__ void fused(f32x4 (&acc)[2][2][4][2], const Unit& u, int wr, int wc, int fr, int fq, PG8_LAS unsigned char* lds, int wid, int lane) const {
;     ...
;             for (int grp = 0; grp < 4; ++grp) {
;                 float nw[16];
; #pragma unroll
;                 for (int i = 0; i < 4; ++i) { const int g = half * 16 + grp * 4 + i; const f32x4 v = *(const PG8_LAS f32x4*)(tile + row * 128 + ((g ^ (row & 15)) << 2));
;                     nw[4 * i] = v[0]; nw[4 * i + 1] = v[1]; nw[4 * i + 2] = v[2]; nw[4 * i + 3] = v[3]; }
;                 sort16_desc(nw);
;                 if (grp == 0) {
; #pragma unroll
;                     for (int q = 0; q < 16; ++q) run[q] = nw[q];
;                 } else merge_top16(run, nw);
	v_max_f32_e32 v2, v34, v2
	v_max_f32_e32 v34, v36, v42
	v_max_f32_e32 v36, v37, v39
	v_max_f32_e32 v3, v3, v7
	v_max_f32_e32 v4, v47, v4
	v_max_f32_e32 v41, v44, v40
	v_max_f32_e32 v48, v50, v5
	v_min_f32_e32 v37, v34, v36
	v_min_f32_e32 v7, v3, v4
	v_min_f32_e32 v40, v44, v40
	v_min_f32_e32 v5, v50, v5
	v_max_f32_e32 v34, v34, v36
	v_max_f32_e32 v3, v3, v4
	v_max_f32_e32 v29, v29, v33
	v_max_f32_e32 v0, v0, v1
	v_max_f32_e32 v54, v46, v53
	v_min_f32_e32 v51, v41, v48
	v_min_f32_e32 v45, v35, v6
	v_min_f32_e32 v39, v37, v7
	v_min_f32_e32 v44, v40, v5
	v_max_f32_e32 v6, v35, v6
	v_min_f32_e32 v4, v34, v3
	v_max_f32_e32 v5, v40, v5
	v_min_f32_e32 v1, v29, v0
	v_min_f32_e32 v52, v54, v51
	v_min_f32_e32 v42, v2, v39
	v_max_f32_e32 v51, v54, v51
	v_min_f32_e32 v35, v6, v4
	v_max_f32_e32 v2, v2, v39
	v_min_f32_e32 v33, v5, v1
	v_max_f32_e32 v41, v41, v48
	v_max_f32_e32 v4, v6, v4
	v_max_f32_e32 v7, v37, v7
	v_max_f32_e32 v1, v5, v1
	v_max_f32_e32 v21, v28, v21
	v_min_f32_e32 v23, v18, v20
	v_max_f32_e32 v18, v18, v20
	v_min_f32_e32 v49, v52, v45
	v_max_f32_e32 v45, v52, v45
	v_min_f32_e32 v47, v42, v44
	v_min_f32_e32 v36, v51, v35
	v_max_f32_e32 v42, v42, v44
	v_max_f32_e32 v35, v51, v35
	v_min_f32_e32 v39, v2, v33
	v_min_f32_e32 v6, v41, v4
	v_max_f32_e32 v2, v2, v33
	v_max_f32_e32 v4, v41, v4
	v_min_f32_e32 v5, v7, v1
	v_max_f32_e32 v3, v34, v3
	v_max_f32_e32 v1, v7, v1
	v_min_f32_e32 v19, v25, v14
	v_min_f32_e32 v26, v21, v23
	v_min_f32_e32 v20, v12, v18
	v_min_f32_e32 v16, v11, v15
	v_min_f32_e32 v28, v24, v27
	v_min_f32_e32 v30, v17, v13
	v_min_f32_e32 v32, v10, v31
	v_min_f32_e32 v43, v49, v38
	v_min_f32_e32 v50, v45, v47
	v_min_f32_e32 v44, v36, v42
	v_min_f32_e32 v40, v35, v39
	v_min_f32_e32 v33, v6, v2
	v_min_f32_e32 v37, v4, v5
	v_min_f32_e32 v7, v3, v1
	v_min_f32_e32 v34, v46, v53
	v_max3_f32 v8, v8, v9, v34
	v_max3_f32 v9, v10, v31, v43
	v_max3_f32 v10, v32, v49, v38
	v_max3_f32 v13, v17, v13, v50
	v_max3_f32 v17, v30, v45, v47
	v_max3_f32 v24, v24, v27, v44
	v_max3_f32 v27, v28, v36, v42
	v_max3_f32 v11, v11, v15, v40
	v_max3_f32 v15, v16, v35, v39
	v_max3_f32 v12, v12, v18, v33
	v_max3_f32 v2, v20, v6, v2
	v_max3_f32 v6, v21, v23, v37
	v_max3_f32 v4, v26, v4, v5
	v_max3_f32 v5, v25, v14, v7
	v_max3_f32 v1, v19, v3, v1
	v_max3_f32 v0, v22, v29, v0
	v_max_f32_e32 v3, v8, v15
	v_min_f32_e32 v7, v8, v15
	v_max_f32_e32 v8, v9, v12
	v_min_f32_e32 v9, v9, v12
	v_max_f32_e32 v12, v10, v2
	v_min_f32_e32 v2, v10, v2
	v_max_f32_e32 v10, v13, v6
	v_min_f32_e32 v6, v13, v6
	v_max_f32_e32 v13, v17, v4
	v_min_f32_e32 v4, v17, v4
	v_max_f32_e32 v14, v24, v5
	v_min_f32_e32 v5, v24, v5
	v_max_f32_e32 v15, v27, v1
	v_min_f32_e32 v1, v27, v1
	v_max_f32_e32 v16, v11, v0
	v_min_f32_e32 v0, v11, v0
	v_max_f32_e32 v11, v3, v13
	v_min_f32_e32 v3, v3, v13
	v_max_f32_e32 v13, v8, v14
	v_min_f32_e32 v8, v8, v14
	v_max_f32_e32 v14, v12, v15
	v_min_f32_e32 v12, v12, v15
	v_max_f32_e32 v15, v10, v16
	v_min_f32_e32 v10, v10, v16
	v_max_f32_e32 v16, v7, v4
	v_min_f32_e32 v4, v7, v4
	v_max_f32_e32 v7, v9, v5
	v_min_f32_e32 v5, v9, v5
	v_max_f32_e32 v9, v2, v1
	v_min_f32_e32 v1, v2, v1
	v_max_f32_e32 v2, v6, v0
	v_min_f32_e32 v0, v6, v0
	v_max_f32_e32 v17, v11, v14
	v_min_f32_e32 v11, v11, v14
	v_max_f32_e32 v14, v13, v15
	v_min_f32_e32 v13, v13, v15
	v_max_f32_e32 v15, v3, v12
	v_min_f32_e32 v12, v3, v12
	v_max_f32_e32 v18, v8, v10
	v_min_f32_e32 v8, v8, v10
	v_max_f32_e32 v10, v16, v9
	v_min_f32_e32 v9, v16, v9
	v_max_f32_e32 v16, v7, v2
	v_min_f32_e32 v19, v7, v2
	v_max_f32_e32 v20, v4, v1
	v_min_f32_e32 v21, v4, v1
	v_max_f32_e32 v22, v5, v0
	v_min_f32_e32 v23, v5, v0
	ds_read_b128 v[0:3], v102
	ds_read_b128 v[4:7], v101
	v_min_f32_e32 v24, v17, v14
	v_min_f32_e32 v25, v11, v13
	v_min_f32_e32 v26, v15, v18
	s_waitcnt lgkmcnt(0)
	v_min_f32_e32 v34, v0, v1
	v_max_f32_e32 v32, v0, v1
	v_min_f32_e32 v37, v2, v3
	v_max_f32_e32 v33, v2, v3
	v_min_f32_e32 v41, v4, v5
	v_max_f32_e32 v39, v4, v5
	v_min_f32_e32 v44, v6, v7
	v_max_f32_e32 v40, v6, v7
	ds_read_b128 v[0:3], v95
	ds_read_b128 v[4:7], v94
	s_waitcnt lgkmcnt(0)
	v_min_f32_e32 v47, v0, v1
	v_min_f32_e32 v48, v2, v3
	v_min_f32_e32 v50, v4, v5
	v_min_f32_e32 v51, v6, v7
	v_max_f32_e32 v0, v0, v1
	v_max_f32_e32 v1, v2, v3
	v_max_f32_e32 v4, v4, v5
	v_max_f32_e32 v5, v6, v7
	v_min_f32_e32 v38, v34, v37
	v_min_f32_e32 v45, v41, v44
	v_min_f32_e32 v49, v47, v48
	v_max_f32_e32 v34, v34, v37
	v_min_f32_e32 v35, v32, v33
	v_max_f32_e32 v37, v41, v44
	v_min_f32_e32 v41, v39, v40
	v_max_f32_e32 v47, v47, v48
	v_min_f32_e32 v2, v0, v1
	v_max_f32_e32 v48, v50, v51
	v_min_f32_e32 v6, v4, v5
	v_min_f32_e32 v52, v50, v51
	v_max_f32_e32 v36, v34, v35
	v_max_f32_e32 v42, v37, v41
	v_max_f32_e32 v3, v47, v2
	v_max_f32_e32 v7, v48, v6
	v_min_f32_e32 v46, v38, v45
	v_min_f32_e32 v53, v49, v52
	v_max_f32_e32 v38, v38, v45
	v_min_f32_e32 v43, v36, v42
	v_min_f32_e32 v34, v34, v35
	v_min_f32_e32 v35, v37, v41
	v_max_f32_e32 v45, v49, v52
	v_min_f32_e32 v49, v3, v7
	v_min_f32_e32 v2, v47, v2
	v_min_f32_e32 v6, v48, v6
	v_max_f32_e32 v44, v38, v43
	v_max_f32_e32 v37, v34, v35
	v_max_f32_e32 v32, v32, v33
	v_max_f32_e32 v33, v39, v40
	v_max_f32_e32 v47, v2, v6
	v_max_f32_e32 v0, v0, v1
	v_max_f32_e32 v1, v4, v5
	v_min_f32_e32 v38, v38, v43
	v_min_f32_e32 v34, v34, v35
	v_min_f32_e32 v43, v45, v49
	v_min_f32_e32 v2, v2, v6
	v_min_f32_e32 v39, v32, v33
	v_min_f32_e32 v4, v0, v1
	v_max_f32_e32 v35, v38, v34
	v_max_f32_e32 v6, v43, v2
	v_min_f32_e32 v34, v38, v34
	v_min_f32_e32 v2, v43, v2
	v_min_f32_e32 v40, v37, v39
	v_max_f32_e32 v50, v45, v49
	v_min_f32_e32 v5, v47, v4
	v_min_f32_e32 v38, v34, v2
	v_max_f32_e32 v2, v34, v2
; #define PG8_LAS __attribute__((address_space(3)))
;     __device__ __forceinline__ void fused(f32x4 (&acc)[2][2][4][2], const Unit& u, int wr, int wc, int fr, int fq, PG8_LAS unsigned char* lds, int wid, int lane) const {
;     ...
;             for (int grp = 0; grp < 4; ++grp) {
;                 float nw[16];
; #pragma unroll
;                 for (int i = 0; i < 4; ++i) { const int g = half * 16 + grp * 4 + i; const f32x4 v = *(const PG8_LAS f32x4*)(tile + row * 128 + ((g ^ (row & 15)) << 2));
;                     nw[4 * i] = v[0]; nw[4 * i + 1] = v[1]; nw[4 * i + 2] = v[2]; nw[4 * i + 3] = v[3]; }
;                 sort16_desc(nw);
;                 if (grp == 0) {
; #pragma unroll
;                     for (int q = 0; q < 16; ++q) run[q] = nw[q];
;                 } else merge_top16(run, nw);
	v_max_f32_e32 v34, v36, v42
	v_max_f32_e32 v36, v37, v39
	v_max_f32_e32 v3, v3, v7
	v_max_f32_e32 v4, v47, v4
	v_max_f32_e32 v41, v44, v40
	v_max_f32_e32 v48, v50, v5
	v_min_f32_e32 v37, v34, v36
	v_min_f32_e32 v7, v3, v4
	v_max_f32_e32 v54, v46, v53
	v_min_f32_e32 v51, v41, v48
	v_min_f32_e32 v39, v37, v7
	v_min_f32_e32 v40, v44, v40
	v_min_f32_e32 v5, v50, v5
	v_min_f32_e32 v52, v54, v51
	v_min_f32_e32 v45, v35, v6
	v_min_f32_e32 v42, v2, v39
	v_min_f32_e32 v44, v40, v5
	v_max_f32_e32 v34, v34, v36
	v_max_f32_e32 v3, v3, v4
	v_max_f32_e32 v32, v32, v33
	v_max_f32_e32 v0, v0, v1
	v_min_f32_e32 v49, v52, v45
	v_max_f32_e32 v45, v52, v45
	v_min_f32_e32 v47, v42, v44
	v_max_f32_e32 v6, v35, v6
	v_min_f32_e32 v4, v34, v3
	v_max_f32_e32 v5, v40, v5
	v_min_f32_e32 v1, v32, v0
	v_min_f32_e32 v43, v49, v38
	v_max_f32_e32 v38, v49, v38
	v_min_f32_e32 v49, v45, v47
	v_max_f32_e32 v45, v45, v47
	v_max_f32_e32 v47, v54, v51
	v_min_f32_e32 v35, v6, v4
	v_max_f32_e32 v2, v2, v39
	v_min_f32_e32 v33, v5, v1
	v_min_f32_e32 v36, v47, v35
	v_max_f32_e32 v35, v47, v35
	v_min_f32_e32 v39, v2, v33
	v_min_f32_e32 v40, v35, v39
	v_max_f32_e32 v35, v35, v39
	v_max_f32_e32 v39, v41, v48
	v_max_f32_e32 v4, v6, v4
	v_min_f32_e32 v6, v39, v4
	v_max_f32_e32 v2, v2, v33
	v_min_f32_e32 v33, v6, v2
	v_max_f32_e32 v2, v6, v2
	v_max_f32_e32 v6, v37, v7
	v_max_f32_e32 v1, v5, v1
	v_max_f32_e32 v42, v42, v44
	v_max_f32_e32 v4, v39, v4
	v_min_f32_e32 v5, v6, v1
	v_max_f32_e32 v3, v34, v3
	v_max_f32_e32 v1, v6, v1
	v_min_f32_e32 v27, v12, v8
	v_min_f32_e32 v28, v10, v16
	v_min_f32_e32 v29, v9, v19
	v_min_f32_e32 v30, v20, v22
	v_min_f32_e32 v31, v21, v23
	v_min_f32_e32 v44, v36, v42
	v_max_f32_e32 v36, v36, v42
	v_min_f32_e32 v7, v4, v5
	v_max_f32_e32 v4, v4, v5
	v_min_f32_e32 v5, v3, v1
	v_max_f32_e32 v1, v3, v1
	v_min_f32_e32 v3, v46, v53
	v_max3_f32 v3, v17, v14, v3
	v_max_f32_e32 v6, v24, v43
	v_max3_f32 v11, v11, v13, v38
	v_max_f32_e32 v13, v25, v49
	v_max3_f32 v14, v15, v18, v45
	v_max_f32_e32 v15, v26, v44
	v_max3_f32 v8, v12, v8, v36
	v_max_f32_e32 v12, v27, v40
	v_max3_f32 v10, v10, v16, v35
	v_max_f32_e32 v16, v28, v33
	v_max3_f32 v2, v9, v19, v2
	v_max_f32_e32 v7, v29, v7
	v_max3_f32 v4, v20, v22, v4
	v_max_f32_e32 v5, v30, v5
	v_max3_f32 v1, v21, v23, v1
	v_max3_f32 v0, v31, v32, v0
	v_max_f32_e32 v9, v3, v10
	v_min_f32_e32 v3, v3, v10
	v_max_f32_e32 v10, v6, v16
	v_min_f32_e32 v6, v6, v16
	v_max_f32_e32 v16, v11, v2
	v_min_f32_e32 v2, v11, v2
	v_max_f32_e32 v11, v13, v7
	v_min_f32_e32 v7, v13, v7
	v_max_f32_e32 v13, v14, v4
	v_min_f32_e32 v4, v14, v4
	v_max_f32_e32 v14, v15, v5
	v_min_f32_e32 v5, v15, v5
	v_max_f32_e32 v15, v8, v1
	v_min_f32_e32 v1, v8, v1
	v_max_f32_e32 v8, v12, v0
	v_min_f32_e32 v0, v12, v0
	v_max_f32_e32 v12, v9, v13
	v_min_f32_e32 v9, v9, v13
	v_max_f32_e32 v13, v10, v14
	v_min_f32_e32 v10, v10, v14
	v_max_f32_e32 v14, v16, v15
	v_min_f32_e32 v15, v16, v15
	v_max_f32_e32 v16, v11, v8
	v_min_f32_e32 v8, v11, v8
	v_max_f32_e32 v11, v3, v4
	v_min_f32_e32 v3, v3, v4
	v_max_f32_e32 v4, v6, v5
	v_min_f32_e32 v5, v6, v5
	v_max_f32_e32 v6, v2, v1
	v_min_f32_e32 v1, v2, v1
	v_max_f32_e32 v2, v7, v0
	v_min_f32_e32 v0, v7, v0
	v_max_f32_e32 v17, v12, v14
	v_min_f32_e32 v12, v12, v14
	v_max_f32_e32 v14, v13, v16
	v_min_f32_e32 v13, v13, v16
	v_max_f32_e32 v16, v9, v15
	v_min_f32_e32 v9, v9, v15
	v_max_f32_e32 v15, v10, v8
	v_min_f32_e32 v8, v10, v8
	v_max_f32_e32 v10, v11, v6
	v_min_f32_e32 v11, v11, v6
	v_max_f32_e32 v18, v4, v2
	v_min_f32_e32 v19, v4, v2
	v_max_f32_e32 v20, v3, v1
	v_min_f32_e32 v21, v3, v1
	v_max_f32_e32 v22, v5, v0
	v_min_f32_e32 v23, v5, v0
	ds_read_b128 v[0:3], v104
	ds_read_b128 v[4:7], v103
	v_min_f32_e32 v24, v17, v14
	v_min_f32_e32 v25, v12, v13
	v_min_f32_e32 v26, v16, v15
	s_waitcnt lgkmcnt(0)
	v_min_f32_e32 v34, v0, v1
	v_max_f32_e32 v32, v0, v1
	v_min_f32_e32 v37, v2, v3
	v_max_f32_e32 v33, v2, v3
	v_min_f32_e32 v41, v4, v5
	v_max_f32_e32 v39, v4, v5
	v_min_f32_e32 v44, v6, v7
	v_max_f32_e32 v40, v6, v7
	ds_read_b128 v[0:3], v100
	ds_read_b128 v[4:7], v98
	s_waitcnt lgkmcnt(0)
	v_min_f32_e32 v47, v0, v1
	v_min_f32_e32 v48, v2, v3
	v_min_f32_e32 v50, v4, v5
	v_min_f32_e32 v51, v6, v7
	v_max_f32_e32 v0, v0, v1
	v_max_f32_e32 v1, v2, v3
	v_max_f32_e32 v4, v4, v5
	v_max_f32_e32 v5, v6, v7
	v_min_f32_e32 v38, v34, v37
	v_min_f32_e32 v45, v41, v44
	v_min_f32_e32 v49, v47, v48
	v_max_f32_e32 v34, v34, v37
	v_min_f32_e32 v35, v32, v33
	v_max_f32_e32 v37, v41, v44
	v_min_f32_e32 v41, v39, v40
	v_max_f32_e32 v47, v47, v48
	v_min_f32_e32 v2, v0, v1
	v_max_f32_e32 v48, v50, v51
	v_min_f32_e32 v6, v4, v5
	v_min_f32_e32 v52, v50, v51
	v_max_f32_e32 v36, v34, v35
	v_max_f32_e32 v42, v37, v41
	v_max_f32_e32 v3, v47, v2
	v_max_f32_e32 v7, v48, v6
	v_min_f32_e32 v46, v38, v45
	v_min_f32_e32 v53, v49, v52
	v_max_f32_e32 v38, v38, v45
	v_min_f32_e32 v43, v36, v42
	v_min_f32_e32 v34, v34, v35
	v_min_f32_e32 v35, v37, v41
	v_max_f32_e32 v45, v49, v52
	v_min_f32_e32 v49, v3, v7
	v_min_f32_e32 v2, v47, v2
	v_min_f32_e32 v6, v48, v6
	v_max_f32_e32 v44, v38, v43
	v_max_f32_e32 v37, v34, v35
	v_max_f32_e32 v32, v32, v33
	v_max_f32_e32 v33, v39, v40
	v_max_f32_e32 v47, v2, v6
	v_max_f32_e32 v0, v0, v1
	v_max_f32_e32 v1, v4, v5
	v_min_f32_e32 v38, v38, v43
	v_min_f32_e32 v34, v34, v35
	v_min_f32_e32 v43, v45, v49
	v_min_f32_e32 v2, v2, v6
	v_min_f32_e32 v39, v32, v33
	v_min_f32_e32 v4, v0, v1
	v_max_f32_e32 v35, v38, v34
	v_max_f32_e32 v6, v43, v2
	v_min_f32_e32 v34, v38, v34
	v_min_f32_e32 v2, v43, v2
	v_min_f32_e32 v40, v37, v39
	v_max_f32_e32 v50, v45, v49
	v_min_f32_e32 v5, v47, v4
	v_min_f32_e32 v38, v34, v2
	v_max_f32_e32 v2, v34, v2
; #define PG8_LAS __attribute__((address_space(3)))
; #define RT_BAR() do { asm volatile("s_waitcnt lgkmcnt(0)" ::: "memory"); __builtin_amdgcn_s_barrier(); asm volatile("" ::: "memory"); } while (0)
;     __device__ __forceinline__ void fused(f32x4 (&acc)[2][2][4][2], const Unit& u, int wr, int wc, int fr, int fq, PG8_LAS unsigned char* lds, int wid, int lane) const {
;     ...
;             for (int grp = 0; grp < 4; ++grp) {
;                 float nw[16];
; #pragma unroll
;                 for (int i = 0; i < 4; ++i) { const int g = half * 16 + grp * 4 + i; const f32x4 v = *(const PG8_LAS f32x4*)(tile + row * 128 + ((g ^ (row & 15)) << 2));
;                     nw[4 * i] = v[0]; nw[4 * i + 1] = v[1]; nw[4 * i + 2] = v[2]; nw[4 * i + 3] = v[3]; }
;                 sort16_desc(nw);
;                 if (grp == 0) {
; #pragma unroll
;                     for (int q = 0; q < 16; ++q) run[q] = nw[q];
;                 } else merge_top16(run, nw);
;             }
;             RT_BAR();
;             if (half == 1) {
; #pragma unroll
;                 for (int i = 0; i < 4; ++i) *(PG8_LAS f32x4*)(tile + row * 16 + 4 * i) = (f32x4){run[4 * i], run[4 * i + 1], run[4 * i + 2], run[4 * i + 3]};
;             }
	v_max_f32_e32 v34, v36, v42
	v_max_f32_e32 v36, v37, v39
	v_max_f32_e32 v3, v3, v7
	v_max_f32_e32 v4, v47, v4
	v_max_f32_e32 v41, v44, v40
	v_max_f32_e32 v48, v50, v5
	v_min_f32_e32 v37, v34, v36
	v_min_f32_e32 v7, v3, v4
	v_max_f32_e32 v54, v46, v53
	v_min_f32_e32 v51, v41, v48
	v_min_f32_e32 v39, v37, v7
	v_min_f32_e32 v40, v44, v40
	v_min_f32_e32 v5, v50, v5
	v_min_f32_e32 v52, v54, v51
	v_min_f32_e32 v45, v35, v6
	v_min_f32_e32 v42, v2, v39
	v_min_f32_e32 v44, v40, v5
	v_max_f32_e32 v34, v34, v36
	v_max_f32_e32 v3, v3, v4
	v_max_f32_e32 v32, v32, v33
	v_max_f32_e32 v0, v0, v1
	v_min_f32_e32 v49, v52, v45
	v_max_f32_e32 v45, v52, v45
	v_min_f32_e32 v47, v42, v44
	v_max_f32_e32 v6, v35, v6
	v_min_f32_e32 v4, v34, v3
	v_max_f32_e32 v5, v40, v5
	v_min_f32_e32 v1, v32, v0
	v_min_f32_e32 v43, v49, v38
	v_max_f32_e32 v38, v49, v38
	v_min_f32_e32 v49, v45, v47
	v_max_f32_e32 v45, v45, v47
	v_max_f32_e32 v47, v54, v51
	v_min_f32_e32 v35, v6, v4
	v_max_f32_e32 v2, v2, v39
	v_min_f32_e32 v33, v5, v1
	v_min_f32_e32 v36, v47, v35
	v_max_f32_e32 v35, v47, v35
	v_min_f32_e32 v39, v2, v33
	v_min_f32_e32 v40, v35, v39
	v_max_f32_e32 v35, v35, v39
	v_max_f32_e32 v39, v41, v48
	v_max_f32_e32 v4, v6, v4
	v_min_f32_e32 v6, v39, v4
	v_max_f32_e32 v2, v2, v33
	v_min_f32_e32 v33, v6, v2
	v_max_f32_e32 v2, v6, v2
	v_max_f32_e32 v6, v37, v7
	v_max_f32_e32 v1, v5, v1
	v_max_f32_e32 v42, v42, v44
	v_max_f32_e32 v4, v39, v4
	v_min_f32_e32 v5, v6, v1
	v_max_f32_e32 v3, v34, v3
	v_max_f32_e32 v1, v6, v1
	v_min_f32_e32 v27, v9, v8
	v_min_f32_e32 v28, v10, v18
	v_min_f32_e32 v29, v11, v19
	v_min_f32_e32 v30, v20, v22
	v_min_f32_e32 v31, v21, v23
	v_min_f32_e32 v44, v36, v42
	v_max_f32_e32 v36, v36, v42
	v_min_f32_e32 v7, v4, v5
	v_max_f32_e32 v4, v4, v5
	v_min_f32_e32 v5, v3, v1
	v_max_f32_e32 v1, v3, v1
	v_min_f32_e32 v3, v46, v53
	v_max3_f32 v3, v17, v14, v3
	v_max_f32_e32 v6, v24, v43
	v_max3_f32 v12, v12, v13, v38
	v_max_f32_e32 v13, v25, v49
	v_max3_f32 v14, v16, v15, v45
	v_max_f32_e32 v15, v26, v44
	v_max3_f32 v8, v9, v8, v36
	v_max_f32_e32 v9, v27, v40
	v_max3_f32 v10, v10, v18, v35
	v_max_f32_e32 v16, v28, v33
	v_max3_f32 v2, v11, v19, v2
	v_max_f32_e32 v7, v29, v7
	v_max3_f32 v4, v20, v22, v4
	v_max_f32_e32 v5, v30, v5
	v_max3_f32 v1, v21, v23, v1
	v_max3_f32 v0, v31, v32, v0
	v_max_f32_e32 v11, v3, v10
	v_min_f32_e32 v3, v3, v10
	v_max_f32_e32 v10, v6, v16
	v_min_f32_e32 v6, v6, v16
	v_max_f32_e32 v16, v12, v2
	v_min_f32_e32 v2, v12, v2
	v_max_f32_e32 v12, v13, v7
	v_min_f32_e32 v7, v13, v7
	v_max_f32_e32 v13, v14, v4
	v_min_f32_e32 v4, v14, v4
	v_max_f32_e32 v14, v15, v5
	v_min_f32_e32 v5, v15, v5
	v_max_f32_e32 v15, v8, v1
	v_min_f32_e32 v1, v8, v1
	v_max_f32_e32 v8, v9, v0
	v_min_f32_e32 v0, v9, v0
	v_max_f32_e32 v9, v11, v13
	v_min_f32_e32 v11, v11, v13
	v_max_f32_e32 v13, v10, v14
	v_min_f32_e32 v10, v10, v14
	v_max_f32_e32 v14, v16, v15
	v_min_f32_e32 v15, v16, v15
	v_max_f32_e32 v16, v12, v8
	v_min_f32_e32 v8, v12, v8
	v_max_f32_e32 v12, v3, v4
	v_min_f32_e32 v3, v3, v4
	v_max_f32_e32 v4, v6, v5
	v_min_f32_e32 v5, v6, v5
	v_max_f32_e32 v6, v2, v1
	v_min_f32_e32 v1, v2, v1
	v_max_f32_e32 v2, v7, v0
	v_min_f32_e32 v0, v7, v0
	s_waitcnt lgkmcnt(0)
	s_barrier
	v_max_f32_e32 v7, v9, v14
	v_min_f32_e32 v9, v9, v14
	v_max_f32_e32 v14, v13, v16
	v_min_f32_e32 v16, v13, v16
	v_max_f32_e32 v17, v11, v15
	v_min_f32_e32 v11, v11, v15
	v_max_f32_e32 v18, v10, v8
	v_min_f32_e32 v19, v10, v8
	v_max_f32_e32 v20, v12, v6
	v_min_f32_e32 v21, v12, v6
	v_max_f32_e32 v6, v4, v2
	v_min_f32_e32 v2, v4, v2
	v_max_f32_e32 v22, v3, v1
	v_min_f32_e32 v3, v3, v1
	v_max_f32_e32 v1, v5, v0
	v_min_f32_e32 v23, v5, v0
	v_max_f32_e32 v12, v7, v14
	v_min_f32_e32 v13, v7, v14
	v_max_f32_e32 v14, v9, v16
	v_min_f32_e32 v15, v9, v16
	v_max_f32_e32 v8, v17, v18
	v_min_f32_e32 v9, v17, v18
	v_max_f32_e32 v10, v11, v19
	v_min_f32_e32 v11, v11, v19
	v_max_f32_e32 v4, v20, v6
	v_min_f32_e32 v5, v20, v6
	v_max_f32_e32 v6, v21, v2
	v_min_f32_e32 v7, v21, v2
	v_max_f32_e32 v0, v22, v1
	v_min_f32_e32 v1, v22, v1
	v_max_f32_e32 v2, v3, v23
	v_min_f32_e32 v3, v3, v23
	s_cbranch_vccnz .LBB0_586
	ds_write_b128 v97, v[12:15]
	ds_write_b128 v97, v[8:11] offset:16
	ds_write_b128 v97, v[4:7] offset:32
	ds_write_b128 v97, v[0:3] offset:48
; #define PG8_LAS __attribute__((address_space(3)))
;     __device__ __forceinline__ void fused(f32x4 (&acc)[2][2][4][2], const Unit& u, int wr, int wc, int fr, int fq, PG8_LAS unsigned char* lds, int wid, int lane) const {
;     ...
;             if (half == 0) {
;                 float nw[16];
; #pragma unroll
;                 for (int i = 0; i < 4; ++i) { const f32x4 v = *(const PG8_LAS f32x4*)(tile + row * 16 + 4 * i); nw[4 * i] = v[0]; nw[4 * i + 1] = v[1]; nw[4 * i + 2] = v[2]; nw[4 * i + 3] = v[3]; }
;                 merge_top16(run, nw);
;             }
; #pragma unroll
;             for (int q = 0; q < 16; ++q) { if (bj == 0) top0[q] = run[q]; else top1[q] = run[q]; }
;             RT_BAR();
;         }
;         if (half == 0) {
;             PG8_LAS int* idxl = (PG8_LAS int*)(lds + 65536) + row * 32;
;             float v0[16], v1[16];
; #pragma unroll
;             for (int q = 0; q < 16; ++q) { const unsigned b0 = __float_as_uint(top0[q]), b1 = __float_as_uint(top1[q]);
;                 v0[q] = __uint_as_float(b0 & ~127u); v1[q] = __uint_as_float(b1 & ~127u); idxl[q] = (int)(b0 & 127u); idxl[16 + q] = (int)(b1 & 127u); }
;             float best[16];
;             { float cv[16]; cv[0] = __uint_as_float((__float_as_uint(v0[0] + v1[0]) & ~255u) | 0u); cv[1] = __uint_as_float((__float_as_uint(v0[0] + v1[1]) & ~255u) | 1u); cv[2] = __uint_as_float((__float_as_uint(v0[0] + v1[2]) & ~255u) | 2u); cv[3] = __uint_as_float((__float_as_uint(v0[0] + v1[3]) & ~255u) | 3u); cv[4] = __uint_as_float((__float_as_uint(v0[0] + v1[4]) & ~255u) | 4u); cv[5] = __uint_as_float((__float_as_uint(v0[0] + v1[5]) & ~255u) | 5u); cv[6] = __uint_as_float((__float_as_uint(v0[0] + v1[6]) & ~255u) | 6u); cv[7] = __uint_as_float((__float_as_uint(v0[0] + v1[7]) & ~255u) | 7u); cv[8] = __uint_as_float((__float_as_uint(v0[0] + v1[8]) & ~255u) | 8u); cv[9] = __uint_as_float((__float_as_uint(v0[0] + v1[9]) & ~255u) | 9u); cv[10] = __uint_as_float((__float_as_uint(v0[0] + v1[10]) & ~255u) | 10u); cv[11] = __uint_as_float((__float_as_uint(v0[0] + v1[11]) & ~255u) | 11u); cv[12] = __uint_as_float((__float_as_uint(v0[0] + v1[12]) & ~255u) | 12u); cv[13] = __uint_as_float((__float_as_uint(v0[0] + v1[13]) & ~255u) | 13u); cv[14] = __uint_as_float((__float_as_uint(v0[0] + v1[14]) & ~255u) | 14u); cv[15] = __uint_as_float((__float_as_uint(v0[0] + v1[15]) & ~255u) | 15u); sort16_desc(cv);
.LBB0_586:
	s_waitcnt lgkmcnt(0)
	s_barrier
	v_cndmask_b32_e64 v16, 0, 1, s[20:21]
	v_cmp_ne_u32_e64 s[4:5], 1, v16
	s_andn2_b64 vcc, exec, s[20:21]
	s_cbranch_vccnz .LBB0_588
	ds_read_b128 v[16:19], v97 offset:48
	ds_read_b128 v[20:23], v97 offset:32
	ds_read_b128 v[24:27], v97
	ds_read_b128 v[28:31], v97 offset:16
	s_waitcnt lgkmcnt(0)
	v_max_f32_e32 v15, v15, v16
	v_max_f32_e32 v16, v23, v23
	v_max_f32_e32 v8, v8, v16
	v_max_f32_e32 v16, v22, v22
	v_max_f32_e32 v9, v9, v16
	v_max_f32_e32 v16, v21, v21
	v_max_f32_e32 v10, v10, v16
	v_max_f32_e32 v16, v20, v20
	v_max_f32_e32 v11, v11, v16
	v_max_f32_e32 v16, v31, v31
	v_max_f32_e32 v4, v4, v16
	v_max_f32_e32 v16, v30, v30
	v_max_f32_e32 v5, v5, v16
	v_max_f32_e32 v16, v29, v29
	v_max_f32_e32 v6, v6, v16
	v_max_f32_e32 v16, v28, v28
	v_max_f32_e32 v7, v7, v16
	v_max_f32_e32 v16, v27, v27
	v_max_f32_e32 v0, v0, v16
	v_max_f32_e32 v16, v26, v26
	v_max_f32_e32 v1, v1, v16
	v_max_f32_e32 v16, v25, v25
	v_max_f32_e32 v2, v2, v16
	v_max_f32_e32 v16, v24, v24
	v_max_f32_e32 v12, v12, v19
	v_max_f32_e32 v13, v13, v18
	v_max_f32_e32 v14, v14, v17
	v_max_f32_e32 v3, v3, v16
	v_max_f32_e32 v16, v12, v4
	v_min_f32_e32 v4, v12, v4
	v_max_f32_e32 v12, v13, v5
	v_min_f32_e32 v5, v13, v5
	v_max_f32_e32 v13, v14, v6
	v_min_f32_e32 v6, v14, v6
	v_max_f32_e32 v14, v15, v7
	v_min_f32_e32 v7, v15, v7
	v_max_f32_e32 v15, v8, v0
	v_min_f32_e32 v0, v8, v0
	v_max_f32_e32 v8, v9, v1
	v_min_f32_e32 v1, v9, v1
	v_max_f32_e32 v9, v10, v2
	v_min_f32_e32 v2, v10, v2
	v_max_f32_e32 v10, v11, v3
	v_min_f32_e32 v3, v11, v3
	v_max_f32_e32 v11, v16, v15
	v_min_f32_e32 v15, v16, v15
	v_max_f32_e32 v16, v12, v8
	v_min_f32_e32 v8, v12, v8
	v_max_f32_e32 v12, v13, v9
	v_min_f32_e32 v9, v13, v9
	v_max_f32_e32 v13, v14, v10
	v_min_f32_e32 v10, v14, v10
	v_max_f32_e32 v14, v4, v0
	v_min_f32_e32 v0, v4, v0
	v_max_f32_e32 v4, v5, v1
	v_min_f32_e32 v1, v5, v1
	v_max_f32_e32 v5, v6, v2
	v_min_f32_e32 v2, v6, v2
	v_max_f32_e32 v6, v7, v3
	v_min_f32_e32 v3, v7, v3
	v_max_f32_e32 v7, v11, v12
	v_min_f32_e32 v11, v11, v12
	v_max_f32_e32 v17, v16, v13
	v_min_f32_e32 v16, v16, v13
	v_max_f32_e32 v18, v15, v9
	v_min_f32_e32 v19, v15, v9
	v_max_f32_e32 v9, v8, v10
	v_min_f32_e32 v20, v8, v10
	v_max_f32_e32 v21, v14, v5
	v_min_f32_e32 v22, v14, v5
	v_max_f32_e32 v5, v4, v6
	v_min_f32_e32 v23, v4, v6
	v_max_f32_e32 v24, v0, v2
	v_min_f32_e32 v25, v0, v2
	v_max_f32_e32 v2, v1, v3
	v_min_f32_e32 v3, v1, v3
	v_max_f32_e32 v12, v7, v17
	v_min_f32_e32 v13, v7, v17
	v_max_f32_e32 v14, v11, v16
	v_min_f32_e32 v15, v11, v16
	v_max_f32_e32 v8, v18, v9
	v_min_f32_e32 v9, v18, v9
	v_max_f32_e32 v10, v19, v20
	v_min_f32_e32 v11, v19, v20
	v_max_f32_e32 v4, v21, v5
	v_min_f32_e32 v5, v21, v5
	v_max_f32_e32 v6, v22, v23
	v_min_f32_e32 v7, v22, v23
	v_max_f32_e32 v0, v24, v2
	v_min_f32_e32 v1, v24, v2
	v_max_f32_e32 v2, v25, v3
	v_min_f32_e32 v3, v25, v3
.LBB0_588:
	s_waitcnt lgkmcnt(0)
	s_barrier
	s_and_b64 vcc, exec, s[4:5]
	s_cbranch_vccnz .LBB0_590
	v_lshl_add_u32 v16, v128, 7, 0
	v_add_u32_e32 v16, 0x10000, v16
	v_and_b32_e32 v17, 0xffffff80, v12
	v_and_b32_e32 v18, 0xffffff80, v13
	v_and_b32_e32 v21, 0x7f, v77
	v_and_b32_e32 v20, 0x7f, v76
	v_and_b32_e32 v13, 0x7f, v13
	v_and_b32_e32 v12, 0x7f, v12
	v_and_b32_e32 v26, 0xffffff80, v14
	v_and_b32_e32 v28, 0xffffff80, v15
	v_and_b32_e32 v23, 0x7f, v79
	v_and_b32_e32 v22, 0x7f, v78
	v_and_b32_e32 v15, 0x7f, v15
	v_and_b32_e32 v14, 0x7f, v14
	ds_write_b128 v16, v[20:23]
	ds_write_b128 v16, v[12:15] offset:64
	v_and_b32_e32 v21, 0xffffff80, v8
	v_and_b32_e32 v23, 0xffffff80, v9
	v_and_b32_e32 v13, 0x7f, v73
	v_and_b32_e32 v12, 0x7f, v72
	v_and_b32_e32 v9, 0x7f, v9
	v_and_b32_e32 v8, 0x7f, v8
	v_and_b32_e32 v30, 0xffffff80, v10
	v_and_b32_e32 v32, 0xffffff80, v11
	v_and_b32_e32 v15, 0x7f, v75
	v_and_b32_e32 v14, 0x7f, v74
	v_and_b32_e32 v11, 0x7f, v11
	v_and_b32_e32 v10, 0x7f, v10
	v_and_b32_e32 v19, 0xffffff80, v76
	ds_write_b128 v16, v[12:15] offset:16
	ds_write_b128 v16, v[8:11] offset:80
	v_and_b32_e32 v13, 0xffffff80, v4
	v_and_b32_e32 v15, 0xffffff80, v5
	v_and_b32_e32 v9, 0x7f, v69
	v_and_b32_e32 v8, 0x7f, v68
	v_and_b32_e32 v5, 0x7f, v5
	v_and_b32_e32 v4, 0x7f, v4
	v_and_b32_e32 v34, 0xffffff80, v6
	v_and_b32_e32 v36, 0xffffff80, v7
	v_and_b32_e32 v11, 0x7f, v71
	v_and_b32_e32 v10, 0x7f, v70
	v_and_b32_e32 v7, 0x7f, v7
	v_and_b32_e32 v6, 0x7f, v6
	ds_write_b128 v16, v[8:11] offset:32
	ds_write_b128 v16, v[4:7] offset:96
	v_and_b32_e32 v5, 0x7f, v65
	v_and_b32_e32 v4, 0x7f, v64
	v_and_b32_e32 v41, 0xffffff80, v2
	v_and_b32_e32 v42, 0xffffff80, v3
	v_and_b32_e32 v7, 0x7f, v67
	v_and_b32_e32 v6, 0x7f, v66
	v_and_b32_e32 v11, 0x7f, v3
	v_and_b32_e32 v10, 0x7f, v2
	v_add_f32_e32 v2, v19, v17
	s_movk_i32 s4, 0xff00
	v_add_f32_e32 v3, v19, v18
	v_and_b32_e32 v24, 0xffffff80, v77
	ds_write_b128 v16, v[4:7] offset:48
	v_and_b32_e32 v2, 0xffffff00, v2
	v_and_or_b32 v3, v3, s4, 1
	v_add_f32_e32 v4, v19, v26
	v_add_f32_e32 v5, v19, v28
	v_and_b32_e32 v40, 0xffffff80, v1
	v_and_b32_e32 v9, 0x7f, v1
	v_and_b32_e32 v8, 0x7f, v0
	v_and_or_b32 v4, v4, s4, 2
	v_and_or_b32 v5, v5, s4, 3
	v_add_f32_e32 v48, v24, v17
	v_add_f32_e32 v49, v24, v18
	ds_write_b128 v16, v[8:11] offset:112
	v_add_f32_e32 v6, v19, v21
	v_add_f32_e32 v7, v19, v23
	v_add_f32_e32 v11, v19, v15
	v_add_f32_e32 v15, v19, v36
	v_add_f32_e32 v36, v19, v40
	v_max_f32_e32 v40, v2, v3
	v_min_f32_e32 v2, v2, v3
	v_max_f32_e32 v3, v5, v5
	v_and_or_b32 v48, v48, s4, 16
	v_and_or_b32 v49, v49, s4, 17
	v_add_f32_e32 v50, v24, v26
	v_add_f32_e32 v51, v24, v28
	v_and_or_b32 v6, v6, s4, 4
	v_and_or_b32 v7, v7, s4, 5
	v_add_f32_e32 v8, v19, v30
	v_add_f32_e32 v9, v19, v32
;     __device__ __forceinline__ void fused(f32x4 (&acc)[2][2][4][2], const Unit& u, int wr, int wc, int fr, int fq, PG8_LAS unsigned char* lds, int wid, int lane) const {
;     ...
;             { float cv[16]; cv[0] = __uint_as_float((__float_as_uint(v0[0] + v1[0]) & ~255u) | 0u); cv[1] = __uint_as_float((__float_as_uint(v0[0] + v1[1]) & ~255u) | 1u); cv[2] = __uint_as_float((__float_as_uint(v0[0] + v1[2]) & ~255u) | 2u); cv[3] = __uint_as_float((__float_as_uint(v0[0] + v1[3]) & ~255u) | 3u); cv[4] = __uint_as_float((__float_as_uint(v0[0] + v1[4]) & ~255u) | 4u); cv[5] = __uint_as_float((__float_as_uint(v0[0] + v1[5]) & ~255u) | 5u); cv[6] = __uint_as_float((__float_as_uint(v0[0] + v1[6]) & ~255u) | 6u); cv[7] = __uint_as_float((__float_as_uint(v0[0] + v1[7]) & ~255u) | 7u); cv[8] = __uint_as_float((__float_as_uint(v0[0] + v1[8]) & ~255u) | 8u); cv[9] = __uint_as_float((__float_as_uint(v0[0] + v1[9]) & ~255u) | 9u); cv[10] = __uint_as_float((__float_as_uint(v0[0] + v1[10]) & ~255u) | 10u); cv[11] = __uint_as_float((__float_as_uint(v0[0] + v1[11]) & ~255u) | 11u); cv[12] = __uint_as_float((__float_as_uint(v0[0] + v1[12]) & ~255u) | 12u); cv[13] = __uint_as_float((__float_as_uint(v0[0] + v1[13]) & ~255u) | 13u); cv[14] = __uint_as_float((__float_as_uint(v0[0] + v1[14]) & ~255u) | 14u); cv[15] = __uint_as_float((__float_as_uint(v0[0] + v1[15]) & ~255u) | 15u); sort16_desc(cv);
; #pragma unroll
;               for (int q = 0; q < 16; ++q) best[q] = cv[q]; }
	v_max_f32_e32 v5, v4, v3
	v_min_f32_e32 v3, v4, v3
	v_and_or_b32 v50, v50, s4, 18
	v_and_or_b32 v51, v51, s4, 19
	v_and_or_b32 v8, v8, s4, 6
	v_and_or_b32 v9, v9, s4, 7
	v_max_f32_e32 v4, v40, v5
	v_min_f32_e32 v5, v40, v5
	v_max_f32_e32 v40, v2, v3
	v_add_f32_e32 v52, v24, v21
	v_add_f32_e32 v23, v24, v23
	v_add_f32_e32 v30, v24, v30
	v_add_f32_e32 v24, v24, v32
	v_max_f32_e32 v58, v48, v49
	v_min_f32_e32 v48, v48, v49
	v_max_f32_e32 v49, v51, v51
	v_min_f32_e32 v2, v2, v3
	v_max_f32_e32 v3, v40, v5
	v_min_f32_e32 v5, v40, v5
	v_max_f32_e32 v40, v6, v7
	v_min_f32_e32 v6, v6, v7
	v_max_f32_e32 v7, v9, v9
	v_and_or_b32 v52, v52, s4, 20
	v_and_or_b32 v23, v23, s4, 21
	v_and_or_b32 v30, v30, s4, 22
	v_and_or_b32 v24, v24, s4, 23
	v_max_f32_e32 v51, v50, v49
	v_min_f32_e32 v49, v50, v49
	v_max_f32_e32 v9, v8, v7
	v_min_f32_e32 v7, v8, v7
	v_max_f32_e32 v50, v58, v51
	v_min_f32_e32 v51, v58, v51
	v_max_f32_e32 v58, v48, v49
	v_max_f32_e32 v8, v40, v9
	v_min_f32_e32 v9, v40, v9
	v_max_f32_e32 v40, v6, v7
	v_min_f32_e32 v48, v48, v49
	v_max_f32_e32 v49, v58, v51
	v_min_f32_e32 v51, v58, v51
	v_max_f32_e32 v58, v52, v23
	v_min_f32_e32 v23, v52, v23
	v_max_f32_e32 v52, v30, v24
	v_min_f32_e32 v24, v30, v24
	v_min_f32_e32 v6, v6, v7
	v_max_f32_e32 v7, v40, v9
	v_min_f32_e32 v9, v40, v9
	v_max_f32_e32 v30, v58, v52
	v_min_f32_e32 v52, v58, v52
	v_max_f32_e32 v58, v23, v24
	v_max_f32_e32 v40, v4, v8
	v_min_f32_e32 v4, v4, v8
	v_max_f32_e32 v8, v5, v9
	v_min_f32_e32 v23, v23, v24
	v_max_f32_e32 v24, v58, v52
	v_min_f32_e32 v52, v58, v52
	v_and_b32_e32 v25, 0xffffff80, v78
	v_add_f32_e32 v10, v19, v13
	v_min_f32_e32 v5, v5, v9
	v_max_f32_e32 v9, v8, v4
	v_min_f32_e32 v4, v8, v4
	v_max_f32_e32 v8, v3, v7
	v_min_f32_e32 v3, v3, v7
	v_max_f32_e32 v7, v2, v6
	v_max_f32_e32 v58, v50, v30
	v_min_f32_e32 v30, v50, v30
	v_max_f32_e32 v50, v51, v52
	v_and_or_b32 v10, v10, s4, 8
	v_and_or_b32 v11, v11, s4, 9
	v_add_f32_e32 v13, v19, v34
	v_min_f32_e32 v2, v2, v6
	v_max_f32_e32 v6, v7, v3
	v_min_f32_e32 v3, v7, v3
	v_add_f32_e32 v32, v25, v17
	v_add_f32_e32 v53, v25, v18
	v_min_f32_e32 v51, v51, v52
	v_max_f32_e32 v52, v50, v30
	v_min_f32_e32 v30, v50, v30
	v_max_f32_e32 v50, v49, v24
	v_min_f32_e32 v24, v49, v24
	v_max_f32_e32 v49, v48, v23
	v_and_or_b32 v13, v13, s4, 10
	v_and_or_b32 v15, v15, s4, 11
	v_max_f32_e32 v7, v8, v9
	v_min_f32_e32 v8, v8, v9
	v_max_f32_e32 v9, v6, v4
	v_min_f32_e32 v4, v6, v4
	v_max_f32_e32 v6, v3, v5
	v_min_f32_e32 v3, v3, v5
	v_max_f32_e32 v5, v11, v11
	v_and_or_b32 v32, v32, s4, 32
	v_and_or_b32 v53, v53, s4, 33
	v_add_f32_e32 v54, v25, v26
	v_add_f32_e32 v55, v25, v28
	v_min_f32_e32 v23, v48, v23
	v_max_f32_e32 v48, v49, v24
	v_min_f32_e32 v24, v49, v24
	v_and_b32_e32 v27, 0xffffff80, v79
	v_and_b32_e32 v38, 0xffffff80, v0
	v_max_f32_e32 v11, v10, v5
	v_min_f32_e32 v5, v10, v5
	v_max_f32_e32 v10, v15, v15
	v_and_or_b32 v54, v54, s4, 34
	v_and_or_b32 v55, v55, s4, 35
	v_max_f32_e32 v49, v50, v52
	v_min_f32_e32 v50, v50, v52
	v_max_f32_e32 v52, v48, v30
	v_min_f32_e32 v30, v48, v30
	v_max_f32_e32 v48, v24, v51
	v_min_f32_e32 v24, v24, v51
	v_max_f32_e32 v51, v53, v53
	v_add_f32_e32 v34, v19, v38
	v_max_f32_e32 v15, v13, v10
	v_min_f32_e32 v10, v13, v10
	v_add_f32_e32 v21, v25, v21
	v_add_f32_e32 v25, v27, v17
	v_max_f32_e32 v53, v32, v51
	v_min_f32_e32 v32, v32, v51
	v_max_f32_e32 v51, v55, v55
	v_and_or_b32 v34, v34, s4, 12
	v_and_or_b32 v36, v36, s4, 13
	v_add_f32_e32 v38, v19, v41
	v_add_f32_e32 v19, v19, v42
	v_max_f32_e32 v13, v11, v15
	v_min_f32_e32 v11, v11, v15
	v_max_f32_e32 v15, v5, v10
	v_and_or_b32 v21, v21, s4, 36
	v_and_or_b32 v25, v25, s4, 48
	v_add_f32_e32 v56, v27, v18
	v_add_f32_e32 v57, v27, v26
	v_max_f32_e32 v55, v54, v51
	v_min_f32_e32 v51, v54, v51
	v_and_or_b32 v38, v38, s4, 14
	v_and_or_b32 v19, v19, s4, 15
	v_min_f32_e32 v5, v5, v10
	v_max_f32_e32 v10, v15, v11
	v_min_f32_e32 v11, v15, v11
	v_max_f32_e32 v15, v36, v36
	v_and_or_b32 v56, v56, s4, 49
	v_and_or_b32 v57, v57, s4, 50
	v_max_f32_e32 v54, v53, v55
	v_min_f32_e32 v53, v53, v55
	v_max_f32_e32 v55, v32, v51
	v_max_f32_e32 v36, v34, v15
	v_min_f32_e32 v15, v34, v15
	v_max_f32_e32 v34, v38, v38
	v_min_f32_e32 v32, v32, v51
	v_max_f32_e32 v51, v55, v53
	v_min_f32_e32 v53, v55, v53
	v_max_f32_e32 v55, v21, v25
	v_min_f32_e32 v21, v21, v25
	v_max_f32_e32 v25, v57, v57
	v_max_f32_e32 v38, v34, v19
	v_min_f32_e32 v19, v34, v19
	v_max_f32_e32 v57, v56, v25
	v_min_f32_e32 v25, v56, v25
	v_max_f32_e32 v34, v36, v38
	v_min_f32_e32 v36, v36, v38
	v_max_f32_e32 v38, v15, v19
	v_max_f32_e32 v56, v55, v57
	v_min_f32_e32 v55, v55, v57
	v_max_f32_e32 v57, v21, v25
	v_min_f32_e32 v15, v15, v19
	v_max_f32_e32 v19, v38, v36
	v_min_f32_e32 v36, v38, v36
	v_min_f32_e32 v21, v21, v25
	v_max_f32_e32 v25, v57, v55
	v_min_f32_e32 v55, v57, v55
	v_max_f32_e32 v38, v13, v34
	v_min_f32_e32 v13, v13, v34
	v_max_f32_e32 v34, v11, v36
	v_max_f32_e32 v57, v54, v56
	v_min_f32_e32 v54, v54, v56
	v_max_f32_e32 v56, v53, v55
	v_min_f32_e32 v11, v11, v36
	v_max_f32_e32 v36, v34, v13
	v_min_f32_e32 v13, v34, v13
	v_max_f32_e32 v34, v10, v19
	v_min_f32_e32 v10, v10, v19
	v_max_f32_e32 v19, v5, v15
	v_min_f32_e32 v53, v53, v55
	v_max_f32_e32 v55, v56, v54
	v_min_f32_e32 v54, v56, v54
	v_max_f32_e32 v56, v51, v25
	v_min_f32_e32 v25, v51, v25
	v_max_f32_e32 v51, v32, v21
	v_min_f32_e32 v5, v5, v15
	v_max_f32_e32 v15, v19, v10
	v_min_f32_e32 v21, v32, v21
	v_max_f32_e32 v32, v51, v25
	v_min_f32_e32 v10, v19, v10
	v_max_f32_e32 v19, v34, v36
	v_min_f32_e32 v34, v34, v36
	v_max_f32_e32 v36, v15, v13
	v_min_f32_e32 v13, v15, v13
	v_min_f32_e32 v25, v51, v25
	v_max_f32_e32 v51, v56, v55
;     __device__ __forceinline__ void fused(f32x4 (&acc)[2][2][4][2], const Unit& u, int wr, int wc, int fr, int fq, PG8_LAS unsigned char* lds, int wid, int lane) const {
;     ...
;             { float cv[16]; cv[0] = __uint_as_float((__float_as_uint(v0[1] + v1[0]) & ~255u) | 16u); cv[1] = __uint_as_float((__float_as_uint(v0[1] + v1[1]) & ~255u) | 17u); cv[2] = __uint_as_float((__float_as_uint(v0[1] + v1[2]) & ~255u) | 18u); cv[3] = __uint_as_float((__float_as_uint(v0[1] + v1[3]) & ~255u) | 19u); cv[4] = __uint_as_float((__float_as_uint(v0[1] + v1[4]) & ~255u) | 20u); cv[5] = __uint_as_float((__float_as_uint(v0[1] + v1[5]) & ~255u) | 21u); cv[6] = __uint_as_float((__float_as_uint(v0[1] + v1[6]) & ~255u) | 22u); cv[7] = __uint_as_float((__float_as_uint(v0[1] + v1[7]) & ~255u) | 23u); cv[8] = __uint_as_float((__float_as_uint(v0[2] + v1[0]) & ~255u) | 32u); cv[9] = __uint_as_float((__float_as_uint(v0[2] + v1[1]) & ~255u) | 33u); cv[10] = __uint_as_float((__float_as_uint(v0[2] + v1[2]) & ~255u) | 34u); cv[11] = __uint_as_float((__float_as_uint(v0[2] + v1[3]) & ~255u) | 35u); cv[12] = __uint_as_float((__float_as_uint(v0[2] + v1[4]) & ~255u) | 36u); cv[13] = __uint_as_float((__float_as_uint(v0[3] + v1[0]) & ~255u) | 48u); cv[14] = __uint_as_float((__float_as_uint(v0[3] + v1[1]) & ~255u) | 49u); cv[15] = __uint_as_float((__float_as_uint(v0[3] + v1[2]) & ~255u) | 50u); sort16_desc(cv); merge_top16(best, cv); }
	v_min_f32_e32 v55, v56, v55
	v_max_f32_e32 v56, v32, v54
	v_min_f32_e32 v32, v32, v54
	v_max_f32_e32 v15, v10, v11
	v_min_f32_e32 v10, v10, v11
	v_min_f32_e32 v11, v40, v38
	v_max_f32_e32 v41, v4, v13
	v_max_f32_e32 v54, v25, v53
	v_min_f32_e32 v25, v25, v53
	v_min_f32_e32 v53, v58, v57
	v_max_f32_e32 v59, v30, v32
	v_min_f32_e32 v4, v4, v13
	v_max_f32_e32 v13, v41, v11
	v_min_f32_e32 v11, v41, v11
	v_max_f32_e32 v41, v8, v34
	v_min_f32_e32 v8, v8, v34
	v_max_f32_e32 v34, v3, v10
	v_min_f32_e32 v30, v30, v32
	v_max_f32_e32 v32, v59, v53
	v_min_f32_e32 v53, v59, v53
	v_max_f32_e32 v59, v50, v55
	v_min_f32_e32 v50, v50, v55
	v_max_f32_e32 v55, v24, v25
	v_min_f32_e32 v3, v3, v10
	v_max_f32_e32 v10, v34, v8
	v_min_f32_e32 v8, v34, v8
	v_min_f32_e32 v24, v24, v25
	v_max_f32_e32 v25, v55, v50
	v_min_f32_e32 v50, v55, v50
	v_max_f32_e32 v34, v41, v13
	v_min_f32_e32 v13, v41, v13
	v_max_f32_e32 v41, v10, v11
	v_min_f32_e32 v10, v10, v11
	v_max_f32_e32 v11, v8, v4
	v_min_f32_e32 v4, v8, v4
	v_max_f32_e32 v8, v7, v19
	v_min_f32_e32 v7, v7, v19
	v_max_f32_e32 v19, v6, v15
	v_max_f32_e32 v55, v59, v32
	v_min_f32_e32 v32, v59, v32
	v_max_f32_e32 v59, v25, v53
	v_min_f32_e32 v25, v25, v53
	v_max_f32_e32 v53, v50, v30
	v_min_f32_e32 v30, v50, v30
	v_max_f32_e32 v50, v49, v51
	v_min_f32_e32 v49, v49, v51
	v_max_f32_e32 v51, v48, v54
	v_min_f32_e32 v6, v6, v15
	v_max_f32_e32 v15, v19, v7
	v_min_f32_e32 v7, v19, v7
	v_max_f32_e32 v19, v9, v36
	v_min_f32_e32 v9, v9, v36
	v_max_f32_e32 v36, v2, v5
	v_min_f32_e32 v48, v48, v54
	v_max_f32_e32 v54, v51, v49
	v_min_f32_e32 v49, v51, v49
	v_max_f32_e32 v51, v52, v56
	v_min_f32_e32 v52, v52, v56
	v_max_f32_e32 v56, v23, v21
	v_min_f32_e32 v2, v2, v5
	v_max_f32_e32 v5, v36, v9
	v_min_f32_e32 v9, v36, v9
	v_max_f32_e32 v36, v19, v15
	v_min_f32_e32 v21, v23, v21
	v_max_f32_e32 v23, v56, v52
	v_min_f32_e32 v52, v56, v52
	v_and_b32_e32 v20, 0xffffff80, v72
	v_min_f32_e32 v15, v19, v15
	v_max_f32_e32 v19, v5, v7
	v_min_f32_e32 v5, v5, v7
	v_max_f32_e32 v7, v9, v6
	v_min_f32_e32 v6, v9, v6
	v_min_f32_e32 v9, v8, v34
	v_min_f32_e32 v42, v36, v13
	v_max_f32_e32 v56, v51, v54
	v_min_f32_e32 v51, v51, v54
	v_max_f32_e32 v54, v23, v49
	v_min_f32_e32 v23, v23, v49
	v_max_f32_e32 v49, v52, v48
	v_min_f32_e32 v48, v52, v48
	v_and_b32_e32 v39, 0xffffff80, v65
	v_min_f32_e32 v65, v48, v24
	v_max3_f32 v9, v9, v48, v24
	v_max3_f32 v24, v42, v49, v30
	v_add_f32_e32 v27, v27, v28
	v_add_f32_e32 v28, v20, v17
	v_add_f32_e32 v42, v20, v18
	v_add_f32_e32 v20, v20, v26
	v_and_b32_e32 v22, 0xffffff80, v73
	v_and_or_b32 v27, v27, s4, 51
	v_and_or_b32 v28, v28, s4, 64
	v_and_b32_e32 v42, 0xffffff00, v42
	v_and_b32_e32 v20, 0xffffff00, v20
	v_and_b32_e32 v29, 0xffffff80, v74
	v_and_b32_e32 v31, 0xffffff80, v75
	v_and_b32_e32 v33, 0xffffff80, v70
	v_and_b32_e32 v35, 0xffffff80, v71
	v_and_b32_e32 v37, 0xffffff80, v64
	v_min_f32_e32 v43, v15, v41
	v_min_f32_e32 v44, v19, v10
	v_min_f32_e32 v62, v54, v25
	v_or_b32_e32 v42, 0x41, v42
	v_or_b32_e32 v20, 0x42, v20
	v_add_f32_e32 v26, v22, v17
	v_add_f32_e32 v22, v22, v18
	v_min_f32_e32 v63, v23, v53
	v_max3_f32 v23, v43, v23, v53
	v_max3_f32 v10, v19, v10, v62
	v_max3_f32 v19, v44, v54, v25
	v_and_b32_e32 v26, 0xffffff00, v26
	v_and_b32_e32 v22, 0xffffff00, v22
	v_add_f32_e32 v43, v29, v17
	v_add_f32_e32 v29, v29, v18
	v_add_f32_e32 v44, v31, v17
	v_add_f32_e32 v18, v31, v18
	v_add_f32_e32 v31, v33, v17
	v_add_f32_e32 v33, v35, v17
	v_add_f32_e32 v35, v37, v17
	v_add_f32_e32 v37, v39, v17
	v_max_f32_e32 v39, v27, v28
	v_min_f32_e32 v27, v27, v28
	v_max_f32_e32 v28, v42, v42
	v_or_b32_e32 v26, 0x50, v26
	v_or_b32_e32 v22, 0x51, v22
	v_and_b32_e32 v43, 0xffffff00, v43
	v_and_b32_e32 v29, 0xffffff00, v29
	v_max_f32_e32 v42, v28, v20
	v_min_f32_e32 v20, v28, v20
	v_or_b32_e32 v43, 0x60, v43
	v_or_b32_e32 v29, 0x61, v29
	v_max_f32_e32 v28, v39, v42
	v_min_f32_e32 v39, v39, v42
	v_max_f32_e32 v42, v27, v20
	v_min_f32_e32 v20, v27, v20
	v_max_f32_e32 v27, v42, v39
	v_min_f32_e32 v39, v42, v39
	v_max_f32_e32 v42, v26, v22
	v_min_f32_e32 v22, v26, v22
	v_max_f32_e32 v26, v29, v29
	v_max_f32_e32 v29, v43, v43
	v_max_f32_e32 v43, v29, v26
	v_min_f32_e32 v26, v29, v26
	v_max_f32_e32 v29, v42, v43
	v_min_f32_e32 v42, v42, v43
	v_max_f32_e32 v43, v22, v26
	v_and_b32_e32 v12, 0xffffff80, v68
	v_and_b32_e32 v14, 0xffffff80, v69
	v_min_f32_e32 v22, v22, v26
	v_max_f32_e32 v26, v43, v42
	v_min_f32_e32 v42, v43, v42
	v_add_f32_e32 v12, v12, v17
	v_add_f32_e32 v14, v14, v17
	v_max_f32_e32 v43, v28, v29
	v_min_f32_e32 v28, v28, v29
	v_max_f32_e32 v29, v39, v42
	v_and_b32_e32 v44, 0xffffff00, v44
	v_and_b32_e32 v18, 0xffffff00, v18
	v_and_b32_e32 v12, 0xffffff00, v12
	v_and_b32_e32 v14, 0xffffff00, v14
	v_min_f32_e32 v39, v39, v42
	v_max_f32_e32 v42, v29, v28
	v_min_f32_e32 v28, v29, v28
	v_max_f32_e32 v29, v27, v26
	v_min_f32_e32 v26, v27, v26
	v_max_f32_e32 v27, v20, v22
	v_or_b32_e32 v44, 0x70, v44
	v_or_b32_e32 v18, 0x71, v18
	v_or_b32_e32 v12, 0x80, v12
	v_or_b32_e32 v14, 0x90, v14
	v_min_f32_e32 v20, v20, v22
	v_max_f32_e32 v22, v27, v26
	v_min_f32_e32 v26, v27, v26
	v_and_b32_e32 v31, 0xffffff00, v31
	v_and_b32_e32 v33, 0xffffff00, v33
	v_max_f32_e32 v27, v29, v42
	v_min_f32_e32 v29, v29, v42
	v_max_f32_e32 v42, v22, v28
	v_min_f32_e32 v22, v22, v28
	v_max_f32_e32 v28, v26, v39
	v_min_f32_e32 v26, v26, v39
	v_max_f32_e32 v39, v44, v44
	v_or_b32_e32 v31, 0xa0, v31
	v_or_b32_e32 v33, 0xb0, v33
	v_and_b32_e32 v35, 0xffffff00, v35
	v_and_b32_e32 v37, 0xffffff00, v37
	v_max_f32_e32 v44, v39, v18
	v_min_f32_e32 v18, v39, v18
	v_max_f32_e32 v39, v12, v14
	v_min_f32_e32 v12, v12, v14
	v_or_b32_e32 v35, 0xc0, v35
;     __device__ __forceinline__ void fused(f32x4 (&acc)[2][2][4][2], const Unit& u, int wr, int wc, int fr, int fq, PG8_LAS unsigned char* lds, int wid, int lane) const {
;     ...
;             { float cv[16]; cv[0] = __uint_as_float((__float_as_uint(v0[3] + v1[3]) & ~255u) | 51u); cv[1] = __uint_as_float((__float_as_uint(v0[4] + v1[0]) & ~255u) | 64u); cv[2] = __uint_as_float((__float_as_uint(v0[4] + v1[1]) & ~255u) | 65u); cv[3] = __uint_as_float((__float_as_uint(v0[4] + v1[2]) & ~255u) | 66u); cv[4] = __uint_as_float((__float_as_uint(v0[5] + v1[0]) & ~255u) | 80u); cv[5] = __uint_as_float((__float_as_uint(v0[5] + v1[1]) & ~255u) | 81u); cv[6] = __uint_as_float((__float_as_uint(v0[6] + v1[0]) & ~255u) | 96u); cv[7] = __uint_as_float((__float_as_uint(v0[6] + v1[1]) & ~255u) | 97u); cv[8] = __uint_as_float((__float_as_uint(v0[7] + v1[0]) & ~255u) | 112u); cv[9] = __uint_as_float((__float_as_uint(v0[7] + v1[1]) & ~255u) | 113u); cv[10] = __uint_as_float((__float_as_uint(v0[8] + v1[0]) & ~255u) | 128u); cv[11] = __uint_as_float((__float_as_uint(v0[9] + v1[0]) & ~255u) | 144u); cv[12] = __uint_as_float((__float_as_uint(v0[10] + v1[0]) & ~255u) | 160u); cv[13] = __uint_as_float((__float_as_uint(v0[11] + v1[0]) & ~255u) | 176u); cv[14] = __uint_as_float((__float_as_uint(v0[12] + v1[0]) & ~255u) | 192u); cv[15] = __uint_as_float((__float_as_uint(v0[13] + v1[0]) & ~255u) | 208u); sort16_desc(cv); merge_top16(best, cv); }
;             { float cv[16]; cv[0] = __uint_as_float((__float_as_uint(v0[14] + v1[0]) & ~255u) | 224u); cv[1] = __uint_as_float((__float_as_uint(v0[15] + v1[0]) & ~255u) | 240u); cv[2] = -INFINITY; cv[3] = -INFINITY; cv[4] = -INFINITY; cv[5] = -INFINITY; cv[6] = -INFINITY; cv[7] = -INFINITY; cv[8] = -INFINITY; cv[9] = -INFINITY; cv[10] = -INFINITY; cv[11] = -INFINITY; cv[12] = -INFINITY; cv[13] = -INFINITY; cv[14] = -INFINITY; cv[15] = -INFINITY; sort16_desc(cv); merge_top16(best, cv); }
	v_or_b32_e32 v37, 0xd0, v37
	v_max_f32_e32 v14, v44, v39
	v_min_f32_e32 v39, v44, v39
	v_max_f32_e32 v44, v18, v12
	v_min_f32_e32 v12, v18, v12
	v_max_f32_e32 v18, v44, v39
	v_min_f32_e32 v39, v44, v39
	v_max_f32_e32 v44, v31, v33
	v_min_f32_e32 v31, v31, v33
	v_max_f32_e32 v33, v37, v37
	v_max_f32_e32 v37, v35, v33
	v_min_f32_e32 v33, v35, v33
	v_max_f32_e32 v35, v44, v37
	v_min_f32_e32 v37, v44, v37
	v_max_f32_e32 v44, v31, v33
	v_min_f32_e32 v31, v31, v33
	v_max_f32_e32 v33, v44, v37
	v_min_f32_e32 v37, v44, v37
	v_max_f32_e32 v44, v14, v35
	v_min_f32_e32 v14, v14, v35
	v_max_f32_e32 v35, v39, v37
	v_min_f32_e32 v37, v39, v37
	v_max_f32_e32 v39, v35, v14
	v_min_f32_e32 v14, v35, v14
	v_max_f32_e32 v35, v18, v33
	v_min_f32_e32 v18, v18, v33
	v_max_f32_e32 v33, v12, v31
	v_min_f32_e32 v12, v12, v31
	v_max_f32_e32 v31, v33, v18
	v_min_f32_e32 v45, v5, v11
	v_min_f32_e32 v61, v51, v59
	v_min_f32_e32 v18, v33, v18
	v_max_f32_e32 v33, v35, v39
	v_min_f32_e32 v35, v35, v39
	v_max_f32_e32 v39, v31, v14
	v_min_f32_e32 v14, v31, v14
	v_max3_f32 v5, v5, v11, v61
	v_max3_f32 v11, v45, v51, v59
	v_max_f32_e32 v31, v18, v37
	v_min_f32_e32 v18, v18, v37
	v_min_f32_e32 v37, v43, v44
	v_max_f32_e32 v45, v22, v14
	v_min_f32_e32 v14, v22, v14
	v_max_f32_e32 v22, v45, v37
	v_min_f32_e32 v37, v45, v37
	v_max_f32_e32 v45, v29, v35
	v_min_f32_e32 v29, v29, v35
	v_max_f32_e32 v35, v26, v18
	v_min_f32_e32 v46, v7, v4
	v_min_f32_e32 v47, v6, v3
	v_min_f32_e32 v52, v50, v55
	v_min_f32_e32 v60, v56, v32
	v_min_f32_e32 v64, v49, v30
	v_min_f32_e32 v18, v26, v18
	v_max_f32_e32 v26, v35, v29
	v_min_f32_e32 v29, v35, v29
	v_max3_f32 v21, v40, v38, v21
	v_max3_f32 v8, v8, v34, v65
	v_max3_f32 v13, v36, v13, v64
	v_max3_f32 v15, v15, v41, v63
	v_max3_f32 v4, v7, v4, v60
	v_max3_f32 v7, v46, v56, v32
	v_max3_f32 v3, v6, v3, v52
	v_max3_f32 v6, v47, v50, v55
	v_max3_f32 v2, v2, v58, v57
	v_max_f32_e32 v35, v45, v22
	v_min_f32_e32 v22, v45, v22
	v_max_f32_e32 v45, v26, v37
	v_min_f32_e32 v26, v26, v37
	v_max_f32_e32 v37, v29, v14
	v_min_f32_e32 v14, v29, v14
	v_max_f32_e32 v29, v27, v33
	v_min_f32_e32 v27, v27, v33
	v_max_f32_e32 v33, v28, v31
	v_max_f32_e32 v25, v21, v19
	v_min_f32_e32 v19, v21, v19
	v_max_f32_e32 v21, v8, v5
	v_min_f32_e32 v5, v8, v5
	v_max_f32_e32 v8, v9, v11
	v_min_f32_e32 v9, v9, v11
	v_max_f32_e32 v11, v13, v4
	v_min_f32_e32 v4, v13, v4
	v_max_f32_e32 v13, v24, v7
	v_min_f32_e32 v7, v24, v7
	v_max_f32_e32 v24, v15, v3
	v_min_f32_e32 v3, v15, v3
	v_max_f32_e32 v15, v23, v6
	v_min_f32_e32 v6, v23, v6
	v_max_f32_e32 v23, v10, v2
	v_min_f32_e32 v2, v10, v2
	v_min_f32_e32 v28, v28, v31
	v_max_f32_e32 v31, v33, v27
	v_min_f32_e32 v27, v33, v27
	v_max_f32_e32 v33, v42, v39
	v_min_f32_e32 v39, v42, v39
	v_max_f32_e32 v42, v20, v12
	v_max_f32_e32 v10, v25, v13
	v_min_f32_e32 v13, v25, v13
	v_max_f32_e32 v25, v21, v24
	v_min_f32_e32 v21, v21, v24
	v_max_f32_e32 v24, v8, v15
	v_min_f32_e32 v8, v8, v15
	v_max_f32_e32 v15, v11, v23
	v_min_f32_e32 v11, v11, v23
	v_max_f32_e32 v23, v19, v7
	v_min_f32_e32 v7, v19, v7
	v_max_f32_e32 v19, v5, v3
	v_min_f32_e32 v3, v5, v3
	v_max_f32_e32 v5, v9, v6
	v_min_f32_e32 v6, v9, v6
	v_max_f32_e32 v9, v4, v2
	v_min_f32_e32 v2, v4, v2
	v_min_f32_e32 v12, v20, v12
	v_max_f32_e32 v20, v42, v39
	v_min_f32_e32 v39, v42, v39
	v_and_b32_e32 v1, 0xffffff80, v66
	v_and_b32_e32 v0, 0xffffff80, v67
	v_max_f32_e32 v4, v10, v24
	v_min_f32_e32 v10, v10, v24
	v_max_f32_e32 v24, v25, v15
	v_min_f32_e32 v15, v25, v15
	v_max_f32_e32 v25, v13, v8
	v_min_f32_e32 v8, v13, v8
	v_max_f32_e32 v13, v21, v11
	v_min_f32_e32 v11, v21, v11
	v_max_f32_e32 v21, v23, v5
	v_min_f32_e32 v5, v23, v5
	v_max_f32_e32 v23, v19, v9
	v_min_f32_e32 v9, v19, v9
	v_max_f32_e32 v19, v7, v6
	v_min_f32_e32 v6, v7, v6
	v_max_f32_e32 v7, v3, v2
	v_min_f32_e32 v2, v3, v2
	v_max_f32_e32 v42, v33, v31
	v_min_f32_e32 v31, v33, v31
	v_max_f32_e32 v33, v20, v27
	v_min_f32_e32 v20, v20, v27
	v_max_f32_e32 v27, v39, v28
	v_min_f32_e32 v28, v39, v28
	v_min_f32_e32 v3, v4, v24
	v_min_f32_e32 v30, v10, v15
	v_min_f32_e32 v32, v25, v13
	v_min_f32_e32 v34, v8, v11
	v_min_f32_e32 v36, v21, v23
	v_min_f32_e32 v38, v5, v9
	v_min_f32_e32 v40, v19, v7
	v_min_f32_e32 v41, v6, v2
	v_max_f32_e32 v39, v29, v35
	v_min_f32_e32 v29, v29, v35
	v_max_f32_e32 v35, v42, v22
	v_min_f32_e32 v22, v42, v22
	v_max_f32_e32 v42, v31, v45
	v_min_f32_e32 v31, v31, v45
	v_max_f32_e32 v45, v33, v26
	v_min_f32_e32 v26, v33, v26
	v_max_f32_e32 v33, v20, v37
	v_min_f32_e32 v20, v20, v37
	v_max_f32_e32 v37, v27, v14
	v_min_f32_e32 v14, v27, v14
	v_max_f32_e32 v27, v28, v18
	v_min_f32_e32 v18, v28, v18
	v_add_f32_e32 v1, v1, v17
	v_add_f32_e32 v0, v0, v17
	v_max3_f32 v4, v4, v24, v12
	v_max_f32_e32 v3, v3, v18
	v_max3_f32 v10, v10, v15, v27
	v_max_f32_e32 v12, v30, v14
	v_max3_f32 v13, v25, v13, v37
	v_max_f32_e32 v14, v32, v20
	v_max3_f32 v8, v8, v11, v33
	v_max_f32_e32 v11, v34, v26
	v_max3_f32 v15, v21, v23, v45
	v_max_f32_e32 v18, v36, v31
	v_max3_f32 v5, v5, v9, v42
	v_max_f32_e32 v9, v38, v22
	v_max3_f32 v7, v19, v7, v35
	v_max_f32_e32 v19, v40, v29
	v_max3_f32 v2, v6, v2, v39
	v_max3_f32 v6, v41, v43, v44
	v_and_b32_e32 v1, 0xffffff00, v1
	v_and_b32_e32 v0, 0xffffff00, v0
	v_max_f32_e32 v20, v4, v15
	v_min_f32_e32 v4, v4, v15
	v_max_f32_e32 v15, v3, v18
	v_min_f32_e32 v3, v3, v18
	v_max_f32_e32 v18, v10, v5
	v_min_f32_e32 v5, v10, v5
	v_max_f32_e32 v10, v12, v9
	v_min_f32_e32 v9, v12, v9
	v_max_f32_e32 v12, v13, v7
	v_min_f32_e32 v7, v13, v7
	v_max_f32_e32 v13, v14, v19
	v_min_f32_e32 v14, v14, v19
	v_max_f32_e32 v19, v8, v2
	v_min_f32_e32 v2, v8, v2
	v_max_f32_e32 v8, v11, v6
	v_min_f32_e32 v6, v11, v6
; #define RT_PK(q_) (ex[q_] | (int)((__float_as_uint(usc[ex[q_]]) >> 23) << 14))
;     __device__ __forceinline__ void fused(f32x4 (&acc)[2][2][4][2], const Unit& u, int wr, int wc, int fr, int fq, PG8_LAS unsigned char* lds, int wid, int lane) const {
;     ...
;             { float cv[16]; cv[0] = __uint_as_float((__float_as_uint(v0[14] + v1[0]) & ~255u) | 224u); cv[1] = __uint_as_float((__float_as_uint(v0[15] + v1[0]) & ~255u) | 240u); cv[2] = -INFINITY; cv[3] = -INFINITY; cv[4] = -INFINITY; cv[5] = -INFINITY; cv[6] = -INFINITY; cv[7] = -INFINITY; cv[8] = -INFINITY; cv[9] = -INFINITY; cv[10] = -INFINITY; cv[11] = -INFINITY; cv[12] = -INFINITY; cv[13] = -INFINITY; cv[14] = -INFINITY; cv[15] = -INFINITY; sort16_desc(cv); merge_top16(best, cv); }
;             float sc[16], sum = 0.f;
; #pragma unroll
;             for (int q = 0; q < 16; ++q) { sc[q] = __uint_as_float(__float_as_uint(best[q]) & ~255u); }
;             const float smax = sc[0];
; #pragma unroll
;             for (int q = 0; q < 16; ++q) { sc[q] = __builtin_amdgcn_exp2f((sc[q] - smax) * 1.4426950408889634f); }
; #pragma unroll
;             for (int q = 0; q < 16; ++q) sum += sc[q];
;             const float rs = 1.0f / sum;
;             asm volatile("s_waitcnt lgkmcnt(0)" ::: "memory");
;             int ex[16];
; #pragma unroll
;             for (int q = 0; q < 16; ++q) { const unsigned cid = __float_as_uint(best[q]) & 255u; ex[q] = idxl[cid >> 4] * 128 + idxl[16 + (cid & 15u)]; }
;             const size_t o = ((size_t)u.pn * 16384 + (size_t)(u.pm * BM + row)) * 16;
;             typedef int i32x4 __attribute__((ext_vector_type(4)));
; #pragma unroll
;             for (int i = 0; i < 4; ++i) {
;     ...
;                 *(i32x4*)(eidx + o + 4 * i) = (i32x4){RT_PK(4 * i), RT_PK(4 * i + 1), RT_PK(4 * i + 2), RT_PK(4 * i + 3)};
;                 *(f32x4*)(egate + o + 4 * i) = (f32x4){sc[4 * i] * rs * vsc[ex[4 * i]], sc[4 * i + 1] * rs * vsc[ex[4 * i + 1]], sc[4 * i + 2] * rs * vsc[ex[4 * i + 2]], sc[4 * i + 3] * rs * vsc[ex[4 * i + 3]]};
	v_or_b32_e32 v1, 0xe0, v1
	v_or_b32_e32 v0, 0xf0, v0
	v_max_f32_e32 v11, v20, v12
	v_min_f32_e32 v12, v20, v12
	v_max_f32_e32 v20, v15, v13
	v_min_f32_e32 v13, v15, v13
	v_max_f32_e32 v15, v18, v19
	v_min_f32_e32 v18, v18, v19
	v_max_f32_e32 v19, v10, v8
	v_min_f32_e32 v8, v10, v8
	v_max_f32_e32 v10, v4, v7
	v_min_f32_e32 v4, v4, v7
	v_max_f32_e32 v7, v3, v14
	v_min_f32_e32 v3, v3, v14
	v_max_f32_e32 v14, v5, v2
	v_min_f32_e32 v2, v5, v2
	v_max_f32_e32 v5, v9, v6
	v_min_f32_e32 v6, v9, v6
	v_max_f32_e32 v9, v11, v15
	v_min_f32_e32 v11, v11, v15
	v_max_f32_e32 v15, v20, v19
	v_min_f32_e32 v19, v20, v19
	v_max_f32_e32 v20, v12, v18
	v_min_f32_e32 v12, v12, v18
	v_max_f32_e32 v18, v13, v8
	v_min_f32_e32 v8, v13, v8
	v_max_f32_e32 v13, v10, v14
	v_min_f32_e32 v10, v10, v14
	v_max_f32_e32 v14, v7, v5
	v_min_f32_e32 v5, v7, v5
	v_max_f32_e32 v7, v4, v2
	v_min_f32_e32 v2, v4, v2
	v_max_f32_e32 v4, v3, v6
	v_min_f32_e32 v3, v3, v6
	v_max_f32_e32 v17, v1, v0
	v_min_f32_e32 v0, v1, v0
	v_min_f32_e32 v6, v9, v15
	v_min_f32_e32 v21, v11, v19
	v_min_f32_e32 v22, v20, v18
	v_min_f32_e32 v23, v12, v8
	v_min_f32_e32 v24, v13, v14
	v_min_f32_e32 v25, v10, v5
	v_min_f32_e32 v26, v7, v4
	v_min_f32_e32 v27, v2, v3
	s_mov_b32 s4, 0xff800000
	v_max_f32_e32 v0, 0xff800000, v0
	v_max3_f32 v1, v9, v15, s4
	v_max_f32_e32 v6, 0xff800000, v6
	v_max3_f32 v9, v11, v19, s4
	v_max_f32_e32 v11, 0xff800000, v21
	v_max3_f32 v15, v20, v18, s4
	v_max_f32_e32 v18, 0xff800000, v22
	v_max3_f32 v8, v12, v8, s4
	v_max_f32_e32 v12, 0xff800000, v23
	v_max3_f32 v13, v13, v14, s4
	v_max_f32_e32 v14, 0xff800000, v24
	v_max3_f32 v5, v10, v5, s4
	v_max_f32_e32 v10, 0xff800000, v25
	v_max3_f32 v4, v7, v4, s4
	v_max_f32_e32 v7, 0xff800000, v26
	v_max3_f32 v0, v2, v3, v0
	v_max3_f32 v2, v27, v17, s4
	v_max_f32_e32 v3, v1, v13
	v_min_f32_e32 v1, v1, v13
	v_max_f32_e32 v13, v6, v14
	v_min_f32_e32 v6, v6, v14
	v_max_f32_e32 v14, v9, v5
	v_min_f32_e32 v5, v9, v5
	v_max_f32_e32 v9, v11, v10
	v_min_f32_e32 v10, v11, v10
	v_max_f32_e32 v11, v15, v4
	v_min_f32_e32 v4, v15, v4
	v_max_f32_e32 v15, v18, v7
	v_max_f32_e32 v17, v8, v0
	v_min_f32_e32 v0, v8, v0
	v_max_f32_e32 v8, v12, v2
	v_min_f32_e32 v2, v12, v2
	v_max_f32_e32 v12, v3, v11
	v_min_f32_e32 v3, v3, v11
	v_max_f32_e32 v11, v13, v15
	v_min_f32_e32 v13, v13, v15
	v_max_f32_e32 v15, v14, v17
	v_min_f32_e32 v14, v14, v17
	v_max_f32_e32 v17, v9, v8
	v_min_f32_e32 v8, v9, v8
	v_max_f32_e32 v9, v1, v4
	v_min_f32_e32 v24, v1, v4
	v_max_f32_e32 v27, v5, v0
	v_min_f32_e32 v28, v5, v0
	v_max_f32_e32 v29, v10, v2
	v_min_f32_e32 v30, v10, v2
	v_max_f32_e32 v0, v12, v15
	v_min_f32_e32 v1, v12, v15
	v_max_f32_e32 v2, v11, v17
	v_min_f32_e32 v4, v11, v17
	v_min_f32_e32 v7, v18, v7
	v_max_f32_e32 v33, v0, v2
	v_min_f32_e32 v34, v0, v2
	v_min_f32_e32 v36, v1, v4
	v_max_f32_e32 v25, v6, v7
	v_min_f32_e32 v26, v6, v7
	v_max_f32_e32 v35, v1, v4
	v_lshrrev_b32_e32 v0, 2, v33
	v_lshrrev_b32_e32 v2, 2, v34
	v_lshrrev_b32_e32 v6, 2, v36
	v_max_f32_e32 v17, v3, v14
	v_min_f32_e32 v31, v3, v14
	v_and_b32_e32 v0, 60, v0
	v_and_b32_e32 v1, 15, v33
	v_and_b32_e32 v2, 60, v2
	v_and_b32_e32 v3, 15, v34
	v_lshrrev_b32_e32 v4, 2, v35
	v_and_b32_e32 v5, 15, v35
	v_and_b32_e32 v6, 60, v6
	v_and_b32_e32 v7, 15, v36
	s_waitcnt lgkmcnt(0)
	v_add_u32_e32 v0, v16, v0
	v_lshl_add_u32 v1, v1, 2, v16
	v_add_u32_e32 v2, v16, v2
	v_lshl_add_u32 v3, v3, 2, v16
	v_and_b32_e32 v4, 60, v4
	v_lshl_add_u32 v5, v5, 2, v16
	v_add_u32_e32 v6, v16, v6
	v_lshl_add_u32 v7, v7, 2, v16
	v_add_u32_e32 v4, v16, v4
	ds_read_b32 v0, v0
	ds_read_b32 v1, v1 offset:64
	ds_read_b32 v2, v2
	ds_read_b32 v3, v3 offset:64
	ds_read_b32 v10, v4
	ds_read_b32 v5, v5 offset:64
	ds_read_b32 v6, v6
	ds_read_b32 v7, v7 offset:64
	s_waitcnt lgkmcnt(0)
	v_lshl_add_u32 v0, v0, 7, v1
	v_ashrrev_i32_e32 v1, 31, v0
	v_lshl_add_u32 v4, v2, 7, v3
	v_lshlrev_b64 v[14:15], 2, v[0:1]
	v_lshl_add_u32 v10, v10, 7, v5
	v_lshl_add_u32 v12, v6, 7, v7
	v_lshl_add_u64 v[2:3], s[8:9], 0, v[14:15]
	v_ashrrev_i32_e32 v5, 31, v4
	v_max_f32_e32 v32, v13, v8
	v_min_f32_e32 v8, v13, v8
	global_load_dword v1, v[2:3], off
	v_lshlrev_b64 v[18:19], 2, v[4:5]
	v_ashrrev_i32_e32 v11, 31, v10
	v_ashrrev_i32_e32 v13, 31, v12
	v_lshl_add_u64 v[2:3], s[8:9], 0, v[18:19]
	v_lshlrev_b64 v[20:21], 2, v[10:11]
	v_lshlrev_b64 v[22:23], 2, v[12:13]
	v_lshl_add_u64 v[6:7], s[8:9], 0, v[20:21]
	global_load_dword v5, v[2:3], off
	global_load_dword v11, v[6:7], off
	v_lshl_add_u64 v[2:3], s[8:9], 0, v[22:23]
	global_load_dword v13, v[2:3], off
	v_min_f32_e32 v2, v9, v27
	v_min_f32_e32 v6, v25, v29
	v_max_f32_e32 v43, v2, v6
	v_min_f32_e32 v44, v2, v6
	v_and_b32_e32 v2, 0xffffff00, v34
	v_and_b32_e32 v51, 0xffffff00, v33
	v_max_f32_e32 v37, v9, v27
	v_max_f32_e32 v3, v25, v29
	v_sub_f32_e32 v2, v2, v51
	v_min_f32_e32 v9, v24, v28
	v_min_f32_e32 v25, v26, v30
	v_max_f32_e32 v41, v37, v3
	v_min_f32_e32 v42, v37, v3
	v_and_b32_e32 v3, 0xffffff00, v35
	v_mul_f32_e32 v2, 0x3fb8aa3b, v2
	v_max_f32_e32 v47, v9, v25
	v_min_f32_e32 v48, v9, v25
	v_exp_f32_e32 v25, v2
	v_sub_f32_e32 v2, v3, v51
	v_and_b32_e32 v6, 0xffffff00, v36
	v_mul_f32_e32 v2, 0x3fb8aa3b, v2
	v_max_f32_e32 v7, v24, v28
	v_max_f32_e32 v24, v26, v30
	v_max_f32_e32 v38, v17, v32
	v_exp_f32_e32 v26, v2
	v_sub_f32_e32 v2, v6, v51
	v_max_f32_e32 v45, v7, v24
	v_min_f32_e32 v46, v7, v24
	v_and_b32_e32 v7, 0xffffff00, v38
	v_mul_f32_e32 v2, 0x3fb8aa3b, v2
	v_min_f32_e32 v17, v17, v32
	v_exp_f32_e32 v27, v2
	v_sub_f32_e32 v2, v7, v51
	v_max_f32_e32 v39, v31, v8
	v_min_f32_e32 v40, v31, v8
	v_and_b32_e32 v8, 0xffffff00, v17
	v_mul_f32_e32 v2, 0x3fb8aa3b, v2
	v_exp_f32_e32 v28, v2
	v_sub_f32_e32 v2, v8, v51
	v_and_b32_e32 v9, 0xffffff00, v39
	v_mul_f32_e32 v2, 0x3fb8aa3b, v2
	v_exp_f32_e32 v29, v2
	v_sub_f32_e32 v2, v9, v51
	v_and_b32_e32 v31, 0xffffff00, v40
	v_mul_f32_e32 v2, 0x3fb8aa3b, v2
	v_exp_f32_e32 v30, v2
	v_sub_f32_e32 v2, v31, v51
	v_and_b32_e32 v32, 0xffffff00, v41
	v_mul_f32_e32 v2, 0x3fb8aa3b, v2
	v_exp_f32_e32 v31, v2
	v_sub_f32_e32 v2, v32, v51
	v_and_b32_e32 v34, 0xffffff00, v42
	v_mul_f32_e32 v2, 0x3fb8aa3b, v2
	v_exp_f32_e32 v6, v2
	v_sub_f32_e32 v2, v34, v51
	v_and_b32_e32 v35, 0xffffff00, v43
	v_mul_f32_e32 v2, 0x3fb8aa3b, v2
	v_exp_f32_e32 v7, v2
	v_sub_f32_e32 v2, v35, v51
	v_mul_f32_e32 v2, 0x3fb8aa3b, v2
	v_exp_f32_e32 v8, v2
	v_lshl_or_b32 v2, s18, 8, v128
	v_ashrrev_i32_e32 v3, 31, v2
	s_lshl_b64 s[4:5], s[16:17], 18
	v_lshl_add_u64 v[32:33], v[2:3], 4, s[4:5]
	s_mov_b32 s4, 0x7fc000
	v_sub_f32_e32 v24, v51, v51
	v_mul_f32_e32 v24, 0x3fb8aa3b, v24
	v_exp_f32_e32 v24, v24
	s_waitcnt vmcnt(0)
; #define RT_PK(q_) (ex[q_] | (int)((__float_as_uint(usc[ex[q_]]) >> 23) << 14))
;     __device__ __forceinline__ void fused(f32x4 (&acc)[2][2][4][2], const Unit& u, int wr, int wc, int fr, int fq, PG8_LAS unsigned char* lds, int wid, int lane) const {
;     ...
;             for (int q = 0; q < 16; ++q) { sc[q] = __builtin_amdgcn_exp2f((sc[q] - smax) * 1.4426950408889634f); }
; #pragma unroll
;             for (int q = 0; q < 16; ++q) sum += sc[q];
;             const float rs = 1.0f / sum;
;             asm volatile("s_waitcnt lgkmcnt(0)" ::: "memory");
;             int ex[16];
; #pragma unroll
;             for (int q = 0; q < 16; ++q) { const unsigned cid = __float_as_uint(best[q]) & 255u; ex[q] = idxl[cid >> 4] * 128 + idxl[16 + (cid & 15u)]; }
;             const size_t o = ((size_t)u.pn * 16384 + (size_t)(u.pm * BM + row)) * 16;
;             typedef int i32x4 __attribute__((ext_vector_type(4)));
; #pragma unroll
;             for (int i = 0; i < 4; ++i) {
;     ...
;                 *(i32x4*)(eidx + o + 4 * i) = (i32x4){RT_PK(4 * i), RT_PK(4 * i + 1), RT_PK(4 * i + 2), RT_PK(4 * i + 3)};
;                 *(f32x4*)(egate + o + 4 * i) = (f32x4){sc[4 * i] * rs * vsc[ex[4 * i]], sc[4 * i + 1] * rs * vsc[ex[4 * i + 1]], sc[4 * i + 2] * rs * vsc[ex[4 * i + 2]], sc[4 * i + 3] * rs * vsc[ex[4 * i + 3]]};
	v_lshrrev_b32_e32 v1, 9, v1
	v_and_or_b32 v2, v1, s4, v0
	v_and_b32_e32 v36, 0xffffff00, v44
	v_and_b32_e32 v37, 0xffffff00, v45
	v_and_b32_e32 v49, 0xffffff00, v46
	v_and_b32_e32 v50, 0xffffff00, v47
	v_and_b32_e32 v52, 0xffffff00, v48
	v_lshrrev_b32_e32 v0, 9, v5
	v_and_or_b32 v3, v0, s4, v4
	v_lshrrev_b32_e32 v0, 9, v11
	v_and_or_b32 v4, v0, s4, v10
	v_lshrrev_b32_e32 v0, 9, v13
	v_and_or_b32 v5, v0, s4, v12
	v_lshlrev_b64 v[12:13], 2, v[32:33]
	v_lshl_add_u64 v[0:1], s[12:13], 0, v[12:13]
	global_store_dwordx4 v[0:1], v[2:5], off
	v_lshl_add_u64 v[10:11], s[6:7], 0, v[20:21]
	v_lshrrev_b32_e32 v32, 2, v40
	v_lshl_add_u64 v[2:3], s[6:7], 0, v[14:15]
	v_lshl_add_u64 v[4:5], s[6:7], 0, v[18:19]
	v_lshl_add_u64 v[14:15], s[6:7], 0, v[22:23]
	global_load_dword v18, v[2:3], off
	global_load_dword v19, v[4:5], off
	global_load_dword v20, v[10:11], off
	global_load_dword v21, v[14:15], off
	v_add_f32_e32 v10, 0, v24
	v_add_f32_e32 v10, v25, v10
	v_add_f32_e32 v10, v26, v10
	v_add_f32_e32 v10, v27, v10
	v_sub_f32_e32 v2, v36, v51
	v_add_f32_e32 v10, v28, v10
	v_mul_f32_e32 v2, 0x3fb8aa3b, v2
	v_add_f32_e32 v10, v29, v10
	v_exp_f32_e32 v9, v2
	v_sub_f32_e32 v2, v37, v51
	v_add_f32_e32 v10, v30, v10
	v_mul_f32_e32 v2, 0x3fb8aa3b, v2
	v_sub_f32_e32 v3, v49, v51
	v_add_f32_e32 v10, v31, v10
	v_exp_f32_e32 v2, v2
	v_mul_f32_e32 v3, 0x3fb8aa3b, v3
	v_sub_f32_e32 v4, v50, v51
	v_add_f32_e32 v10, v6, v10
	v_exp_f32_e32 v3, v3
	v_mul_f32_e32 v4, 0x3fb8aa3b, v4
	v_sub_f32_e32 v5, v52, v51
	v_add_f32_e32 v10, v7, v10
	v_exp_f32_e32 v4, v4
	v_mul_f32_e32 v5, 0x3fb8aa3b, v5
	v_add_f32_e32 v10, v8, v10
	v_exp_f32_e32 v5, v5
	v_add_f32_e32 v10, v9, v10
	v_add_f32_e32 v10, v2, v10
	v_lshrrev_b32_e32 v11, 2, v38
	v_lshrrev_b32_e32 v15, 2, v17
	v_add_f32_e32 v10, v3, v10
	v_and_b32_e32 v11, 60, v11
	v_and_b32_e32 v14, 15, v38
	v_and_b32_e32 v15, 60, v15
	v_and_b32_e32 v17, 15, v17
	v_lshrrev_b32_e32 v22, 2, v39
	v_and_b32_e32 v23, 15, v39
	v_and_b32_e32 v33, 15, v40
	v_add_f32_e32 v10, v4, v10
	v_add_u32_e32 v11, v16, v11
	v_lshl_add_u32 v14, v14, 2, v16
	v_add_u32_e32 v15, v16, v15
	v_lshl_add_u32 v17, v17, 2, v16
	v_and_b32_e32 v22, 60, v22
	v_lshl_add_u32 v23, v23, 2, v16
	v_and_b32_e32 v32, 60, v32
	v_lshl_add_u32 v33, v33, 2, v16
	v_add_f32_e32 v10, v5, v10
	v_add_u32_e32 v22, v16, v22
	v_add_u32_e32 v32, v16, v32
	ds_read_b32 v11, v11
	ds_read_b32 v14, v14 offset:64
	ds_read_b32 v15, v15
	ds_read_b32 v17, v17 offset:64
	ds_read_b32 v34, v22
	ds_read_b32 v23, v23 offset:64
	ds_read_b32 v35, v32
	ds_read_b32 v33, v33 offset:64
	s_waitcnt lgkmcnt(6)
	v_lshl_add_u32 v14, v11, 7, v14
	v_div_scale_f32 v11, s[16:17], v10, v10, 1.0
	v_rcp_f32_e32 v36, v11
	s_waitcnt lgkmcnt(4)
	v_lshl_add_u32 v22, v15, 7, v17
	s_waitcnt lgkmcnt(2)
	v_lshl_add_u32 v32, v34, 7, v23
	s_waitcnt lgkmcnt(0)
	v_lshl_add_u32 v34, v35, 7, v33
	v_fma_f32 v15, -v11, v36, 1.0
	v_fmac_f32_e32 v36, v15, v36
	v_div_scale_f32 v15, vcc, 1.0, v10, 1.0
	v_mul_f32_e32 v17, v15, v36
	v_fma_f32 v23, -v11, v17, v15
	v_fmac_f32_e32 v17, v23, v36
	v_fma_f32 v11, -v11, v17, v15
	v_div_fmas_f32 v11, v11, v36, v17
	v_div_fixup_f32 v10, v11, v10, 1.0
	v_pk_mul_f32 v[24:25], v[24:25], v[10:11] op_sel_hi:[1,0]
	v_pk_mul_f32 v[26:27], v[26:27], v[10:11] op_sel_hi:[1,0]
	v_ashrrev_i32_e32 v15, 31, v14
	v_ashrrev_i32_e32 v33, 31, v32
	v_lshl_add_u64 v[12:13], s[10:11], 0, v[12:13]
	v_ashrrev_i32_e32 v23, 31, v22
	v_lshlrev_b64 v[36:37], 2, v[32:33]
	v_lshl_add_u64 v[38:39], s[8:9], 0, v[36:37]
	v_ashrrev_i32_e32 v35, 31, v34
	s_waitcnt vmcnt(2)
	v_pk_mul_f32 v[18:19], v[24:25], v[18:19]
	v_lshlrev_b64 v[24:25], 2, v[14:15]
	s_waitcnt vmcnt(0)
	v_pk_mul_f32 v[20:21], v[26:27], v[20:21]
	global_store_dwordx4 v[12:13], v[18:21], off
	v_lshlrev_b64 v[26:27], 2, v[22:23]
	s_nop 0
	v_lshl_add_u64 v[18:19], s[8:9], 0, v[24:25]
	v_lshl_add_u64 v[20:21], s[8:9], 0, v[26:27]
	global_load_dword v11, v[18:19], off
	global_load_dword v15, v[20:21], off
	global_load_dword v17, v[38:39], off
	v_lshlrev_b64 v[38:39], 2, v[34:35]
	v_lshl_add_u64 v[18:19], s[8:9], 0, v[38:39]
	global_load_dword v21, v[18:19], off
	s_waitcnt vmcnt(3)
	v_lshrrev_b32_e32 v11, 9, v11
	v_and_or_b32 v18, v11, s4, v14
	s_waitcnt vmcnt(2)
	v_lshrrev_b32_e32 v11, 9, v15
	v_and_or_b32 v19, v11, s4, v22
	s_waitcnt vmcnt(1)
	v_lshrrev_b32_e32 v11, 9, v17
	v_and_or_b32 v20, v11, s4, v32
	s_waitcnt vmcnt(0)
	v_lshrrev_b32_e32 v11, 9, v21
	v_and_or_b32 v21, v11, s4, v34
	global_store_dwordx4 v[0:1], v[18:21], off offset:16
	v_lshl_add_u64 v[14:15], s[6:7], 0, v[24:25]
	v_lshl_add_u64 v[22:23], s[6:7], 0, v[38:39]
	v_lshl_add_u64 v[18:19], s[6:7], 0, v[26:27]
	v_lshl_add_u64 v[20:21], s[6:7], 0, v[36:37]
	global_load_dword v24, v[14:15], off
	global_load_dword v26, v[20:21], off
	global_load_dword v27, v[22:23], off
	global_load_dword v25, v[18:19], off
	v_lshrrev_b32_e32 v11, 2, v41
	v_lshrrev_b32_e32 v15, 2, v42
	v_lshrrev_b32_e32 v18, 2, v43
	v_lshrrev_b32_e32 v20, 2, v44
	v_and_b32_e32 v11, 60, v11
	v_and_b32_e32 v14, 15, v41
	v_and_b32_e32 v15, 60, v15
	v_and_b32_e32 v17, 15, v42
	v_and_b32_e32 v18, 60, v18
	v_and_b32_e32 v19, 15, v43
	v_and_b32_e32 v20, 60, v20
	v_and_b32_e32 v21, 15, v44
	v_add_u32_e32 v11, v16, v11
	v_lshl_add_u32 v14, v14, 2, v16
	v_add_u32_e32 v15, v16, v15
	v_lshl_add_u32 v17, v17, 2, v16
	v_add_u32_e32 v18, v16, v18
	v_lshl_add_u32 v19, v19, 2, v16
	v_add_u32_e32 v20, v16, v20
	v_lshl_add_u32 v21, v21, 2, v16
	ds_read_b32 v11, v11
	ds_read_b32 v14, v14 offset:64
	ds_read_b32 v15, v15
	ds_read_b32 v17, v17 offset:64
	ds_read_b32 v18, v18
	ds_read_b32 v19, v19 offset:64
	ds_read_b32 v20, v20
	ds_read_b32 v21, v21 offset:64
	s_waitcnt lgkmcnt(6)
; #define RT_PK(q_) (ex[q_] | (int)((__float_as_uint(usc[ex[q_]]) >> 23) << 14))
;     __device__ __forceinline__ void fused(f32x4 (&acc)[2][2][4][2], const Unit& u, int wr, int wc, int fr, int fq, PG8_LAS unsigned char* lds, int wid, int lane) const {
;     ...
;             for (int q = 0; q < 16; ++q) { const unsigned cid = __float_as_uint(best[q]) & 255u; ex[q] = idxl[cid >> 4] * 128 + idxl[16 + (cid & 15u)]; }
;             const size_t o = ((size_t)u.pn * 16384 + (size_t)(u.pm * BM + row)) * 16;
;             typedef int i32x4 __attribute__((ext_vector_type(4)));
; #pragma unroll
;             for (int i = 0; i < 4; ++i) {
;     ...
;                 *(i32x4*)(eidx + o + 4 * i) = (i32x4){RT_PK(4 * i), RT_PK(4 * i + 1), RT_PK(4 * i + 2), RT_PK(4 * i + 3)};
;                 *(f32x4*)(egate + o + 4 * i) = (f32x4){sc[4 * i] * rs * vsc[ex[4 * i]], sc[4 * i + 1] * rs * vsc[ex[4 * i + 1]], sc[4 * i + 2] * rs * vsc[ex[4 * i + 2]], sc[4 * i + 3] * rs * vsc[ex[4 * i + 3]]};
	v_lshl_add_u32 v14, v11, 7, v14
	s_waitcnt lgkmcnt(4)
	v_lshl_add_u32 v22, v15, 7, v17
	s_waitcnt lgkmcnt(2)
	v_lshl_add_u32 v32, v18, 7, v19
	v_pk_mul_f32 v[18:19], v[28:29], v[10:11] op_sel_hi:[1,0]
	s_waitcnt lgkmcnt(0)
	v_lshl_add_u32 v34, v20, 7, v21
	v_pk_mul_f32 v[20:21], v[30:31], v[10:11] op_sel_hi:[1,0]
	v_ashrrev_i32_e32 v15, 31, v14
	v_ashrrev_i32_e32 v33, 31, v32
	v_ashrrev_i32_e32 v23, 31, v22
	v_lshlrev_b64 v[28:29], 2, v[32:33]
	v_lshl_add_u64 v[30:31], s[8:9], 0, v[28:29]
	v_ashrrev_i32_e32 v35, 31, v34
	s_waitcnt vmcnt(1)
	v_pk_mul_f32 v[20:21], v[20:21], v[26:27]
	s_waitcnt vmcnt(0)
	v_pk_mul_f32 v[18:19], v[18:19], v[24:25]
	v_lshlrev_b64 v[24:25], 2, v[14:15]
	global_store_dwordx4 v[12:13], v[18:21], off offset:16
	v_lshlrev_b64 v[26:27], 2, v[22:23]
	s_nop 0
	v_lshl_add_u64 v[18:19], s[8:9], 0, v[24:25]
	v_lshl_add_u64 v[20:21], s[8:9], 0, v[26:27]
	global_load_dword v11, v[18:19], off
	global_load_dword v15, v[20:21], off
	global_load_dword v17, v[30:31], off
	v_lshlrev_b64 v[30:31], 2, v[34:35]
	v_lshl_add_u64 v[18:19], s[8:9], 0, v[30:31]
	global_load_dword v21, v[18:19], off
	s_waitcnt vmcnt(3)
	v_lshrrev_b32_e32 v11, 9, v11
	v_and_or_b32 v18, v11, s4, v14
	s_waitcnt vmcnt(2)
	v_lshrrev_b32_e32 v11, 9, v15
	v_and_or_b32 v19, v11, s4, v22
	s_waitcnt vmcnt(1)
	v_lshrrev_b32_e32 v11, 9, v17
	v_and_or_b32 v20, v11, s4, v32
	s_waitcnt vmcnt(0)
	v_lshrrev_b32_e32 v11, 9, v21
	v_and_or_b32 v21, v11, s4, v34
	global_store_dwordx4 v[0:1], v[18:21], off offset:32
	v_lshl_add_u64 v[14:15], s[6:7], 0, v[24:25]
	v_lshl_add_u64 v[22:23], s[6:7], 0, v[30:31]
	v_lshl_add_u64 v[18:19], s[6:7], 0, v[26:27]
	v_lshl_add_u64 v[20:21], s[6:7], 0, v[28:29]
	global_load_dword v24, v[14:15], off
	global_load_dword v26, v[20:21], off
	global_load_dword v27, v[22:23], off
	global_load_dword v25, v[18:19], off
	v_lshrrev_b32_e32 v11, 2, v45
	v_lshrrev_b32_e32 v15, 2, v46
	v_lshrrev_b32_e32 v18, 2, v47
	v_lshrrev_b32_e32 v20, 2, v48
	v_and_b32_e32 v11, 60, v11
	v_and_b32_e32 v14, 15, v45
	v_and_b32_e32 v15, 60, v15
	v_and_b32_e32 v17, 15, v46
	v_and_b32_e32 v18, 60, v18
	v_and_b32_e32 v19, 15, v47
	v_and_b32_e32 v20, 60, v20
	v_add_u32_e32 v11, v16, v11
	v_lshl_add_u32 v14, v14, 2, v16
	v_add_u32_e32 v15, v16, v15
	v_lshl_add_u32 v17, v17, 2, v16
	v_add_u32_e32 v18, v16, v18
	v_lshl_add_u32 v19, v19, 2, v16
	v_add_u32_e32 v20, v16, v20
	v_and_b32_e32 v21, 15, v48
	v_lshl_add_u32 v16, v21, 2, v16
	ds_read_b32 v11, v11
	ds_read_b32 v14, v14 offset:64
	ds_read_b32 v15, v15
	ds_read_b32 v17, v17 offset:64
	ds_read_b32 v18, v18
	ds_read_b32 v19, v19 offset:64
	ds_read_b32 v20, v20
	ds_read_b32 v21, v16 offset:64
	s_waitcnt lgkmcnt(6)
	v_lshl_add_u32 v14, v11, 7, v14
	s_waitcnt lgkmcnt(4)
	v_lshl_add_u32 v16, v15, 7, v17
	s_waitcnt lgkmcnt(2)
	v_lshl_add_u32 v18, v18, 7, v19
	v_pk_mul_f32 v[6:7], v[6:7], v[10:11] op_sel_hi:[1,0]
	v_pk_mul_f32 v[8:9], v[8:9], v[10:11] op_sel_hi:[1,0]
	v_ashrrev_i32_e32 v15, 31, v14
	v_ashrrev_i32_e32 v19, 31, v18
	s_waitcnt lgkmcnt(0)
	v_lshl_add_u32 v20, v20, 7, v21
	v_lshlrev_b64 v[22:23], 2, v[14:15]
	v_ashrrev_i32_e32 v17, 31, v16
	v_ashrrev_i32_e32 v21, 31, v20
	s_waitcnt vmcnt(1)
	v_pk_mul_f32 v[8:9], v[8:9], v[26:27]
	s_waitcnt vmcnt(0)
	v_pk_mul_f32 v[6:7], v[6:7], v[24:25]
	v_lshlrev_b64 v[26:27], 2, v[18:19]
	global_store_dwordx4 v[12:13], v[6:9], off offset:32
	v_lshlrev_b64 v[24:25], 2, v[16:17]
	v_lshl_add_u64 v[28:29], s[8:9], 0, v[26:27]
	v_lshl_add_u64 v[6:7], s[8:9], 0, v[22:23]
	v_lshl_add_u64 v[8:9], s[8:9], 0, v[24:25]
	global_load_dword v11, v[6:7], off
	global_load_dword v15, v[8:9], off
	global_load_dword v17, v[28:29], off
	v_lshlrev_b64 v[28:29], 2, v[20:21]
	v_lshl_add_u64 v[6:7], s[8:9], 0, v[28:29]
	global_load_dword v9, v[6:7], off
	s_waitcnt vmcnt(3)
	v_lshrrev_b32_e32 v6, 9, v11
	s_waitcnt vmcnt(2)
	v_lshrrev_b32_e32 v7, 9, v15
	s_waitcnt vmcnt(1)
	v_lshrrev_b32_e32 v8, 9, v17
	v_and_or_b32 v6, v6, s4, v14
	v_and_or_b32 v7, v7, s4, v16
	s_waitcnt vmcnt(0)
	v_lshrrev_b32_e32 v9, 9, v9
	v_and_or_b32 v8, v8, s4, v18
	v_and_or_b32 v9, v9, s4, v20
	global_store_dwordx4 v[0:1], v[6:9], off offset:48
	v_lshl_add_u64 v[0:1], s[6:7], 0, v[22:23]
	v_lshl_add_u64 v[14:15], s[6:7], 0, v[28:29]
	v_lshl_add_u64 v[6:7], s[6:7], 0, v[24:25]
	v_lshl_add_u64 v[8:9], s[6:7], 0, v[26:27]
	global_load_dword v16, v[0:1], off
	global_load_dword v18, v[8:9], off
	global_load_dword v19, v[14:15], off
	global_load_dword v17, v[6:7], off
	v_pk_mul_f32 v[0:1], v[2:3], v[10:11] op_sel_hi:[1,0]
	v_pk_mul_f32 v[2:3], v[4:5], v[10:11] op_sel_hi:[1,0]
	s_waitcnt vmcnt(0)
	v_pk_mul_f32 v[0:1], v[0:1], v[16:17]
	v_pk_mul_f32 v[2:3], v[2:3], v[18:19]
	global_store_dwordx4 v[12:13], v[0:3], off offset:48

; #define PG8_LAS __attribute__((address_space(3)))
;     __device__ __forceinline__ void fused(f32x4 (&acc)[2][2][4][2], const Unit& u, int wr, int wc, int fr, int fq, PG8_LAS unsigned char* lds, int wid, int lane) const {
;     ...
;                 for (int m = 0; m < 4; ++m)
; #pragma unroll
;                     for (int n = 0; n < 2; ++n) {
;                         const int rw = ai * HALF + wr * 64 + m * 16 + fr, g = 8 * wc + 4 * n + fq, col = 32 * wc + 16 * n + 4 * fq;
;                         const f32x4 v = acc[ai][bj][m][n]; f32x4 p;
; #pragma unroll
;                         for (int e = 0; e < 4; ++e) p[e] = __uint_as_float((__float_as_uint(v[e]) & ~127u) | (unsigned)(col + e));
;                         *(PG8_LAS f32x4*)(tile + rw * 128 + ((g ^ fr) << 2)) = p;
.LBB0_598:
	v_and_b32_e32 v128, 63, v137
	v_bfe_u32 v137, v137, 4, 2
	v_lshlrev_b32_e32 v129, 2, v137
	s_lshl_b32 s4, s45, 15
	v_lshl_or_b32 v129, s48, 5, v129
	s_movk_i32 s98, 0xff80
	v_or_b32_e32 v224, 1, v129
	v_or_b32_e32 v225, 2, v129
	v_or_b32_e32 v226, 3, v129
	v_or_b32_e32 v227, 17, v129
	v_or_b32_e32 v228, 18, v129
	v_or_b32_e32 v229, 19, v129
	s_add_i32 s14, s4, 0
	s_movk_i32 s4, 0xff80
	v_and_or_b32 v132, v124, s4, v129
	v_and_or_b32 v133, v125, s98, v224
	s_lshl_b32 s5, s48, 3
	v_and_or_b32 v134, v126, s98, v225
	v_lshlrev_b32_e32 v140, 9, v138
	v_and_or_b32 v135, v127, s98, v226
	v_bitop3_b32 v124, s5, v138, v137 bitop3:0x36
	v_add_u32_e32 v141, s14, v140
	v_lshlrev_b32_e32 v126, 4, v124
	v_add_u32_e32 v125, v141, v126
	v_or_b32_e32 v124, 16, v129
	s_barrier
	ds_write_b128 v125, v[132:135]
	v_and_or_b32 v132, v120, s4, v124
	v_and_or_b32 v133, v121, s98, v227
	v_or_b32_e32 v139, s5, v137
	v_and_or_b32 v134, v122, s98, v228
	v_and_or_b32 v135, v123, s98, v229
	v_bitop3_b32 v120, v139, v138, 4 bitop3:0x36
	v_lshlrev_b32_e32 v121, 4, v120
	v_add_u32_e32 v120, v141, v121
	v_and_or_b32 v96, v96, s4, v124
	v_and_or_b32 v97, v97, s98, v227
	v_and_or_b32 v98, v98, s98, v228
	v_and_or_b32 v99, v99, s98, v229
	ds_write_b128 v120, v[96:99] offset:24576
	v_and_or_b32 v96, v92, s4, v129
	v_and_or_b32 v100, v100, s4, v129
	v_and_or_b32 v101, v101, s98, v224
	v_and_or_b32 v102, v102, s98, v225
	v_and_or_b32 v103, v103, s98, v226
	s_add_i32 s5, s14, 0x10000
	v_and_or_b32 v97, v93, s98, v224
	ds_write_b128 v125, v[100:103] offset:24576
	v_add_u32_e32 v100, s5, v140
	v_and_or_b32 v98, v94, s98, v225
	v_and_or_b32 v94, v88, s4, v124
	v_and_or_b32 v99, v95, s98, v226
	v_add_u32_e32 v92, v100, v126
	v_and_or_b32 v95, v89, s98, v227
	ds_write_b128 v92, v[96:99]
	v_and_or_b32 v96, v90, s98, v228
	v_and_or_b32 v97, v91, s98, v229
	v_add_u32_e32 v88, v100, v121
	ds_write_b128 v88, v[94:97]
	v_and_or_b32 v94, v84, s4, v129
	s_add_i32 s5, s14, 0x12000
	v_and_or_b32 v95, v85, s98, v224
	v_add_u32_e32 v89, s5, v140
	v_and_or_b32 v96, v86, s98, v225
	v_and_or_b32 v97, v87, s98, v226
	v_add_u32_e32 v84, v89, v126
	ds_write_b128 v84, v[94:97]
	v_and_or_b32 v94, v80, s4, v124
	v_and_or_b32 v95, v81, s98, v227
	v_and_or_b32 v96, v82, s98, v228
	s_add_i32 s5, s14, 0x14000
	v_and_or_b32 v97, v83, s98, v229
	v_add_u32_e32 v80, s5, v140
	v_and_or_b32 v72, v72, s4, v124
	v_and_or_b32 v73, v73, s98, v227
	v_and_or_b32 v74, v74, s98, v228
	v_and_or_b32 v75, v75, s98, v229
	v_add_u32_e32 v86, v80, v121
	s_add_i32 s14, s14, 0x16000
	s_and_b32 s3, s49, 0xc0
	ds_write_b128 v86, v[72:75]
	v_add_u32_e32 v72, s14, v140
	v_or_b32_e32 v128, s3, v128
	s_lshl_b32 s3, s45, 4
	v_and_or_b32 v64, v64, s4, v124
	v_and_or_b32 v65, v65, s98, v227
	v_and_or_b32 v66, v66, s98, v228
	v_and_or_b32 v67, v67, s98, v229
	v_add_u32_e32 v91, v72, v121
	ds_write_b128 v91, v[64:67]
	v_or_b32_e32 v64, s3, v138
	v_lshl_add_u32 v130, v128, 9, 0
	v_lshlrev_b32_e32 v64, 4, v64
	v_add_u32_e32 v93, v130, v64
	v_bitop3_b32 v64, s3, v138, 1 bitop3:0x36
	v_and_or_b32 v116, v116, s4, v129
	v_and_or_b32 v117, v117, s98, v224
	v_and_or_b32 v118, v118, s98, v225
	v_and_or_b32 v119, v119, s98, v226
	v_and_or_b32 v112, v112, s4, v124
	v_and_or_b32 v113, v113, s98, v227
	v_and_or_b32 v114, v114, s98, v228
	v_and_or_b32 v115, v115, s98, v229
	v_and_or_b32 v108, v108, s4, v129
	v_and_or_b32 v109, v109, s98, v224
	v_and_or_b32 v110, v110, s98, v225
	v_and_or_b32 v111, v111, s98, v226
	v_and_or_b32 v104, v104, s4, v124
	v_and_or_b32 v105, v105, s98, v227
	v_and_or_b32 v106, v106, s98, v228
	v_and_or_b32 v107, v107, s98, v229
	v_add_u32_e32 v82, v89, v121
	v_and_or_b32 v76, v76, s4, v129
	v_and_or_b32 v77, v77, s98, v224
	v_and_or_b32 v78, v78, s98, v225
	v_and_or_b32 v79, v79, s98, v226
	v_add_u32_e32 v85, v80, v126
	v_and_or_b32 v68, v68, s4, v129
	v_and_or_b32 v69, v69, s98, v224
	v_and_or_b32 v70, v70, s98, v225
	v_and_or_b32 v71, v71, s98, v226
	v_add_u32_e32 v90, v72, v126
	v_lshlrev_b32_e32 v64, 4, v64
	ds_write_b128 v120, v[132:135]
	ds_write_b128 v125, v[116:119] offset:8192
	ds_write_b128 v120, v[112:115] offset:8192
	ds_write_b128 v125, v[108:111] offset:16384
	ds_write_b128 v120, v[104:107] offset:16384
	ds_write_b128 v82, v[94:97]
	ds_write_b128 v85, v[76:79]
	ds_write_b128 v90, v[68:71]
	v_add_u32_e32 v89, v130, v64
	v_bitop3_b32 v64, s3, v138, 2 bitop3:0x36
	v_bitop3_b32 v68, s3, v138, 3 bitop3:0x36
	s_waitcnt lgkmcnt(0)
	s_barrier
; #define PG8_LAS __attribute__((address_space(3)))
; #define CE(a, b) do { const float hi_ = fmaxf(a, b), lo_ = fminf(a, b); a = hi_; b = lo_; } while (0)
; __device__ __forceinline__ void sort16_desc(float (&v)[16]) {
;     CE(v[0], v[1]); CE(v[2], v[3]); CE(v[0], v[2]); CE(v[1], v[3]);
;     CE(v[1], v[2]); CE(v[4], v[5]); CE(v[6], v[7]); CE(v[4], v[6]);
;     CE(v[5], v[7]); CE(v[5], v[6]); CE(v[0], v[4]); CE(v[2], v[6]);
;     CE(v[2], v[4]); CE(v[1], v[5]); CE(v[3], v[7]); CE(v[3], v[5]);
;     CE(v[1], v[2]); CE(v[3], v[4]); CE(v[5], v[6]); CE(v[8], v[9]);
;     CE(v[10], v[11]); CE(v[8], v[10]); CE(v[9], v[11]); CE(v[9], v[10]);
;     CE(v[12], v[13]); CE(v[14], v[15]); CE(v[12], v[14]); CE(v[13], v[15]);
;     CE(v[13], v[14]); CE(v[8], v[12]); CE(v[10], v[14]); CE(v[10], v[12]);
;     CE(v[9], v[13]); CE(v[11], v[15]); CE(v[11], v[13]); CE(v[9], v[10]);
;     CE(v[11], v[12]); CE(v[13], v[14]); CE(v[0], v[8]); CE(v[4], v[12]);
;     CE(v[4], v[8]); CE(v[2], v[10]); CE(v[6], v[14]); CE(v[6], v[10]);
;     CE(v[2], v[4]); CE(v[6], v[8]); CE(v[10], v[12]); CE(v[1], v[9]);
;     CE(v[5], v[13]); CE(v[5], v[9]); CE(v[3], v[11]); CE(v[7], v[15]);
;     CE(v[7], v[11]); CE(v[3], v[5]); CE(v[7], v[9]); CE(v[11], v[13]);
;     CE(v[1], v[2]); CE(v[3], v[4]); CE(v[5], v[6]); CE(v[7], v[8]);
;     CE(v[9], v[10]); CE(v[11], v[12]); CE(v[13], v[14]);
; }
;     __device__ __forceinline__ void fused(f32x4 (&acc)[2][2][4][2], const Unit& u, int wr, int wc, int fr, int fq, PG8_LAS unsigned char* lds, int wid, int lane) const {
;     ...
;             for (int grp = 0; grp < 4; ++grp) {
;                 float nw[16];
; #pragma unroll
;                 for (int i = 0; i < 4; ++i) { const int g = half * 16 + grp * 4 + i; const f32x4 v = *(const PG8_LAS f32x4*)(tile + row * 128 + ((g ^ (row & 15)) << 2));
;                     nw[4 * i] = v[0]; nw[4 * i + 1] = v[1]; nw[4 * i + 2] = v[2]; nw[4 * i + 3] = v[3]; }
;                 sort16_desc(nw);
;                 if (grp == 0) {
; #pragma unroll
;                     for (int q = 0; q < 16; ++q) run[q] = nw[q];
;                 } else merge_top16(run, nw);
	v_lshlrev_b32_e32 v64, 4, v64
	v_lshlrev_b32_e32 v68, 4, v68
	v_add_u32_e32 v81, v130, v64
	ds_read_b128 v[64:67], v93
	v_add_u32_e32 v80, v130, v68
	ds_read_b128 v[68:71], v89
	v_mul_i32_i24_e32 v131, 0xfffffe40, v128
	s_andn2_b64 vcc, exec, s[20:21]
	s_waitcnt lgkmcnt(0)
	v_min_f32_e32 v74, v64, v65
	v_max_f32_e32 v72, v64, v65
	v_min_f32_e32 v77, v66, v67
	v_max_f32_e32 v73, v66, v67
	v_min_f32_e32 v87, v68, v69
	v_max_f32_e32 v79, v68, v69
	v_min_f32_e32 v96, v70, v71
	v_max_f32_e32 v83, v70, v71
	ds_read_b128 v[64:67], v81
	ds_read_b128 v[68:71], v80
	s_waitcnt lgkmcnt(0)
	v_min_f32_e32 v99, v64, v65
	v_min_f32_e32 v100, v66, v67
	v_min_f32_e32 v102, v68, v69
	v_min_f32_e32 v103, v70, v71
	v_max_f32_e32 v64, v64, v65
	v_max_f32_e32 v65, v66, v67
	v_max_f32_e32 v68, v68, v69
	v_max_f32_e32 v69, v70, v71
	v_min_f32_e32 v78, v74, v77
	v_min_f32_e32 v97, v87, v96
	v_min_f32_e32 v101, v99, v100
	v_max_f32_e32 v74, v74, v77
	v_min_f32_e32 v75, v72, v73
	v_max_f32_e32 v77, v87, v96
	v_min_f32_e32 v87, v79, v83
	v_max_f32_e32 v99, v99, v100
	v_min_f32_e32 v66, v64, v65
	v_max_f32_e32 v100, v102, v103
	v_min_f32_e32 v70, v68, v69
	v_min_f32_e32 v104, v102, v103
	v_max_f32_e32 v76, v74, v75
	v_max_f32_e32 v94, v77, v87
	v_max_f32_e32 v67, v99, v66
	v_max_f32_e32 v71, v100, v70
	v_min_f32_e32 v98, v78, v97
	v_min_f32_e32 v105, v101, v104
	v_max_f32_e32 v78, v78, v97
	v_min_f32_e32 v95, v76, v94
	v_min_f32_e32 v74, v74, v75
	v_min_f32_e32 v75, v77, v87
	v_max_f32_e32 v97, v101, v104
	v_min_f32_e32 v101, v67, v71
	v_min_f32_e32 v66, v99, v66
	v_min_f32_e32 v70, v100, v70
	v_max_f32_e32 v96, v78, v95
	v_max_f32_e32 v77, v74, v75
	v_max_f32_e32 v72, v72, v73
	v_max_f32_e32 v73, v79, v83
	v_max_f32_e32 v99, v66, v70
	v_max_f32_e32 v64, v64, v65
	v_max_f32_e32 v65, v68, v69
	v_min_f32_e32 v78, v78, v95
	v_min_f32_e32 v74, v74, v75
	v_min_f32_e32 v95, v97, v101
	v_min_f32_e32 v66, v66, v70
	v_min_f32_e32 v79, v72, v73
	v_min_f32_e32 v68, v64, v65
	v_max_f32_e32 v75, v78, v74
	v_max_f32_e32 v70, v95, v66
	v_min_f32_e32 v74, v78, v74
	v_min_f32_e32 v66, v95, v66
	v_min_f32_e32 v83, v77, v79
	v_max_f32_e32 v102, v97, v101
	v_min_f32_e32 v69, v99, v68
	v_min_f32_e32 v78, v74, v66
	v_max_f32_e32 v66, v74, v66
	v_max_f32_e32 v74, v76, v94
	v_max_f32_e32 v76, v77, v79
	v_max_f32_e32 v67, v67, v71
	v_max_f32_e32 v68, v99, v68
	v_max_f32_e32 v87, v96, v83
	v_max_f32_e32 v100, v102, v69
	v_min_f32_e32 v77, v74, v76
	v_min_f32_e32 v71, v67, v68
	v_min_f32_e32 v83, v96, v83
	v_min_f32_e32 v69, v102, v69
	v_max_f32_e32 v72, v72, v73
	v_max_f32_e32 v73, v64, v65
	v_min_f32_e32 v79, v77, v71
	v_min_f32_e32 v96, v83, v69
	v_max_f32_e32 v69, v83, v69
	v_min_f32_e32 v64, v72, v73
	v_min_f32_e32 v94, v66, v79
	v_max_f32_e32 v66, v66, v79
	v_min_f32_e32 v65, v69, v64
	v_max_f32_e32 v74, v74, v76
	v_max_f32_e32 v67, v67, v68
	v_min_f32_e32 v79, v66, v65
	v_max_f32_e32 v107, v66, v65
	v_max_f32_e32 v65, v77, v71
	v_max_f32_e32 v64, v69, v64
	v_max_f32_e32 v106, v98, v105
	v_min_f32_e32 v103, v87, v100
	v_min_f32_e32 v97, v75, v70
	v_max_f32_e32 v70, v75, v70
	v_min_f32_e32 v68, v74, v67
	v_min_f32_e32 v77, v65, v64
	v_max_f32_e32 v111, v65, v64
	v_bitop3_b32 v64, s3, v138, 4 bitop3:0x36
	v_max_f32_e32 v99, v106, v103
	v_min_f32_e32 v75, v70, v68
	v_lshlrev_b32_e32 v64, 4, v64
	v_min_f32_e32 v76, v99, v75
	v_max_f32_e32 v75, v99, v75
	v_add_u32_e32 v99, v130, v64
	v_bitop3_b32 v64, s3, v138, 5 bitop3:0x36
	v_max_f32_e32 v83, v87, v100
	v_max_f32_e32 v68, v70, v68
	v_lshlrev_b32_e32 v64, 4, v64
	v_min_f32_e32 v102, v94, v96
	v_max_f32_e32 v94, v94, v96
	v_min_f32_e32 v100, v83, v68
	v_max_f32_e32 v109, v83, v68
	v_add_u32_e32 v96, v130, v64
	v_bitop3_b32 v64, s3, v138, 6 bitop3:0x36
	v_bitop3_b32 v68, s3, v138, 7 bitop3:0x36
	v_lshlrev_b32_e32 v64, 4, v64
	v_lshlrev_b32_e32 v68, 4, v68
	v_max_f32_e32 v74, v74, v67
	v_add_u32_e32 v87, v130, v64
	ds_read_b128 v[64:67], v99
	v_add_u32_e32 v83, v130, v68
	ds_read_b128 v[68:71], v96
	v_min_f32_e32 v98, v98, v105
	v_min_f32_e32 v104, v106, v103
	s_waitcnt lgkmcnt(0)
	v_min_f32_e32 v114, v64, v65
	v_max_f32_e32 v105, v64, v65
	v_min_f32_e32 v117, v66, v67
	v_max_f32_e32 v113, v66, v67
	v_min_f32_e32 v122, v68, v69
	v_max_f32_e32 v119, v68, v69
	v_min_f32_e32 v127, v70, v71
	v_max_f32_e32 v121, v70, v71
	ds_read_b128 v[64:67], v87
	ds_read_b128 v[68:71], v83
	s_waitcnt lgkmcnt(0)
; #define PG8_LAS __attribute__((address_space(3)))
; #define CE(a, b) do { const float hi_ = fmaxf(a, b), lo_ = fminf(a, b); a = hi_; b = lo_; } while (0)
; __device__ __forceinline__ void merge_top16(float (&v)[16], const float (&nw)[16]) {
;     v[0] = fmaxf(v[0], nw[15]); v[1] = fmaxf(v[1], nw[14]); v[2] = fmaxf(v[2], nw[13]); v[3] = fmaxf(v[3], nw[12]); v[4] = fmaxf(v[4], nw[11]); v[5] = fmaxf(v[5], nw[10]); v[6] = fmaxf(v[6], nw[9]); v[7] = fmaxf(v[7], nw[8]); v[8] = fmaxf(v[8], nw[7]); v[9] = fmaxf(v[9], nw[6]); v[10] = fmaxf(v[10], nw[5]); v[11] = fmaxf(v[11], nw[4]); v[12] = fmaxf(v[12], nw[3]); v[13] = fmaxf(v[13], nw[2]); v[14] = fmaxf(v[14], nw[1]); v[15] = fmaxf(v[15], nw[0]);
;     CE(v[0], v[8]); CE(v[1], v[9]); CE(v[2], v[10]); CE(v[3], v[11]);
;     CE(v[4], v[12]); CE(v[5], v[13]); CE(v[6], v[14]); CE(v[7], v[15]);
;     CE(v[0], v[4]); CE(v[1], v[5]); CE(v[2], v[6]); CE(v[3], v[7]);
;     CE(v[8], v[12]); CE(v[9], v[13]); CE(v[10], v[14]); CE(v[11], v[15]);
;     CE(v[0], v[2]); CE(v[1], v[3]); CE(v[4], v[6]); CE(v[5], v[7]);
;     CE(v[8], v[10]); CE(v[9], v[11]); CE(v[12], v[14]); CE(v[13], v[15]);
;     CE(v[0], v[1]); CE(v[2], v[3]); CE(v[4], v[5]); CE(v[6], v[7]);
;     CE(v[8], v[9]); CE(v[10], v[11]); CE(v[12], v[13]); CE(v[14], v[15]);
; }
;     __device__ __forceinline__ void fused(f32x4 (&acc)[2][2][4][2], const Unit& u, int wr, int wc, int fr, int fq, PG8_LAS unsigned char* lds, int wid, int lane) const {
;     ...
;             for (int grp = 0; grp < 4; ++grp) {
;                 float nw[16];
; #pragma unroll
;                 for (int i = 0; i < 4; ++i) { const int g = half * 16 + grp * 4 + i; const f32x4 v = *(const PG8_LAS f32x4*)(tile + row * 128 + ((g ^ (row & 15)) << 2));
;                     nw[4 * i] = v[0]; nw[4 * i + 1] = v[1]; nw[4 * i + 2] = v[2]; nw[4 * i + 3] = v[3]; }
;                 sort16_desc(nw);
;                 if (grp == 0) {
; #pragma unroll
;                     for (int q = 0; q < 16; ++q) run[q] = nw[q];
;                 } else merge_top16(run, nw);
	v_min_f32_e32 v134, v64, v65
	v_min_f32_e32 v135, v66, v67
	v_min_f32_e32 v139, v68, v69
	v_min_f32_e32 v140, v70, v71
	v_max_f32_e32 v64, v64, v65
	v_max_f32_e32 v65, v66, v67
	v_max_f32_e32 v68, v68, v69
	v_max_f32_e32 v69, v70, v71
	v_min_f32_e32 v118, v114, v117
	v_min_f32_e32 v132, v122, v127
	v_min_f32_e32 v137, v134, v135
	v_max_f32_e32 v114, v114, v117
	v_min_f32_e32 v115, v105, v113
	v_max_f32_e32 v117, v122, v127
	v_min_f32_e32 v122, v119, v121
	v_max_f32_e32 v134, v134, v135
	v_min_f32_e32 v66, v64, v65
	v_max_f32_e32 v135, v139, v140
	v_min_f32_e32 v70, v68, v69
	v_min_f32_e32 v141, v139, v140
	v_max_f32_e32 v116, v114, v115
	v_max_f32_e32 v123, v117, v122
	v_max_f32_e32 v67, v134, v66
	v_max_f32_e32 v71, v135, v70
	v_min_f32_e32 v133, v118, v132
	v_min_f32_e32 v142, v137, v141
	v_max_f32_e32 v118, v118, v132
	v_min_f32_e32 v126, v116, v123
	v_min_f32_e32 v114, v114, v115
	v_min_f32_e32 v115, v117, v122
	v_max_f32_e32 v132, v137, v141
	v_min_f32_e32 v137, v67, v71
	v_min_f32_e32 v66, v134, v66
	v_min_f32_e32 v70, v135, v70
	v_max_f32_e32 v127, v118, v126
	v_max_f32_e32 v117, v114, v115
	v_max_f32_e32 v105, v105, v113
	v_max_f32_e32 v113, v119, v121
	v_max_f32_e32 v134, v66, v70
	v_max_f32_e32 v64, v64, v65
	v_max_f32_e32 v65, v68, v69
	v_min_f32_e32 v118, v118, v126
	v_min_f32_e32 v114, v114, v115
	v_min_f32_e32 v126, v132, v137
	v_min_f32_e32 v66, v66, v70
	v_min_f32_e32 v119, v105, v113
	v_min_f32_e32 v68, v64, v65
	v_max_f32_e32 v115, v118, v114
	v_max_f32_e32 v70, v126, v66
	v_min_f32_e32 v114, v118, v114
	v_min_f32_e32 v66, v126, v66
	v_min_f32_e32 v121, v117, v119
	v_max_f32_e32 v139, v132, v137
	v_min_f32_e32 v69, v134, v68
	v_min_f32_e32 v118, v114, v66
	v_max_f32_e32 v66, v114, v66
	v_max_f32_e32 v114, v116, v123
	v_max_f32_e32 v116, v117, v119
	v_max_f32_e32 v67, v67, v71
	v_max_f32_e32 v68, v134, v68
	v_max_f32_e32 v122, v127, v121
	v_max_f32_e32 v135, v139, v69
	v_min_f32_e32 v117, v114, v116
	v_min_f32_e32 v71, v67, v68
	v_min_f32_e32 v121, v127, v121
	v_min_f32_e32 v69, v139, v69
	v_max_f32_e32 v114, v114, v116
	v_max_f32_e32 v67, v67, v68
	v_max_f32_e32 v105, v105, v113
	v_max_f32_e32 v64, v64, v65
	v_max_f32_e32 v143, v133, v142
	v_min_f32_e32 v140, v122, v135
	v_min_f32_e32 v132, v115, v70
	v_min_f32_e32 v119, v117, v71
	v_min_f32_e32 v127, v121, v69
	v_max_f32_e32 v70, v115, v70
	v_min_f32_e32 v68, v114, v67
	v_max_f32_e32 v69, v121, v69
	v_min_f32_e32 v65, v105, v64
	v_min_f32_e32 v141, v143, v140
	v_min_f32_e32 v123, v66, v119
	v_max_f32_e32 v140, v143, v140
	v_min_f32_e32 v115, v70, v68
	v_max_f32_e32 v66, v66, v119
	v_min_f32_e32 v113, v69, v65
	v_max_f32_e32 v122, v122, v135
	v_max_f32_e32 v68, v70, v68
	v_max_f32_e32 v71, v117, v71
	v_max_f32_e32 v65, v69, v65
	v_min_f32_e32 v101, v104, v97
	v_max_f32_e32 v97, v104, v97
	v_min_f32_e32 v137, v141, v132
	v_max_f32_e32 v132, v141, v132
	v_min_f32_e32 v134, v123, v127
	v_min_f32_e32 v116, v140, v115
	v_max_f32_e32 v123, v123, v127
	v_max_f32_e32 v115, v140, v115
	v_min_f32_e32 v119, v66, v113
	v_min_f32_e32 v70, v122, v68
	v_max_f32_e32 v66, v66, v113
	v_max_f32_e32 v68, v122, v68
	v_min_f32_e32 v69, v71, v65
	v_max_f32_e32 v67, v114, v67
	v_max_f32_e32 v65, v71, v65
	v_min_f32_e32 v95, v101, v78
	v_min_f32_e32 v104, v97, v102
	v_min_f32_e32 v103, v76, v94
	v_min_f32_e32 v106, v75, v79
	v_min_f32_e32 v108, v100, v107
	v_min_f32_e32 v110, v109, v77
	v_min_f32_e32 v112, v74, v111
	v_min_f32_e32 v126, v137, v118
	v_min_f32_e32 v139, v132, v134
	v_min_f32_e32 v127, v116, v123
	v_min_f32_e32 v121, v115, v119
	v_min_f32_e32 v113, v70, v66
	v_min_f32_e32 v117, v68, v69
	v_min_f32_e32 v71, v67, v65
	v_min_f32_e32 v114, v133, v142
	v_max3_f32 v72, v72, v73, v114
	v_max3_f32 v73, v74, v111, v126
	v_max3_f32 v74, v112, v137, v118
	v_max3_f32 v77, v109, v77, v139
	v_max3_f32 v109, v110, v132, v134
	v_max3_f32 v100, v100, v107, v127
	v_max3_f32 v107, v108, v116, v123
	v_max3_f32 v75, v75, v79, v121
	v_max3_f32 v79, v106, v115, v119
	v_max3_f32 v76, v76, v94, v113
	v_max3_f32 v66, v103, v70, v66
	v_max3_f32 v70, v97, v102, v117
	v_max3_f32 v68, v104, v68, v69
	v_max3_f32 v69, v101, v78, v71
	v_max3_f32 v65, v95, v67, v65
	v_max3_f32 v64, v98, v105, v64
	v_max_f32_e32 v67, v72, v79
	v_min_f32_e32 v71, v72, v79
	v_max_f32_e32 v72, v73, v76
	v_min_f32_e32 v73, v73, v76
	v_max_f32_e32 v76, v74, v66
	v_min_f32_e32 v66, v74, v66
	v_max_f32_e32 v74, v77, v70
	v_min_f32_e32 v70, v77, v70
	v_max_f32_e32 v77, v109, v68
	v_min_f32_e32 v68, v109, v68
	v_max_f32_e32 v78, v100, v69
	v_min_f32_e32 v69, v100, v69
	v_max_f32_e32 v79, v107, v65
	v_min_f32_e32 v65, v107, v65
	v_max_f32_e32 v94, v75, v64
	v_min_f32_e32 v64, v75, v64
	v_max_f32_e32 v75, v67, v77
	v_min_f32_e32 v67, v67, v77
	v_max_f32_e32 v77, v72, v78
	v_min_f32_e32 v72, v72, v78
	v_max_f32_e32 v78, v76, v79
	v_min_f32_e32 v76, v76, v79
	v_max_f32_e32 v79, v74, v94
	v_min_f32_e32 v74, v74, v94
	v_max_f32_e32 v94, v71, v68
	v_min_f32_e32 v68, v71, v68
	v_max_f32_e32 v71, v73, v69
	v_min_f32_e32 v69, v73, v69
	v_max_f32_e32 v73, v66, v65
	v_min_f32_e32 v65, v66, v65
	v_max_f32_e32 v66, v70, v64
	v_min_f32_e32 v64, v70, v64
	v_max_f32_e32 v106, v69, v64
	v_min_f32_e32 v107, v69, v64
	v_bitop3_b32 v64, s3, v138, 8 bitop3:0x36
	v_lshlrev_b32_e32 v64, 4, v64
	v_add_u32_e32 v102, v130, v64
	v_bitop3_b32 v64, s3, v138, 9 bitop3:0x36
	v_lshlrev_b32_e32 v64, 4, v64
	v_max_f32_e32 v104, v68, v65
	v_min_f32_e32 v105, v68, v65
	v_add_u32_e32 v101, v130, v64
	v_bitop3_b32 v64, s3, v138, 10 bitop3:0x36
	v_bitop3_b32 v68, s3, v138, 11 bitop3:0x36
	v_lshlrev_b32_e32 v64, 4, v64
	v_lshlrev_b32_e32 v68, 4, v68
	v_max_f32_e32 v97, v75, v78
	v_min_f32_e32 v75, v75, v78
	v_max_f32_e32 v78, v77, v79
	v_min_f32_e32 v77, v77, v79
	v_max_f32_e32 v79, v67, v76
	v_min_f32_e32 v76, v67, v76
	v_max_f32_e32 v98, v72, v74
	v_min_f32_e32 v72, v72, v74
	v_max_f32_e32 v74, v94, v73
	v_min_f32_e32 v73, v94, v73
	v_max_f32_e32 v100, v71, v66
	v_min_f32_e32 v103, v71, v66
	v_add_u32_e32 v95, v130, v64
	ds_read_b128 v[64:67], v102
	v_add_u32_e32 v94, v130, v68
	ds_read_b128 v[68:71], v101
	v_min_f32_e32 v108, v97, v78
	v_min_f32_e32 v109, v75, v77
	s_waitcnt lgkmcnt(0)
; #define PG8_LAS __attribute__((address_space(3)))
; #define CE(a, b) do { const float hi_ = fmaxf(a, b), lo_ = fminf(a, b); a = hi_; b = lo_; } while (0)
; __device__ __forceinline__ void merge_top16(float (&v)[16], const float (&nw)[16]) {
;     v[0] = fmaxf(v[0], nw[15]); v[1] = fmaxf(v[1], nw[14]); v[2] = fmaxf(v[2], nw[13]); v[3] = fmaxf(v[3], nw[12]); v[4] = fmaxf(v[4], nw[11]); v[5] = fmaxf(v[5], nw[10]); v[6] = fmaxf(v[6], nw[9]); v[7] = fmaxf(v[7], nw[8]); v[8] = fmaxf(v[8], nw[7]); v[9] = fmaxf(v[9], nw[6]); v[10] = fmaxf(v[10], nw[5]); v[11] = fmaxf(v[11], nw[4]); v[12] = fmaxf(v[12], nw[3]); v[13] = fmaxf(v[13], nw[2]); v[14] = fmaxf(v[14], nw[1]); v[15] = fmaxf(v[15], nw[0]);
;     CE(v[0], v[8]); CE(v[1], v[9]); CE(v[2], v[10]); CE(v[3], v[11]);
;     CE(v[4], v[12]); CE(v[5], v[13]); CE(v[6], v[14]); CE(v[7], v[15]);
;     CE(v[0], v[4]); CE(v[1], v[5]); CE(v[2], v[6]); CE(v[3], v[7]);
;     CE(v[8], v[12]); CE(v[9], v[13]); CE(v[10], v[14]); CE(v[11], v[15]);
;     CE(v[0], v[2]); CE(v[1], v[3]); CE(v[4], v[6]); CE(v[5], v[7]);
;     CE(v[8], v[10]); CE(v[9], v[11]); CE(v[12], v[14]); CE(v[13], v[15]);
;     CE(v[0], v[1]); CE(v[2], v[3]); CE(v[4], v[5]); CE(v[6], v[7]);
;     CE(v[8], v[9]); CE(v[10], v[11]); CE(v[12], v[13]); CE(v[14], v[15]);
; }
;     __device__ __forceinline__ void fused(f32x4 (&acc)[2][2][4][2], const Unit& u, int wr, int wc, int fr, int fq, PG8_LAS unsigned char* lds, int wid, int lane) const {
;     ...
;             for (int grp = 0; grp < 4; ++grp) {
;                 float nw[16];
; #pragma unroll
;                 for (int i = 0; i < 4; ++i) { const int g = half * 16 + grp * 4 + i; const f32x4 v = *(const PG8_LAS f32x4*)(tile + row * 128 + ((g ^ (row & 15)) << 2));
;                     nw[4 * i] = v[0]; nw[4 * i + 1] = v[1]; nw[4 * i + 2] = v[2]; nw[4 * i + 3] = v[3]; }
;                 sort16_desc(nw);
;                 if (grp == 0) {
; #pragma unroll
;                     for (int q = 0; q < 16; ++q) run[q] = nw[q];
;                 } else merge_top16(run, nw);
	v_min_f32_e32 v118, v64, v65
	v_max_f32_e32 v116, v64, v65
	v_min_f32_e32 v122, v66, v67
	v_max_f32_e32 v117, v66, v67
	v_min_f32_e32 v132, v68, v69
	v_max_f32_e32 v126, v68, v69
	v_min_f32_e32 v135, v70, v71
	v_max_f32_e32 v127, v70, v71
	ds_read_b128 v[64:67], v95
	ds_read_b128 v[68:71], v94
	s_waitcnt lgkmcnt(0)
	v_min_f32_e32 v140, v64, v65
	v_min_f32_e32 v141, v66, v67
	v_min_f32_e32 v143, v68, v69
	v_min_f32_e32 v144, v70, v71
	v_max_f32_e32 v64, v64, v65
	v_max_f32_e32 v65, v66, v67
	v_max_f32_e32 v68, v68, v69
	v_max_f32_e32 v69, v70, v71
	v_min_f32_e32 v123, v118, v122
	v_min_f32_e32 v137, v132, v135
	v_min_f32_e32 v142, v140, v141
	v_max_f32_e32 v118, v118, v122
	v_min_f32_e32 v119, v116, v117
	v_max_f32_e32 v122, v132, v135
	v_min_f32_e32 v132, v126, v127
	v_max_f32_e32 v140, v140, v141
	v_min_f32_e32 v66, v64, v65
	v_max_f32_e32 v141, v143, v144
	v_min_f32_e32 v70, v68, v69
	v_min_f32_e32 v145, v143, v144
	v_max_f32_e32 v121, v118, v119
	v_max_f32_e32 v133, v122, v132
	v_max_f32_e32 v67, v140, v66
	v_max_f32_e32 v71, v141, v70
	v_min_f32_e32 v139, v123, v137
	v_min_f32_e32 v146, v142, v145
	v_max_f32_e32 v123, v123, v137
	v_min_f32_e32 v134, v121, v133
	v_min_f32_e32 v118, v118, v119
	v_min_f32_e32 v119, v122, v132
	v_max_f32_e32 v137, v142, v145
	v_min_f32_e32 v142, v67, v71
	v_min_f32_e32 v66, v140, v66
	v_min_f32_e32 v70, v141, v70
	v_max_f32_e32 v135, v123, v134
	v_max_f32_e32 v122, v118, v119
	v_max_f32_e32 v116, v116, v117
	v_max_f32_e32 v117, v126, v127
	v_max_f32_e32 v140, v66, v70
	v_max_f32_e32 v64, v64, v65
	v_max_f32_e32 v65, v68, v69
	v_min_f32_e32 v123, v123, v134
	v_min_f32_e32 v118, v118, v119
	v_min_f32_e32 v134, v137, v142
	v_min_f32_e32 v66, v66, v70
	v_min_f32_e32 v126, v116, v117
	v_min_f32_e32 v68, v64, v65
	v_max_f32_e32 v119, v123, v118
	v_max_f32_e32 v70, v134, v66
	v_min_f32_e32 v118, v123, v118
	v_min_f32_e32 v66, v134, v66
	v_min_f32_e32 v127, v122, v126
	v_max_f32_e32 v143, v137, v142
	v_min_f32_e32 v69, v140, v68
	v_min_f32_e32 v123, v118, v66
	v_max_f32_e32 v66, v118, v66
	v_max_f32_e32 v118, v121, v133
	v_max_f32_e32 v121, v122, v126
	v_max_f32_e32 v67, v67, v71
	v_max_f32_e32 v68, v140, v68
	v_max_f32_e32 v132, v135, v127
	v_max_f32_e32 v141, v143, v69
	v_min_f32_e32 v122, v118, v121
	v_min_f32_e32 v71, v67, v68
	v_max_f32_e32 v147, v139, v146
	v_min_f32_e32 v144, v132, v141
	v_min_f32_e32 v126, v122, v71
	v_min_f32_e32 v127, v135, v127
	v_min_f32_e32 v69, v143, v69
	v_min_f32_e32 v145, v147, v144
	v_min_f32_e32 v137, v119, v70
	v_min_f32_e32 v133, v66, v126
	v_min_f32_e32 v135, v127, v69
	v_max_f32_e32 v118, v118, v121
	v_max_f32_e32 v67, v67, v68
	v_max_f32_e32 v116, v116, v117
	v_max_f32_e32 v64, v64, v65
	v_min_f32_e32 v142, v145, v137
	v_max_f32_e32 v137, v145, v137
	v_min_f32_e32 v140, v133, v135
	v_max_f32_e32 v70, v119, v70
	v_min_f32_e32 v68, v118, v67
	v_max_f32_e32 v69, v127, v69
	v_min_f32_e32 v65, v116, v64
	v_min_f32_e32 v134, v142, v123
	v_max_f32_e32 v123, v142, v123
	v_min_f32_e32 v142, v137, v140
	v_max_f32_e32 v137, v137, v140
	v_max_f32_e32 v140, v147, v144
	v_min_f32_e32 v119, v70, v68
	v_max_f32_e32 v66, v66, v126
	v_min_f32_e32 v117, v69, v65
	v_min_f32_e32 v121, v140, v119
	v_max_f32_e32 v119, v140, v119
	v_min_f32_e32 v126, v66, v117
	v_min_f32_e32 v127, v119, v126
	v_max_f32_e32 v119, v119, v126
	v_max_f32_e32 v126, v132, v141
	v_max_f32_e32 v68, v70, v68
	v_min_f32_e32 v70, v126, v68
	v_max_f32_e32 v66, v66, v117
	v_min_f32_e32 v117, v70, v66
	v_max_f32_e32 v66, v70, v66
	v_max_f32_e32 v70, v122, v71
	v_max_f32_e32 v65, v69, v65
	v_max_f32_e32 v133, v133, v135
	v_max_f32_e32 v68, v126, v68
	v_min_f32_e32 v69, v70, v65
	v_max_f32_e32 v67, v118, v67
	v_max_f32_e32 v65, v70, v65
	v_min_f32_e32 v110, v79, v98
	v_min_f32_e32 v111, v76, v72
	v_min_f32_e32 v112, v74, v100
	v_min_f32_e32 v113, v73, v103
	v_min_f32_e32 v114, v104, v106
	v_min_f32_e32 v115, v105, v107
	v_min_f32_e32 v135, v121, v133
	v_max_f32_e32 v121, v121, v133
	v_min_f32_e32 v71, v68, v69
	v_max_f32_e32 v68, v68, v69
	v_min_f32_e32 v69, v67, v65
	v_max_f32_e32 v65, v67, v65
	v_min_f32_e32 v67, v139, v146
	v_max3_f32 v67, v97, v78, v67
	v_max_f32_e32 v70, v108, v134
	v_max3_f32 v75, v75, v77, v123
	v_max_f32_e32 v77, v109, v142
	v_max3_f32 v78, v79, v98, v137
	v_max_f32_e32 v79, v110, v135
	v_max3_f32 v72, v76, v72, v121
	v_max_f32_e32 v76, v111, v127
	v_max3_f32 v74, v74, v100, v119
	v_max_f32_e32 v97, v112, v117
	v_max3_f32 v66, v73, v103, v66
	v_max_f32_e32 v71, v113, v71
	v_max3_f32 v68, v104, v106, v68
	v_max_f32_e32 v69, v114, v69
	v_max3_f32 v65, v105, v107, v65
	v_max3_f32 v64, v115, v116, v64
	v_max_f32_e32 v73, v67, v74
	v_min_f32_e32 v67, v67, v74
	v_max_f32_e32 v74, v70, v97
	v_min_f32_e32 v70, v70, v97
	v_max_f32_e32 v97, v75, v66
	v_min_f32_e32 v66, v75, v66
	v_max_f32_e32 v75, v77, v71
	v_min_f32_e32 v71, v77, v71
	v_max_f32_e32 v77, v78, v68
	v_min_f32_e32 v68, v78, v68
	v_max_f32_e32 v78, v79, v69
	v_min_f32_e32 v69, v79, v69
	v_max_f32_e32 v79, v72, v65
	v_min_f32_e32 v65, v72, v65
	v_max_f32_e32 v72, v76, v64
	v_min_f32_e32 v64, v76, v64
	v_max_f32_e32 v76, v73, v77
	v_min_f32_e32 v73, v73, v77
	v_max_f32_e32 v77, v74, v78
	v_min_f32_e32 v74, v74, v78
	v_max_f32_e32 v78, v97, v79
	v_min_f32_e32 v79, v97, v79
	v_max_f32_e32 v97, v75, v72
	v_min_f32_e32 v72, v75, v72
	v_max_f32_e32 v75, v67, v68
	v_min_f32_e32 v67, v67, v68
	v_max_f32_e32 v68, v70, v69
	v_min_f32_e32 v69, v70, v69
	v_max_f32_e32 v70, v66, v65
	v_min_f32_e32 v65, v66, v65
	v_max_f32_e32 v66, v71, v64
	v_min_f32_e32 v64, v71, v64
	v_max_f32_e32 v110, v69, v64
	v_min_f32_e32 v111, v69, v64
	v_bitop3_b32 v64, s3, v138, 12 bitop3:0x36
	v_lshlrev_b32_e32 v64, 4, v64
	v_add_u32_e32 v104, v130, v64
	v_bitop3_b32 v64, s3, v138, 13 bitop3:0x36
	v_lshlrev_b32_e32 v64, 4, v64
	v_max_f32_e32 v106, v68, v66
	v_min_f32_e32 v107, v68, v66
	v_add_u32_e32 v103, v130, v64
	v_bitop3_b32 v64, s3, v138, 14 bitop3:0x36
	v_bitop3_b32 v68, s3, v138, 15 bitop3:0x36
	v_lshlrev_b32_e32 v64, 4, v64
	v_lshlrev_b32_e32 v68, 4, v68
	v_max_f32_e32 v105, v76, v78
	v_min_f32_e32 v76, v76, v78
	v_max_f32_e32 v78, v77, v97
	v_min_f32_e32 v77, v77, v97
	v_max_f32_e32 v97, v73, v79
	v_min_f32_e32 v73, v73, v79
	v_max_f32_e32 v79, v74, v72
	v_min_f32_e32 v72, v74, v72
	v_max_f32_e32 v74, v75, v70
	v_min_f32_e32 v75, v75, v70
	v_max_f32_e32 v108, v67, v65
	v_min_f32_e32 v109, v67, v65
	v_add_u32_e32 v100, v130, v64
	ds_read_b128 v[64:67], v104
	v_add_u32_e32 v98, v130, v68
	ds_read_b128 v[68:71], v103
	v_min_f32_e32 v112, v105, v78
	v_min_f32_e32 v113, v76, v77
	s_waitcnt lgkmcnt(0)
; #define PG8_LAS __attribute__((address_space(3)))
; #define CE(a, b) do { const float hi_ = fmaxf(a, b), lo_ = fminf(a, b); a = hi_; b = lo_; } while (0)
; __device__ __forceinline__ void merge_top16(float (&v)[16], const float (&nw)[16]) {
;     v[0] = fmaxf(v[0], nw[15]); v[1] = fmaxf(v[1], nw[14]); v[2] = fmaxf(v[2], nw[13]); v[3] = fmaxf(v[3], nw[12]); v[4] = fmaxf(v[4], nw[11]); v[5] = fmaxf(v[5], nw[10]); v[6] = fmaxf(v[6], nw[9]); v[7] = fmaxf(v[7], nw[8]); v[8] = fmaxf(v[8], nw[7]); v[9] = fmaxf(v[9], nw[6]); v[10] = fmaxf(v[10], nw[5]); v[11] = fmaxf(v[11], nw[4]); v[12] = fmaxf(v[12], nw[3]); v[13] = fmaxf(v[13], nw[2]); v[14] = fmaxf(v[14], nw[1]); v[15] = fmaxf(v[15], nw[0]);
;     CE(v[0], v[8]); CE(v[1], v[9]); CE(v[2], v[10]); CE(v[3], v[11]);
;     CE(v[4], v[12]); CE(v[5], v[13]); CE(v[6], v[14]); CE(v[7], v[15]);
;     CE(v[0], v[4]); CE(v[1], v[5]); CE(v[2], v[6]); CE(v[3], v[7]);
;     CE(v[8], v[12]); CE(v[9], v[13]); CE(v[10], v[14]); CE(v[11], v[15]);
;     CE(v[0], v[2]); CE(v[1], v[3]); CE(v[4], v[6]); CE(v[5], v[7]);
;     CE(v[8], v[10]); CE(v[9], v[11]); CE(v[12], v[14]); CE(v[13], v[15]);
;     CE(v[0], v[1]); CE(v[2], v[3]); CE(v[4], v[5]); CE(v[6], v[7]);
;     CE(v[8], v[9]); CE(v[10], v[11]); CE(v[12], v[13]); CE(v[14], v[15]);
; }
;     __device__ __forceinline__ void fused(f32x4 (&acc)[2][2][4][2], const Unit& u, int wr, int wc, int fr, int fq, PG8_LAS unsigned char* lds, int wid, int lane) const {
;     ...
;             for (int grp = 0; grp < 4; ++grp) {
;                 float nw[16];
; #pragma unroll
;                 for (int i = 0; i < 4; ++i) { const int g = half * 16 + grp * 4 + i; const f32x4 v = *(const PG8_LAS f32x4*)(tile + row * 128 + ((g ^ (row & 15)) << 2));
;                     nw[4 * i] = v[0]; nw[4 * i + 1] = v[1]; nw[4 * i + 2] = v[2]; nw[4 * i + 3] = v[3]; }
;                 sort16_desc(nw);
;                 if (grp == 0) {
; #pragma unroll
;                     for (int q = 0; q < 16; ++q) run[q] = nw[q];
;                 } else merge_top16(run, nw);
;             }
;             RT_BAR();
;             if (half == 1) {
; #pragma unroll
;                 for (int i = 0; i < 4; ++i) *(PG8_LAS f32x4*)(tile + row * 16 + 4 * i) = (f32x4){run[4 * i], run[4 * i + 1], run[4 * i + 2], run[4 * i + 3]};
;             }
;             RT_BAR();
	v_min_f32_e32 v123, v64, v65
	v_max_f32_e32 v121, v64, v65
	v_min_f32_e32 v132, v66, v67
	v_max_f32_e32 v122, v66, v67
	v_min_f32_e32 v137, v68, v69
	v_max_f32_e32 v134, v68, v69
	v_min_f32_e32 v140, v70, v71
	v_max_f32_e32 v135, v70, v71
	ds_read_b128 v[64:67], v100
	ds_read_b128 v[68:71], v98
	s_waitcnt lgkmcnt(0)
	v_min_f32_e32 v143, v64, v65
	v_min_f32_e32 v144, v66, v67
	v_min_f32_e32 v146, v68, v69
	v_min_f32_e32 v147, v70, v71
	v_max_f32_e32 v64, v64, v65
	v_max_f32_e32 v65, v66, v67
	v_max_f32_e32 v68, v68, v69
	v_max_f32_e32 v69, v70, v71
	v_min_f32_e32 v133, v123, v132
	v_min_f32_e32 v141, v137, v140
	v_min_f32_e32 v145, v143, v144
	v_max_f32_e32 v123, v123, v132
	v_min_f32_e32 v126, v121, v122
	v_max_f32_e32 v132, v137, v140
	v_min_f32_e32 v137, v134, v135
	v_max_f32_e32 v143, v143, v144
	v_min_f32_e32 v66, v64, v65
	v_max_f32_e32 v144, v146, v147
	v_min_f32_e32 v70, v68, v69
	v_min_f32_e32 v148, v146, v147
	v_max_f32_e32 v127, v123, v126
	v_max_f32_e32 v138, v132, v137
	v_max_f32_e32 v67, v143, v66
	v_max_f32_e32 v71, v144, v70
	v_min_f32_e32 v142, v133, v141
	v_min_f32_e32 v149, v145, v148
	v_max_f32_e32 v133, v133, v141
	v_min_f32_e32 v139, v127, v138
	v_min_f32_e32 v123, v123, v126
	v_min_f32_e32 v126, v132, v137
	v_max_f32_e32 v141, v145, v148
	v_min_f32_e32 v145, v67, v71
	v_min_f32_e32 v66, v143, v66
	v_min_f32_e32 v70, v144, v70
	v_max_f32_e32 v140, v133, v139
	v_max_f32_e32 v132, v123, v126
	v_max_f32_e32 v121, v121, v122
	v_max_f32_e32 v122, v134, v135
	v_max_f32_e32 v143, v66, v70
	v_max_f32_e32 v64, v64, v65
	v_max_f32_e32 v65, v68, v69
	v_min_f32_e32 v133, v133, v139
	v_min_f32_e32 v123, v123, v126
	v_min_f32_e32 v139, v141, v145
	v_min_f32_e32 v66, v66, v70
	v_min_f32_e32 v134, v121, v122
	v_min_f32_e32 v68, v64, v65
	v_max_f32_e32 v126, v133, v123
	v_max_f32_e32 v70, v139, v66
	v_min_f32_e32 v123, v133, v123
	v_min_f32_e32 v66, v139, v66
	v_min_f32_e32 v135, v132, v134
	v_max_f32_e32 v146, v141, v145
	v_min_f32_e32 v69, v143, v68
	v_min_f32_e32 v133, v123, v66
	v_max_f32_e32 v66, v123, v66
	v_max_f32_e32 v123, v127, v138
	v_max_f32_e32 v127, v132, v134
	v_max_f32_e32 v67, v67, v71
	v_max_f32_e32 v68, v143, v68
	v_max_f32_e32 v137, v140, v135
	v_max_f32_e32 v144, v146, v69
	v_min_f32_e32 v132, v123, v127
	v_min_f32_e32 v71, v67, v68
	v_max_f32_e32 v150, v142, v149
	v_min_f32_e32 v147, v137, v144
	v_min_f32_e32 v134, v132, v71
	v_min_f32_e32 v135, v140, v135
	v_min_f32_e32 v69, v146, v69
	v_min_f32_e32 v148, v150, v147
	v_min_f32_e32 v141, v126, v70
	v_min_f32_e32 v138, v66, v134
	v_min_f32_e32 v140, v135, v69
	v_max_f32_e32 v123, v123, v127
	v_max_f32_e32 v67, v67, v68
	v_max_f32_e32 v121, v121, v122
	v_max_f32_e32 v64, v64, v65
	v_min_f32_e32 v145, v148, v141
	v_max_f32_e32 v141, v148, v141
	v_min_f32_e32 v143, v138, v140
	v_max_f32_e32 v70, v126, v70
	v_min_f32_e32 v68, v123, v67
	v_max_f32_e32 v69, v135, v69
	v_min_f32_e32 v65, v121, v64
	v_min_f32_e32 v139, v145, v133
	v_max_f32_e32 v133, v145, v133
	v_min_f32_e32 v145, v141, v143
	v_max_f32_e32 v141, v141, v143
	v_max_f32_e32 v143, v150, v147
	v_min_f32_e32 v126, v70, v68
	v_max_f32_e32 v66, v66, v134
	v_min_f32_e32 v122, v69, v65
	v_min_f32_e32 v127, v143, v126
	v_max_f32_e32 v126, v143, v126
	v_min_f32_e32 v134, v66, v122
	v_min_f32_e32 v135, v126, v134
	v_max_f32_e32 v126, v126, v134
	v_max_f32_e32 v134, v137, v144
	v_max_f32_e32 v68, v70, v68
	v_min_f32_e32 v70, v134, v68
	v_max_f32_e32 v66, v66, v122
	v_min_f32_e32 v122, v70, v66
	v_max_f32_e32 v66, v70, v66
	v_max_f32_e32 v70, v132, v71
	v_max_f32_e32 v65, v69, v65
	v_max_f32_e32 v138, v138, v140
	v_max_f32_e32 v68, v134, v68
	v_min_f32_e32 v69, v70, v65
	v_max_f32_e32 v67, v123, v67
	v_max_f32_e32 v65, v70, v65
	v_min_f32_e32 v114, v97, v79
	v_min_f32_e32 v115, v73, v72
	v_min_f32_e32 v116, v74, v106
	v_min_f32_e32 v117, v75, v107
	v_min_f32_e32 v118, v108, v110
	v_min_f32_e32 v119, v109, v111
	v_min_f32_e32 v140, v127, v138
	v_max_f32_e32 v127, v127, v138
	v_min_f32_e32 v71, v68, v69
	v_max_f32_e32 v68, v68, v69
	v_min_f32_e32 v69, v67, v65
	v_max_f32_e32 v65, v67, v65
	v_min_f32_e32 v67, v142, v149
	v_max3_f32 v67, v105, v78, v67
	v_max_f32_e32 v70, v112, v139
	v_max3_f32 v76, v76, v77, v133
	v_max_f32_e32 v77, v113, v145
	v_max3_f32 v78, v97, v79, v141
	v_max_f32_e32 v79, v114, v140
	v_max3_f32 v72, v73, v72, v127
	v_max_f32_e32 v73, v115, v135
	v_max3_f32 v74, v74, v106, v126
	v_max_f32_e32 v97, v116, v122
	v_max3_f32 v66, v75, v107, v66
	v_max_f32_e32 v71, v117, v71
	v_max3_f32 v68, v108, v110, v68
	v_max_f32_e32 v69, v118, v69
	v_max3_f32 v65, v109, v111, v65
	v_max3_f32 v64, v119, v121, v64
	v_max_f32_e32 v75, v67, v74
	v_min_f32_e32 v67, v67, v74
	v_max_f32_e32 v74, v70, v97
	v_min_f32_e32 v70, v70, v97
	v_max_f32_e32 v97, v76, v66
	v_min_f32_e32 v66, v76, v66
	v_max_f32_e32 v76, v77, v71
	v_min_f32_e32 v71, v77, v71
	v_max_f32_e32 v77, v78, v68
	v_min_f32_e32 v68, v78, v68
	v_max_f32_e32 v78, v79, v69
	v_min_f32_e32 v69, v79, v69
	v_max_f32_e32 v79, v72, v65
	v_min_f32_e32 v65, v72, v65
	v_max_f32_e32 v72, v73, v64
	v_min_f32_e32 v64, v73, v64
	v_max_f32_e32 v73, v75, v77
	v_min_f32_e32 v75, v75, v77
	v_max_f32_e32 v77, v74, v78
	v_min_f32_e32 v74, v74, v78
	v_max_f32_e32 v78, v97, v79
	v_min_f32_e32 v79, v97, v79
	v_max_f32_e32 v97, v76, v72
	v_min_f32_e32 v72, v76, v72
	v_max_f32_e32 v76, v67, v68
	v_min_f32_e32 v67, v67, v68
	v_max_f32_e32 v68, v70, v69
	v_min_f32_e32 v69, v70, v69
	v_max_f32_e32 v70, v66, v65
	v_min_f32_e32 v65, v66, v65
	v_max_f32_e32 v66, v71, v64
	v_min_f32_e32 v64, v71, v64
	v_max_f32_e32 v71, v73, v78
	v_min_f32_e32 v73, v73, v78
	v_max_f32_e32 v78, v77, v97
	v_min_f32_e32 v97, v77, v97
	s_waitcnt lgkmcnt(0)
	s_barrier
	v_max_f32_e32 v105, v75, v79
	v_min_f32_e32 v75, v75, v79
	v_max_f32_e32 v106, v74, v72
	v_min_f32_e32 v107, v74, v72
	v_max_f32_e32 v108, v76, v70
	v_min_f32_e32 v109, v76, v70
	v_max_f32_e32 v70, v68, v66
	v_min_f32_e32 v66, v68, v66
	v_max_f32_e32 v110, v67, v65
	v_min_f32_e32 v67, v67, v65
	v_max_f32_e32 v65, v69, v64
	v_min_f32_e32 v111, v69, v64
	v_max_f32_e32 v76, v71, v78
	v_min_f32_e32 v77, v71, v78
	v_max_f32_e32 v78, v73, v97
	v_min_f32_e32 v79, v73, v97
	v_cndmask_b32_e64 v97, 0, 1, s[20:21]
	v_max_f32_e32 v72, v105, v106
	v_min_f32_e32 v73, v105, v106
	v_max_f32_e32 v74, v75, v107
	v_min_f32_e32 v75, v75, v107
	v_max_f32_e32 v68, v108, v70
	v_min_f32_e32 v69, v108, v70
	v_max_f32_e32 v70, v109, v66
	v_min_f32_e32 v71, v109, v66
	v_max_f32_e32 v64, v110, v65
	v_min_f32_e32 v65, v110, v65
	v_max_f32_e32 v66, v67, v111
	v_min_f32_e32 v67, v67, v111
	v_cmp_ne_u32_e64 s[4:5], 1, v97
	v_add_u32_e32 v97, v130, v131
	s_cbranch_vccnz .LBB0_600
	ds_write_b128 v97, v[76:79]
	ds_write_b128 v97, v[72:75] offset:16
	ds_write_b128 v97, v[68:71] offset:32
	ds_write_b128 v97, v[64:67] offset:48
; #define PG8_LAS __attribute__((address_space(3)))
;     __device__ __forceinline__ void fused(f32x4 (&acc)[2][2][4][2], const Unit& u, int wr, int wc, int fr, int fq, PG8_LAS unsigned char* lds, int wid, int lane) const {
;     ...
;                 for (int m = 0; m < 4; ++m)
; #pragma unroll
;                     for (int n = 0; n < 2; ++n) {
;                         const int rw = ai * HALF + wr * 64 + m * 16 + fr, g = 8 * wc + 4 * n + fq, col = 32 * wc + 16 * n + 4 * fq;
;                         const f32x4 v = acc[ai][bj][m][n]; f32x4 p;
; #pragma unroll
;                         for (int e = 0; e < 4; ++e) p[e] = __uint_as_float((__float_as_uint(v[e]) & ~127u) | (unsigned)(col + e));
;                         *(PG8_LAS f32x4*)(tile + rw * 128 + ((g ^ fr) << 2)) = p;
;     ...
;             if (half == 0) {
;                 float nw[16];
; #pragma unroll
;                 for (int i = 0; i < 4; ++i) { const f32x4 v = *(const PG8_LAS f32x4*)(tile + row * 16 + 4 * i); nw[4 * i] = v[0]; nw[4 * i + 1] = v[1]; nw[4 * i + 2] = v[2]; nw[4 * i + 3] = v[3]; }
;                 merge_top16(run, nw);
;             }
; #pragma unroll
;             for (int q = 0; q < 16; ++q) { if (bj == 0) top0[q] = run[q]; else top1[q] = run[q]; }
.LBB0_600:
	s_waitcnt lgkmcnt(0)
	s_barrier
	s_cmp_lt_u32 s44, 4
	s_cselect_b64 s[14:15], -1, 0
	s_cmp_gt_u32 s44, 3
	s_cbranch_scc1 .LBB0_602
	ds_read_b128 v[106:109], v97 offset:48
	ds_read_b128 v[110:113], v97 offset:32
	ds_read_b128 v[114:117], v97
	ds_read_b128 v[130:133], v97 offset:16
	s_waitcnt lgkmcnt(0)
	v_max_f32_e32 v105, v109, v109
	v_max_f32_e32 v76, v76, v105
	v_max_f32_e32 v105, v108, v108
	v_max_f32_e32 v77, v77, v105
	v_max_f32_e32 v105, v107, v107
	v_max_f32_e32 v78, v78, v105
	v_max_f32_e32 v105, v106, v106
	v_max_f32_e32 v79, v79, v105
	v_max_f32_e32 v105, v113, v113
	v_max_f32_e32 v72, v72, v105
	v_max_f32_e32 v105, v112, v112
	v_max_f32_e32 v73, v73, v105
	v_max_f32_e32 v105, v111, v111
	v_max_f32_e32 v74, v74, v105
	v_max_f32_e32 v105, v110, v110
	v_max_f32_e32 v75, v75, v105
	v_max_f32_e32 v105, v133, v133
	v_max_f32_e32 v68, v68, v105
	v_max_f32_e32 v105, v132, v132
	v_max_f32_e32 v69, v69, v105
	v_max_f32_e32 v105, v131, v131
	v_max_f32_e32 v70, v70, v105
	v_max_f32_e32 v105, v130, v130
	v_max_f32_e32 v71, v71, v105
	v_max_f32_e32 v105, v117, v117
	v_max_f32_e32 v64, v64, v105
	v_max_f32_e32 v105, v116, v116
	v_max_f32_e32 v65, v65, v105
	v_max_f32_e32 v105, v115, v115
	v_max_f32_e32 v66, v66, v105
	v_max_f32_e32 v105, v114, v114
	v_max_f32_e32 v67, v67, v105
	v_max_f32_e32 v105, v76, v68
	v_min_f32_e32 v68, v76, v68
	v_max_f32_e32 v76, v77, v69
	v_min_f32_e32 v69, v77, v69
	v_max_f32_e32 v77, v78, v70
	v_min_f32_e32 v70, v78, v70
	v_max_f32_e32 v78, v79, v71
	v_min_f32_e32 v71, v79, v71
	v_max_f32_e32 v79, v72, v64
	v_min_f32_e32 v64, v72, v64
	v_max_f32_e32 v72, v73, v65
	v_min_f32_e32 v65, v73, v65
	v_max_f32_e32 v73, v74, v66
	v_min_f32_e32 v66, v74, v66
	v_max_f32_e32 v74, v75, v67
	v_min_f32_e32 v67, v75, v67
	v_max_f32_e32 v75, v105, v79
	v_min_f32_e32 v79, v105, v79
	v_max_f32_e32 v105, v76, v72
	v_min_f32_e32 v72, v76, v72
	v_max_f32_e32 v76, v77, v73
	v_min_f32_e32 v73, v77, v73
	v_max_f32_e32 v77, v78, v74
	v_min_f32_e32 v74, v78, v74
	v_max_f32_e32 v78, v68, v64
	v_min_f32_e32 v64, v68, v64
	v_max_f32_e32 v68, v69, v65
	v_min_f32_e32 v65, v69, v65
	v_max_f32_e32 v69, v70, v66
	v_min_f32_e32 v66, v70, v66
	v_max_f32_e32 v70, v71, v67
	v_min_f32_e32 v67, v71, v67
	v_max_f32_e32 v71, v75, v76
	v_min_f32_e32 v75, v75, v76
	v_max_f32_e32 v106, v105, v77
	v_min_f32_e32 v105, v105, v77
	v_max_f32_e32 v107, v79, v73
	v_min_f32_e32 v108, v79, v73
	v_max_f32_e32 v73, v72, v74
	v_min_f32_e32 v109, v72, v74
	v_max_f32_e32 v110, v78, v69
	v_min_f32_e32 v111, v78, v69
	v_max_f32_e32 v69, v68, v70
	v_min_f32_e32 v112, v68, v70
	v_max_f32_e32 v113, v64, v66
	v_min_f32_e32 v114, v64, v66
	v_max_f32_e32 v66, v65, v67
	v_min_f32_e32 v67, v65, v67
	v_max_f32_e32 v76, v71, v106
	v_min_f32_e32 v77, v71, v106
	v_max_f32_e32 v78, v75, v105
	v_min_f32_e32 v79, v75, v105
	v_max_f32_e32 v72, v107, v73
	v_min_f32_e32 v73, v107, v73
	v_max_f32_e32 v74, v108, v109
	v_min_f32_e32 v75, v108, v109
	v_max_f32_e32 v68, v110, v69
	v_min_f32_e32 v69, v110, v69
	v_max_f32_e32 v70, v111, v112
	v_min_f32_e32 v71, v111, v112
	v_max_f32_e32 v64, v113, v66
	v_min_f32_e32 v65, v113, v66
	v_max_f32_e32 v66, v114, v67
	v_min_f32_e32 v67, v114, v67
.LBB0_602:
	s_movk_i32 s3, 0xff80
	v_and_or_b32 v60, v60, s3, v129
	v_and_or_b32 v61, v61, s98, v224
	v_and_or_b32 v62, v62, s98, v225
	v_and_or_b32 v63, v63, s98, v226
	v_and_or_b32 v56, v56, s3, v124
	v_and_or_b32 v57, v57, s98, v227
	v_and_or_b32 v58, v58, s98, v228
	v_and_or_b32 v59, v59, s98, v229
	v_and_or_b32 v52, v52, s3, v129
	v_and_or_b32 v53, v53, s98, v224
	v_and_or_b32 v54, v54, s98, v225
	v_and_or_b32 v55, v55, s98, v226
	v_and_or_b32 v48, v48, s3, v124
	v_and_or_b32 v49, v49, s98, v227
	v_and_or_b32 v50, v50, s98, v228
	v_and_or_b32 v51, v51, s98, v229
	v_and_or_b32 v44, v44, s3, v129
	v_and_or_b32 v45, v45, s98, v224
	v_and_or_b32 v46, v46, s98, v225
	v_and_or_b32 v47, v47, s98, v226
	v_and_or_b32 v40, v40, s3, v124
	v_and_or_b32 v41, v41, s98, v227
	v_and_or_b32 v42, v42, s98, v228
	v_and_or_b32 v43, v43, s98, v229
	v_and_or_b32 v36, v36, s3, v129
	v_and_or_b32 v37, v37, s98, v224
	v_and_or_b32 v38, v38, s98, v225
	v_and_or_b32 v39, v39, s98, v226
	v_and_or_b32 v32, v32, s3, v124
	v_and_or_b32 v33, v33, s98, v227
	v_and_or_b32 v34, v34, s98, v228
	v_and_or_b32 v35, v35, s98, v229
	v_and_or_b32 v28, v28, s3, v129
	v_and_or_b32 v29, v29, s98, v224
	v_and_or_b32 v30, v30, s98, v225
	v_and_or_b32 v31, v31, s98, v226
	v_and_or_b32 v24, v24, s3, v124
	v_and_or_b32 v25, v25, s98, v227
	v_and_or_b32 v26, v26, s98, v228
	v_and_or_b32 v27, v27, s98, v229
	v_and_or_b32 v20, v20, s3, v129
	v_and_or_b32 v21, v21, s98, v224
	v_and_or_b32 v22, v22, s98, v225
	v_and_or_b32 v23, v23, s98, v226
	v_and_or_b32 v16, v16, s3, v124
	v_and_or_b32 v17, v17, s98, v227
	v_and_or_b32 v18, v18, s98, v228
	v_and_or_b32 v19, v19, s98, v229
	v_and_or_b32 v12, v12, s3, v129
	v_and_or_b32 v13, v13, s98, v224
	v_and_or_b32 v14, v14, s98, v225
	v_and_or_b32 v15, v15, s98, v226
	v_and_or_b32 v8, v8, s3, v124
	v_and_or_b32 v9, v9, s98, v227
	v_and_or_b32 v10, v10, s98, v228
	v_and_or_b32 v11, v11, s98, v229
	v_and_or_b32 v4, v4, s3, v129
	v_and_or_b32 v5, v5, s98, v224
	v_and_or_b32 v6, v6, s98, v225
	v_and_or_b32 v7, v7, s98, v226
	v_and_or_b32 v0, v0, s3, v124
	v_and_or_b32 v1, v1, s98, v227
	v_and_or_b32 v2, v2, s98, v228
	v_and_or_b32 v3, v3, s98, v229
	s_waitcnt lgkmcnt(0)
	s_barrier
; #define PG8_LAS __attribute__((address_space(3)))
; #define CE(a, b) do { const float hi_ = fmaxf(a, b), lo_ = fminf(a, b); a = hi_; b = lo_; } while (0)
; #define RT_BAR() do { asm volatile("s_waitcnt lgkmcnt(0)" ::: "memory"); __builtin_amdgcn_s_barrier(); asm volatile("" ::: "memory"); } while (0)
; __device__ __forceinline__ void sort16_desc(float (&v)[16]) {
;     CE(v[0], v[1]); CE(v[2], v[3]); CE(v[0], v[2]); CE(v[1], v[3]);
;     CE(v[1], v[2]); CE(v[4], v[5]); CE(v[6], v[7]); CE(v[4], v[6]);
;     CE(v[5], v[7]); CE(v[5], v[6]); CE(v[0], v[4]); CE(v[2], v[6]);
;     CE(v[2], v[4]); CE(v[1], v[5]); CE(v[3], v[7]); CE(v[3], v[5]);
;     CE(v[1], v[2]); CE(v[3], v[4]); CE(v[5], v[6]); CE(v[8], v[9]);
;     CE(v[10], v[11]); CE(v[8], v[10]); CE(v[9], v[11]); CE(v[9], v[10]);
;     CE(v[12], v[13]); CE(v[14], v[15]); CE(v[12], v[14]); CE(v[13], v[15]);
;     CE(v[13], v[14]); CE(v[8], v[12]); CE(v[10], v[14]); CE(v[10], v[12]);
;     CE(v[9], v[13]); CE(v[11], v[15]); CE(v[11], v[13]); CE(v[9], v[10]);
;     CE(v[11], v[12]); CE(v[13], v[14]); CE(v[0], v[8]); CE(v[4], v[12]);
;     CE(v[4], v[8]); CE(v[2], v[10]); CE(v[6], v[14]); CE(v[6], v[10]);
;     CE(v[2], v[4]); CE(v[6], v[8]); CE(v[10], v[12]); CE(v[1], v[9]);
;     CE(v[5], v[13]); CE(v[5], v[9]); CE(v[3], v[11]); CE(v[7], v[15]);
;     CE(v[7], v[11]); CE(v[3], v[5]); CE(v[7], v[9]); CE(v[11], v[13]);
;     CE(v[1], v[2]); CE(v[3], v[4]); CE(v[5], v[6]); CE(v[7], v[8]);
;     CE(v[9], v[10]); CE(v[11], v[12]); CE(v[13], v[14]);
; }
;     __device__ __forceinline__ void fused(f32x4 (&acc)[2][2][4][2], const Unit& u, int wr, int wc, int fr, int fq, PG8_LAS unsigned char* lds, int wid, int lane) const {
;     ...
;             RT_BAR();
;             float run[16];
; #pragma unroll
;             for (int grp = 0; grp < 4; ++grp) {
;                 float nw[16];
; #pragma unroll
;                 for (int i = 0; i < 4; ++i) { const int g = half * 16 + grp * 4 + i; const f32x4 v = *(const PG8_LAS f32x4*)(tile + row * 128 + ((g ^ (row & 15)) << 2));
;                     nw[4 * i] = v[0]; nw[4 * i + 1] = v[1]; nw[4 * i + 2] = v[2]; nw[4 * i + 3] = v[3]; }
;                 sort16_desc(nw);
;                 if (grp == 0) {
; #pragma unroll
;                     for (int q = 0; q < 16; ++q) run[q] = nw[q];
;                 } else merge_top16(run, nw);
	ds_write_b128 v125, v[60:63]
	ds_write_b128 v120, v[56:59]
	ds_write_b128 v125, v[52:55] offset:8192
	ds_write_b128 v120, v[48:51] offset:8192
	ds_write_b128 v125, v[44:47] offset:16384
	ds_write_b128 v120, v[40:43] offset:16384
	ds_write_b128 v125, v[36:39] offset:24576
	ds_write_b128 v120, v[32:35] offset:24576
	ds_write_b128 v92, v[28:31]
	ds_write_b128 v88, v[24:27]
	ds_write_b128 v84, v[20:23]
	ds_write_b128 v82, v[16:19]
	ds_write_b128 v85, v[12:15]
	ds_write_b128 v86, v[8:11]
	ds_write_b128 v90, v[4:7]
	ds_write_b128 v91, v[0:3]
	s_waitcnt lgkmcnt(0)
	s_barrier
	ds_read_b128 v[0:3], v93
	ds_read_b128 v[4:7], v89
	s_and_b64 vcc, exec, s[4:5]
	s_waitcnt lgkmcnt(0)
	v_min_f32_e32 v10, v0, v1
	v_max_f32_e32 v8, v0, v1
	v_min_f32_e32 v13, v2, v3
	v_max_f32_e32 v9, v2, v3
	v_min_f32_e32 v17, v4, v5
	v_max_f32_e32 v15, v4, v5
	v_min_f32_e32 v20, v6, v7
	v_max_f32_e32 v16, v6, v7
	ds_read_b128 v[0:3], v81
	ds_read_b128 v[4:7], v80
	s_waitcnt lgkmcnt(0)
	v_min_f32_e32 v23, v0, v1
	v_min_f32_e32 v24, v2, v3
	v_min_f32_e32 v26, v4, v5
	v_min_f32_e32 v27, v6, v7
	v_max_f32_e32 v0, v0, v1
	v_max_f32_e32 v1, v2, v3
	v_max_f32_e32 v4, v4, v5
	v_max_f32_e32 v5, v6, v7
	v_min_f32_e32 v14, v10, v13
	v_min_f32_e32 v21, v17, v20
	v_min_f32_e32 v25, v23, v24
	v_max_f32_e32 v10, v10, v13
	v_min_f32_e32 v11, v8, v9
	v_max_f32_e32 v13, v17, v20
	v_min_f32_e32 v17, v15, v16
	v_max_f32_e32 v23, v23, v24
	v_min_f32_e32 v2, v0, v1
	v_max_f32_e32 v24, v26, v27
	v_min_f32_e32 v6, v4, v5
	v_min_f32_e32 v28, v26, v27
	v_max_f32_e32 v12, v10, v11
	v_max_f32_e32 v18, v13, v17
	v_max_f32_e32 v3, v23, v2
	v_max_f32_e32 v7, v24, v6
	v_min_f32_e32 v22, v14, v21
	v_min_f32_e32 v29, v25, v28
	v_max_f32_e32 v14, v14, v21
	v_min_f32_e32 v19, v12, v18
	v_min_f32_e32 v10, v10, v11
	v_min_f32_e32 v11, v13, v17
	v_max_f32_e32 v21, v25, v28
	v_min_f32_e32 v25, v3, v7
	v_min_f32_e32 v2, v23, v2
	v_min_f32_e32 v6, v24, v6
	v_max_f32_e32 v20, v14, v19
	v_max_f32_e32 v13, v10, v11
	v_max_f32_e32 v8, v8, v9
	v_max_f32_e32 v9, v15, v16
	v_max_f32_e32 v23, v2, v6
	v_max_f32_e32 v0, v0, v1
	v_max_f32_e32 v1, v4, v5
	v_min_f32_e32 v14, v14, v19
	v_min_f32_e32 v10, v10, v11
	v_min_f32_e32 v19, v21, v25
	v_min_f32_e32 v2, v2, v6
	v_min_f32_e32 v15, v8, v9
	v_min_f32_e32 v4, v0, v1
	v_max_f32_e32 v11, v14, v10
	v_max_f32_e32 v6, v19, v2
	v_min_f32_e32 v10, v14, v10
	v_min_f32_e32 v2, v19, v2
	v_min_f32_e32 v5, v23, v4
	v_min_f32_e32 v14, v10, v2
	v_max_f32_e32 v2, v10, v2
	v_max_f32_e32 v10, v12, v18
	v_max_f32_e32 v12, v13, v15
	v_max_f32_e32 v3, v3, v7
	v_max_f32_e32 v4, v23, v4
	v_min_f32_e32 v16, v13, v15
	v_max_f32_e32 v26, v21, v25
	v_min_f32_e32 v13, v10, v12
	v_min_f32_e32 v7, v3, v4
	v_max_f32_e32 v10, v10, v12
	v_max_f32_e32 v3, v3, v4
	v_max_f32_e32 v17, v20, v16
	v_max_f32_e32 v24, v26, v5
	v_min_f32_e32 v21, v11, v6
	v_min_f32_e32 v16, v20, v16
	v_min_f32_e32 v5, v26, v5
	v_max_f32_e32 v6, v11, v6
	v_min_f32_e32 v4, v10, v3
	v_max_f32_e32 v8, v8, v9
	v_max_f32_e32 v9, v0, v1
	v_max_f32_e32 v30, v22, v29
	v_min_f32_e32 v27, v17, v24
	v_min_f32_e32 v15, v13, v7
	v_min_f32_e32 v20, v16, v5
	v_min_f32_e32 v11, v6, v4
	v_max_f32_e32 v5, v16, v5
	v_min_f32_e32 v0, v8, v9
	v_max_f32_e32 v17, v17, v24
	v_max_f32_e32 v4, v6, v4
	v_min_f32_e32 v28, v30, v27
	v_min_f32_e32 v18, v2, v15
	v_max_f32_e32 v27, v30, v27
	v_max_f32_e32 v2, v2, v15
	v_min_f32_e32 v1, v5, v0
	v_min_f32_e32 v24, v17, v4
	v_max_f32_e32 v17, v17, v4
	v_max_f32_e32 v4, v13, v7
	v_max_f32_e32 v5, v5, v0
	v_min_f32_e32 v12, v27, v11
	v_max_f32_e32 v11, v27, v11
	v_min_f32_e32 v15, v2, v1
	v_max_f32_e32 v27, v2, v1
	v_min_f32_e32 v13, v4, v5
	v_max_f32_e32 v10, v10, v3
	ds_read_b128 v[0:3], v99
	v_max_f32_e32 v31, v4, v5
	ds_read_b128 v[4:7], v96
	v_min_f32_e32 v22, v22, v29
	v_min_f32_e32 v25, v28, v21
	s_waitcnt lgkmcnt(0)
	v_min_f32_e32 v34, v0, v1
	v_max_f32_e32 v29, v0, v1
	v_min_f32_e32 v37, v2, v3
	v_max_f32_e32 v33, v2, v3
	v_min_f32_e32 v41, v4, v5
	v_max_f32_e32 v39, v4, v5
	v_min_f32_e32 v44, v6, v7
	v_max_f32_e32 v40, v6, v7
	ds_read_b128 v[0:3], v87
	ds_read_b128 v[4:7], v83
	s_waitcnt lgkmcnt(0)
	v_min_f32_e32 v47, v0, v1
	v_min_f32_e32 v48, v2, v3
	v_min_f32_e32 v50, v4, v5
	v_min_f32_e32 v51, v6, v7
	v_max_f32_e32 v0, v0, v1
	v_max_f32_e32 v1, v2, v3
	v_max_f32_e32 v4, v4, v5
	v_max_f32_e32 v5, v6, v7
	v_min_f32_e32 v38, v34, v37
	v_min_f32_e32 v45, v41, v44
	v_min_f32_e32 v49, v47, v48
	v_max_f32_e32 v34, v34, v37
	v_min_f32_e32 v35, v29, v33
	v_max_f32_e32 v37, v41, v44
	v_min_f32_e32 v41, v39, v40
	v_max_f32_e32 v47, v47, v48
	v_min_f32_e32 v2, v0, v1
	v_max_f32_e32 v48, v50, v51
	v_min_f32_e32 v6, v4, v5
	v_min_f32_e32 v52, v50, v51
	v_max_f32_e32 v36, v34, v35
	v_max_f32_e32 v42, v37, v41
	v_max_f32_e32 v3, v47, v2
	v_max_f32_e32 v7, v48, v6
	v_min_f32_e32 v46, v38, v45
	v_min_f32_e32 v53, v49, v52
	v_max_f32_e32 v38, v38, v45
	v_min_f32_e32 v43, v36, v42
	v_min_f32_e32 v34, v34, v35
	v_min_f32_e32 v35, v37, v41
	v_max_f32_e32 v45, v49, v52
	v_min_f32_e32 v49, v3, v7
	v_min_f32_e32 v2, v47, v2
	v_min_f32_e32 v6, v48, v6
	v_max_f32_e32 v44, v38, v43
	v_max_f32_e32 v37, v34, v35
	v_max_f32_e32 v29, v29, v33
	v_max_f32_e32 v33, v39, v40
	v_max_f32_e32 v47, v2, v6
	v_max_f32_e32 v0, v0, v1
	v_max_f32_e32 v1, v4, v5
	v_min_f32_e32 v38, v38, v43
	v_min_f32_e32 v34, v34, v35
	v_min_f32_e32 v43, v45, v49
	v_min_f32_e32 v2, v2, v6
	v_min_f32_e32 v39, v29, v33
	v_min_f32_e32 v4, v0, v1
	v_max_f32_e32 v35, v38, v34
	v_max_f32_e32 v6, v43, v2
	v_min_f32_e32 v34, v38, v34
	v_min_f32_e32 v2, v43, v2
	v_min_f32_e32 v40, v37, v39
	v_max_f32_e32 v50, v45, v49
	v_min_f32_e32 v5, v47, v4
	v_min_f32_e32 v38, v34, v2
; __device__ __forceinline__ void sort16_desc(float (&v)[16]) {
;     CE(v[0], v[1]); CE(v[2], v[3]); CE(v[0], v[2]); CE(v[1], v[3]);
;     CE(v[1], v[2]); CE(v[4], v[5]); CE(v[6], v[7]); CE(v[4], v[6]);
;     CE(v[5], v[7]); CE(v[5], v[6]); CE(v[0], v[4]); CE(v[2], v[6]);
;     CE(v[2], v[4]); CE(v[1], v[5]); CE(v[3], v[7]); CE(v[3], v[5]);
;     CE(v[1], v[2]); CE(v[3], v[4]); CE(v[5], v[6]); CE(v[8], v[9]);
;     CE(v[10], v[11]); CE(v[8], v[10]); CE(v[9], v[11]); CE(v[9], v[10]);
;     CE(v[12], v[13]); CE(v[14], v[15]); CE(v[12], v[14]); CE(v[13], v[15]);
;     CE(v[13], v[14]); CE(v[8], v[12]); CE(v[10], v[14]); CE(v[10], v[12]);
;     CE(v[9], v[13]); CE(v[11], v[15]); CE(v[11], v[13]); CE(v[9], v[10]);
;     CE(v[11], v[12]); CE(v[13], v[14]); CE(v[0], v[8]); CE(v[4], v[12]);
;     CE(v[4], v[8]); CE(v[2], v[10]); CE(v[6], v[14]); CE(v[6], v[10]);
;     CE(v[2], v[4]); CE(v[6], v[8]); CE(v[10], v[12]); CE(v[1], v[9]);
;     CE(v[5], v[13]); CE(v[5], v[9]); CE(v[3], v[11]); CE(v[7], v[15]);
;     CE(v[7], v[11]); CE(v[3], v[5]); CE(v[7], v[9]); CE(v[11], v[13]);
;     CE(v[1], v[2]); CE(v[3], v[4]); CE(v[5], v[6]); CE(v[7], v[8]);
;     CE(v[9], v[10]); CE(v[11], v[12]); CE(v[13], v[14]);
; }
; __device__ __forceinline__ void merge_top16(float (&v)[16], const float (&nw)[16]) {
;     v[0] = fmaxf(v[0], nw[15]); v[1] = fmaxf(v[1], nw[14]); v[2] = fmaxf(v[2], nw[13]); v[3] = fmaxf(v[3], nw[12]); v[4] = fmaxf(v[4], nw[11]); v[5] = fmaxf(v[5], nw[10]); v[6] = fmaxf(v[6], nw[9]); v[7] = fmaxf(v[7], nw[8]); v[8] = fmaxf(v[8], nw[7]); v[9] = fmaxf(v[9], nw[6]); v[10] = fmaxf(v[10], nw[5]); v[11] = fmaxf(v[11], nw[4]); v[12] = fmaxf(v[12], nw[3]); v[13] = fmaxf(v[13], nw[2]); v[14] = fmaxf(v[14], nw[1]); v[15] = fmaxf(v[15], nw[0]);
;     CE(v[0], v[8]); CE(v[1], v[9]); CE(v[2], v[10]); CE(v[3], v[11]);
;     CE(v[4], v[12]); CE(v[5], v[13]); CE(v[6], v[14]); CE(v[7], v[15]);
;     CE(v[0], v[4]); CE(v[1], v[5]); CE(v[2], v[6]); CE(v[3], v[7]);
;     CE(v[8], v[12]); CE(v[9], v[13]); CE(v[10], v[14]); CE(v[11], v[15]);
;     CE(v[0], v[2]); CE(v[1], v[3]); CE(v[4], v[6]); CE(v[5], v[7]);
;     CE(v[8], v[10]); CE(v[9], v[11]); CE(v[12], v[14]); CE(v[13], v[15]);
;     CE(v[0], v[1]); CE(v[2], v[3]); CE(v[4], v[5]); CE(v[6], v[7]);
;     CE(v[8], v[9]); CE(v[10], v[11]); CE(v[12], v[13]); CE(v[14], v[15]);
; }
	v_max_f32_e32 v2, v34, v2
	v_max_f32_e32 v34, v36, v42
	v_max_f32_e32 v36, v37, v39
	v_max_f32_e32 v3, v3, v7
	v_max_f32_e32 v4, v47, v4
	v_max_f32_e32 v41, v44, v40
	v_max_f32_e32 v48, v50, v5
	v_min_f32_e32 v37, v34, v36
	v_min_f32_e32 v7, v3, v4
	v_min_f32_e32 v40, v44, v40
	v_min_f32_e32 v5, v50, v5
	v_max_f32_e32 v34, v34, v36
	v_max_f32_e32 v3, v3, v4
	v_max_f32_e32 v29, v29, v33
	v_max_f32_e32 v0, v0, v1
	v_max_f32_e32 v54, v46, v53
	v_min_f32_e32 v51, v41, v48
	v_min_f32_e32 v45, v35, v6
	v_min_f32_e32 v39, v37, v7
	v_min_f32_e32 v44, v40, v5
	v_max_f32_e32 v6, v35, v6
	v_min_f32_e32 v4, v34, v3
	v_max_f32_e32 v5, v40, v5
	v_min_f32_e32 v1, v29, v0
	v_min_f32_e32 v52, v54, v51
	v_min_f32_e32 v42, v2, v39
	v_max_f32_e32 v51, v54, v51
	v_min_f32_e32 v35, v6, v4
	v_max_f32_e32 v2, v2, v39
	v_min_f32_e32 v33, v5, v1
	v_max_f32_e32 v41, v41, v48
	v_max_f32_e32 v4, v6, v4
	v_max_f32_e32 v7, v37, v7
	v_max_f32_e32 v1, v5, v1
	v_max_f32_e32 v21, v28, v21
	v_min_f32_e32 v23, v18, v20
	v_max_f32_e32 v18, v18, v20
	v_min_f32_e32 v49, v52, v45
	v_max_f32_e32 v45, v52, v45
	v_min_f32_e32 v47, v42, v44
	v_min_f32_e32 v36, v51, v35
	v_max_f32_e32 v42, v42, v44
	v_max_f32_e32 v35, v51, v35
	v_min_f32_e32 v39, v2, v33
	v_min_f32_e32 v6, v41, v4
	v_max_f32_e32 v2, v2, v33
	v_max_f32_e32 v4, v41, v4
	v_min_f32_e32 v5, v7, v1
	v_max_f32_e32 v3, v34, v3
	v_max_f32_e32 v1, v7, v1
	v_min_f32_e32 v19, v25, v14
	v_min_f32_e32 v26, v21, v23
	v_min_f32_e32 v20, v12, v18
	v_min_f32_e32 v16, v11, v15
	v_min_f32_e32 v28, v24, v27
	v_min_f32_e32 v30, v17, v13
	v_min_f32_e32 v32, v10, v31
	v_min_f32_e32 v43, v49, v38
	v_min_f32_e32 v50, v45, v47
	v_min_f32_e32 v44, v36, v42
	v_min_f32_e32 v40, v35, v39
	v_min_f32_e32 v33, v6, v2
	v_min_f32_e32 v37, v4, v5
	v_min_f32_e32 v7, v3, v1
	v_min_f32_e32 v34, v46, v53
	v_max3_f32 v8, v8, v9, v34
	v_max3_f32 v9, v10, v31, v43
	v_max3_f32 v10, v32, v49, v38
	v_max3_f32 v13, v17, v13, v50
	v_max3_f32 v17, v30, v45, v47
	v_max3_f32 v24, v24, v27, v44
	v_max3_f32 v27, v28, v36, v42
	v_max3_f32 v11, v11, v15, v40
	v_max3_f32 v15, v16, v35, v39
	v_max3_f32 v12, v12, v18, v33
	v_max3_f32 v2, v20, v6, v2
	v_max3_f32 v6, v21, v23, v37
	v_max3_f32 v4, v26, v4, v5
	v_max3_f32 v5, v25, v14, v7
	v_max3_f32 v1, v19, v3, v1
	v_max3_f32 v0, v22, v29, v0
	v_max_f32_e32 v3, v8, v15
	v_min_f32_e32 v7, v8, v15
	v_max_f32_e32 v8, v9, v12
	v_min_f32_e32 v9, v9, v12
	v_max_f32_e32 v12, v10, v2
	v_min_f32_e32 v2, v10, v2
	v_max_f32_e32 v10, v13, v6
	v_min_f32_e32 v6, v13, v6
	v_max_f32_e32 v13, v17, v4
	v_min_f32_e32 v4, v17, v4
	v_max_f32_e32 v14, v24, v5
	v_min_f32_e32 v5, v24, v5
	v_max_f32_e32 v15, v27, v1
	v_min_f32_e32 v1, v27, v1
	v_max_f32_e32 v16, v11, v0
	v_min_f32_e32 v0, v11, v0
	v_max_f32_e32 v11, v3, v13
	v_min_f32_e32 v3, v3, v13
	v_max_f32_e32 v13, v8, v14
	v_min_f32_e32 v8, v8, v14
	v_max_f32_e32 v14, v12, v15
	v_min_f32_e32 v12, v12, v15
	v_max_f32_e32 v15, v10, v16
	v_min_f32_e32 v10, v10, v16
	v_max_f32_e32 v16, v7, v4
	v_min_f32_e32 v4, v7, v4
	v_max_f32_e32 v7, v9, v5
	v_min_f32_e32 v5, v9, v5
	v_max_f32_e32 v9, v2, v1
	v_min_f32_e32 v1, v2, v1
	v_max_f32_e32 v2, v6, v0
	v_min_f32_e32 v0, v6, v0
	v_max_f32_e32 v17, v11, v14
	v_min_f32_e32 v11, v11, v14
	v_max_f32_e32 v14, v13, v15
	v_min_f32_e32 v13, v13, v15
	v_max_f32_e32 v15, v3, v12
	v_min_f32_e32 v12, v3, v12
	v_max_f32_e32 v18, v8, v10
	v_min_f32_e32 v8, v8, v10
	v_max_f32_e32 v10, v16, v9
	v_min_f32_e32 v9, v16, v9
	v_max_f32_e32 v16, v7, v2
	v_min_f32_e32 v19, v7, v2
	v_max_f32_e32 v20, v4, v1
	v_min_f32_e32 v21, v4, v1
	v_max_f32_e32 v22, v5, v0
	v_min_f32_e32 v23, v5, v0
	ds_read_b128 v[0:3], v102
	ds_read_b128 v[4:7], v101
	v_min_f32_e32 v24, v17, v14
	v_min_f32_e32 v25, v11, v13
	v_min_f32_e32 v26, v15, v18
	s_waitcnt lgkmcnt(0)
	v_min_f32_e32 v34, v0, v1
	v_max_f32_e32 v32, v0, v1
	v_min_f32_e32 v37, v2, v3
	v_max_f32_e32 v33, v2, v3
	v_min_f32_e32 v41, v4, v5
	v_max_f32_e32 v39, v4, v5
	v_min_f32_e32 v44, v6, v7
	v_max_f32_e32 v40, v6, v7
	ds_read_b128 v[0:3], v95
	ds_read_b128 v[4:7], v94
	s_waitcnt lgkmcnt(0)
	v_min_f32_e32 v47, v0, v1
	v_min_f32_e32 v48, v2, v3
	v_min_f32_e32 v50, v4, v5
	v_min_f32_e32 v51, v6, v7
	v_max_f32_e32 v0, v0, v1
	v_max_f32_e32 v1, v2, v3
	v_max_f32_e32 v4, v4, v5
	v_max_f32_e32 v5, v6, v7
	v_min_f32_e32 v38, v34, v37
	v_min_f32_e32 v45, v41, v44
	v_min_f32_e32 v49, v47, v48
	v_max_f32_e32 v34, v34, v37
	v_min_f32_e32 v35, v32, v33
	v_max_f32_e32 v37, v41, v44
	v_min_f32_e32 v41, v39, v40
	v_max_f32_e32 v47, v47, v48
	v_min_f32_e32 v2, v0, v1
	v_max_f32_e32 v48, v50, v51
	v_min_f32_e32 v6, v4, v5
	v_min_f32_e32 v52, v50, v51
	v_max_f32_e32 v36, v34, v35
	v_max_f32_e32 v42, v37, v41
	v_max_f32_e32 v3, v47, v2
	v_max_f32_e32 v7, v48, v6
	v_min_f32_e32 v46, v38, v45
	v_min_f32_e32 v53, v49, v52
	v_max_f32_e32 v38, v38, v45
	v_min_f32_e32 v43, v36, v42
	v_min_f32_e32 v34, v34, v35
	v_min_f32_e32 v35, v37, v41
	v_max_f32_e32 v45, v49, v52
	v_min_f32_e32 v49, v3, v7
	v_min_f32_e32 v2, v47, v2
	v_min_f32_e32 v6, v48, v6
	v_max_f32_e32 v44, v38, v43
	v_max_f32_e32 v37, v34, v35
	v_max_f32_e32 v32, v32, v33
	v_max_f32_e32 v33, v39, v40
	v_max_f32_e32 v47, v2, v6
	v_max_f32_e32 v0, v0, v1
	v_max_f32_e32 v1, v4, v5
	v_min_f32_e32 v38, v38, v43
	v_min_f32_e32 v34, v34, v35
	v_min_f32_e32 v43, v45, v49
	v_min_f32_e32 v2, v2, v6
	v_min_f32_e32 v39, v32, v33
	v_min_f32_e32 v4, v0, v1
	v_max_f32_e32 v35, v38, v34
	v_max_f32_e32 v6, v43, v2
	v_min_f32_e32 v34, v38, v34
	v_min_f32_e32 v2, v43, v2
	v_min_f32_e32 v40, v37, v39
	v_max_f32_e32 v50, v45, v49
	v_min_f32_e32 v5, v47, v4
	v_min_f32_e32 v38, v34, v2
	v_max_f32_e32 v2, v34, v2
; __device__ __forceinline__ void sort16_desc(float (&v)[16]) {
;     CE(v[0], v[1]); CE(v[2], v[3]); CE(v[0], v[2]); CE(v[1], v[3]);
;     CE(v[1], v[2]); CE(v[4], v[5]); CE(v[6], v[7]); CE(v[4], v[6]);
;     CE(v[5], v[7]); CE(v[5], v[6]); CE(v[0], v[4]); CE(v[2], v[6]);
;     CE(v[2], v[4]); CE(v[1], v[5]); CE(v[3], v[7]); CE(v[3], v[5]);
;     CE(v[1], v[2]); CE(v[3], v[4]); CE(v[5], v[6]); CE(v[8], v[9]);
;     CE(v[10], v[11]); CE(v[8], v[10]); CE(v[9], v[11]); CE(v[9], v[10]);
;     CE(v[12], v[13]); CE(v[14], v[15]); CE(v[12], v[14]); CE(v[13], v[15]);
;     CE(v[13], v[14]); CE(v[8], v[12]); CE(v[10], v[14]); CE(v[10], v[12]);
;     CE(v[9], v[13]); CE(v[11], v[15]); CE(v[11], v[13]); CE(v[9], v[10]);
;     CE(v[11], v[12]); CE(v[13], v[14]); CE(v[0], v[8]); CE(v[4], v[12]);
;     CE(v[4], v[8]); CE(v[2], v[10]); CE(v[6], v[14]); CE(v[6], v[10]);
;     CE(v[2], v[4]); CE(v[6], v[8]); CE(v[10], v[12]); CE(v[1], v[9]);
;     CE(v[5], v[13]); CE(v[5], v[9]); CE(v[3], v[11]); CE(v[7], v[15]);
;     CE(v[7], v[11]); CE(v[3], v[5]); CE(v[7], v[9]); CE(v[11], v[13]);
;     CE(v[1], v[2]); CE(v[3], v[4]); CE(v[5], v[6]); CE(v[7], v[8]);
;     CE(v[9], v[10]); CE(v[11], v[12]); CE(v[13], v[14]);
; }
; __device__ __forceinline__ void merge_top16(float (&v)[16], const float (&nw)[16]) {
;     v[0] = fmaxf(v[0], nw[15]); v[1] = fmaxf(v[1], nw[14]); v[2] = fmaxf(v[2], nw[13]); v[3] = fmaxf(v[3], nw[12]); v[4] = fmaxf(v[4], nw[11]); v[5] = fmaxf(v[5], nw[10]); v[6] = fmaxf(v[6], nw[9]); v[7] = fmaxf(v[7], nw[8]); v[8] = fmaxf(v[8], nw[7]); v[9] = fmaxf(v[9], nw[6]); v[10] = fmaxf(v[10], nw[5]); v[11] = fmaxf(v[11], nw[4]); v[12] = fmaxf(v[12], nw[3]); v[13] = fmaxf(v[13], nw[2]); v[14] = fmaxf(v[14], nw[1]); v[15] = fmaxf(v[15], nw[0]);
;     CE(v[0], v[8]); CE(v[1], v[9]); CE(v[2], v[10]); CE(v[3], v[11]);
;     CE(v[4], v[12]); CE(v[5], v[13]); CE(v[6], v[14]); CE(v[7], v[15]);
;     CE(v[0], v[4]); CE(v[1], v[5]); CE(v[2], v[6]); CE(v[3], v[7]);
;     CE(v[8], v[12]); CE(v[9], v[13]); CE(v[10], v[14]); CE(v[11], v[15]);
;     CE(v[0], v[2]); CE(v[1], v[3]); CE(v[4], v[6]); CE(v[5], v[7]);
;     CE(v[8], v[10]); CE(v[9], v[11]); CE(v[12], v[14]); CE(v[13], v[15]);
;     CE(v[0], v[1]); CE(v[2], v[3]); CE(v[4], v[5]); CE(v[6], v[7]);
;     CE(v[8], v[9]); CE(v[10], v[11]); CE(v[12], v[13]); CE(v[14], v[15]);
; }
	v_max_f32_e32 v34, v36, v42
	v_max_f32_e32 v36, v37, v39
	v_max_f32_e32 v3, v3, v7
	v_max_f32_e32 v4, v47, v4
	v_max_f32_e32 v41, v44, v40
	v_max_f32_e32 v48, v50, v5
	v_min_f32_e32 v37, v34, v36
	v_min_f32_e32 v7, v3, v4
	v_max_f32_e32 v54, v46, v53
	v_min_f32_e32 v51, v41, v48
	v_min_f32_e32 v39, v37, v7
	v_min_f32_e32 v40, v44, v40
	v_min_f32_e32 v5, v50, v5
	v_min_f32_e32 v52, v54, v51
	v_min_f32_e32 v45, v35, v6
	v_min_f32_e32 v42, v2, v39
	v_min_f32_e32 v44, v40, v5
	v_max_f32_e32 v34, v34, v36
	v_max_f32_e32 v3, v3, v4
	v_max_f32_e32 v32, v32, v33
	v_max_f32_e32 v0, v0, v1
	v_min_f32_e32 v49, v52, v45
	v_max_f32_e32 v45, v52, v45
	v_min_f32_e32 v47, v42, v44
	v_max_f32_e32 v6, v35, v6
	v_min_f32_e32 v4, v34, v3
	v_max_f32_e32 v5, v40, v5
	v_min_f32_e32 v1, v32, v0
	v_min_f32_e32 v43, v49, v38
	v_max_f32_e32 v38, v49, v38
	v_min_f32_e32 v49, v45, v47
	v_max_f32_e32 v45, v45, v47
	v_max_f32_e32 v47, v54, v51
	v_min_f32_e32 v35, v6, v4
	v_max_f32_e32 v2, v2, v39
	v_min_f32_e32 v33, v5, v1
	v_min_f32_e32 v36, v47, v35
	v_max_f32_e32 v35, v47, v35
	v_min_f32_e32 v39, v2, v33
	v_min_f32_e32 v40, v35, v39
	v_max_f32_e32 v35, v35, v39
	v_max_f32_e32 v39, v41, v48
	v_max_f32_e32 v4, v6, v4
	v_min_f32_e32 v6, v39, v4
	v_max_f32_e32 v2, v2, v33
	v_min_f32_e32 v33, v6, v2
	v_max_f32_e32 v2, v6, v2
	v_max_f32_e32 v6, v37, v7
	v_max_f32_e32 v1, v5, v1
	v_max_f32_e32 v42, v42, v44
	v_max_f32_e32 v4, v39, v4
	v_min_f32_e32 v5, v6, v1
	v_max_f32_e32 v3, v34, v3
	v_max_f32_e32 v1, v6, v1
	v_min_f32_e32 v27, v12, v8
	v_min_f32_e32 v28, v10, v16
	v_min_f32_e32 v29, v9, v19
	v_min_f32_e32 v30, v20, v22
	v_min_f32_e32 v31, v21, v23
	v_min_f32_e32 v44, v36, v42
	v_max_f32_e32 v36, v36, v42
	v_min_f32_e32 v7, v4, v5
	v_max_f32_e32 v4, v4, v5
	v_min_f32_e32 v5, v3, v1
	v_max_f32_e32 v1, v3, v1
	v_min_f32_e32 v3, v46, v53
	v_max3_f32 v3, v17, v14, v3
	v_max_f32_e32 v6, v24, v43
	v_max3_f32 v11, v11, v13, v38
	v_max_f32_e32 v13, v25, v49
	v_max3_f32 v14, v15, v18, v45
	v_max_f32_e32 v15, v26, v44
	v_max3_f32 v8, v12, v8, v36
	v_max_f32_e32 v12, v27, v40
	v_max3_f32 v10, v10, v16, v35
	v_max_f32_e32 v16, v28, v33
	v_max3_f32 v2, v9, v19, v2
	v_max_f32_e32 v7, v29, v7
	v_max3_f32 v4, v20, v22, v4
	v_max_f32_e32 v5, v30, v5
	v_max3_f32 v1, v21, v23, v1
	v_max3_f32 v0, v31, v32, v0
	v_max_f32_e32 v9, v3, v10
	v_min_f32_e32 v3, v3, v10
	v_max_f32_e32 v10, v6, v16
	v_min_f32_e32 v6, v6, v16
	v_max_f32_e32 v16, v11, v2
	v_min_f32_e32 v2, v11, v2
	v_max_f32_e32 v11, v13, v7
	v_min_f32_e32 v7, v13, v7
	v_max_f32_e32 v13, v14, v4
	v_min_f32_e32 v4, v14, v4
	v_max_f32_e32 v14, v15, v5
	v_min_f32_e32 v5, v15, v5
	v_max_f32_e32 v15, v8, v1
	v_min_f32_e32 v1, v8, v1
	v_max_f32_e32 v8, v12, v0
	v_min_f32_e32 v0, v12, v0
	v_max_f32_e32 v12, v9, v13
	v_min_f32_e32 v9, v9, v13
	v_max_f32_e32 v13, v10, v14
	v_min_f32_e32 v10, v10, v14
	v_max_f32_e32 v14, v16, v15
	v_min_f32_e32 v15, v16, v15
	v_max_f32_e32 v16, v11, v8
	v_min_f32_e32 v8, v11, v8
	v_max_f32_e32 v11, v3, v4
	v_min_f32_e32 v3, v3, v4
	v_max_f32_e32 v4, v6, v5
	v_min_f32_e32 v5, v6, v5
	v_max_f32_e32 v6, v2, v1
	v_min_f32_e32 v1, v2, v1
	v_max_f32_e32 v2, v7, v0
	v_min_f32_e32 v0, v7, v0
	v_max_f32_e32 v17, v12, v14
	v_min_f32_e32 v12, v12, v14
	v_max_f32_e32 v14, v13, v16
	v_min_f32_e32 v13, v13, v16
	v_max_f32_e32 v16, v9, v15
	v_min_f32_e32 v9, v9, v15
	v_max_f32_e32 v15, v10, v8
	v_min_f32_e32 v8, v10, v8
	v_max_f32_e32 v10, v11, v6
	v_min_f32_e32 v11, v11, v6
	v_max_f32_e32 v18, v4, v2
	v_min_f32_e32 v19, v4, v2
	v_max_f32_e32 v20, v3, v1
	v_min_f32_e32 v21, v3, v1
	v_max_f32_e32 v22, v5, v0
	v_min_f32_e32 v23, v5, v0
	ds_read_b128 v[0:3], v104
	ds_read_b128 v[4:7], v103
	v_min_f32_e32 v24, v17, v14
	v_min_f32_e32 v25, v12, v13
	v_min_f32_e32 v26, v16, v15
	s_waitcnt lgkmcnt(0)
	v_min_f32_e32 v34, v0, v1
	v_max_f32_e32 v32, v0, v1
	v_min_f32_e32 v37, v2, v3
	v_max_f32_e32 v33, v2, v3
	v_min_f32_e32 v41, v4, v5
	v_max_f32_e32 v39, v4, v5
	v_min_f32_e32 v44, v6, v7
	v_max_f32_e32 v40, v6, v7
	ds_read_b128 v[0:3], v100
	ds_read_b128 v[4:7], v98
	s_waitcnt lgkmcnt(0)
	v_min_f32_e32 v47, v0, v1
	v_min_f32_e32 v48, v2, v3
	v_min_f32_e32 v50, v4, v5
	v_min_f32_e32 v51, v6, v7
	v_max_f32_e32 v0, v0, v1
	v_max_f32_e32 v1, v2, v3
	v_max_f32_e32 v4, v4, v5
	v_max_f32_e32 v5, v6, v7
	v_min_f32_e32 v38, v34, v37
	v_min_f32_e32 v45, v41, v44
	v_min_f32_e32 v49, v47, v48
	v_max_f32_e32 v34, v34, v37
	v_min_f32_e32 v35, v32, v33
	v_max_f32_e32 v37, v41, v44
	v_min_f32_e32 v41, v39, v40
	v_max_f32_e32 v47, v47, v48
	v_min_f32_e32 v2, v0, v1
	v_max_f32_e32 v48, v50, v51
	v_min_f32_e32 v6, v4, v5
	v_min_f32_e32 v52, v50, v51
	v_max_f32_e32 v36, v34, v35
	v_max_f32_e32 v42, v37, v41
	v_max_f32_e32 v3, v47, v2
	v_max_f32_e32 v7, v48, v6
	v_min_f32_e32 v46, v38, v45
	v_min_f32_e32 v53, v49, v52
	v_max_f32_e32 v38, v38, v45
	v_min_f32_e32 v43, v36, v42
	v_min_f32_e32 v34, v34, v35
	v_min_f32_e32 v35, v37, v41
	v_max_f32_e32 v45, v49, v52
	v_min_f32_e32 v49, v3, v7
	v_min_f32_e32 v2, v47, v2
	v_min_f32_e32 v6, v48, v6
	v_max_f32_e32 v44, v38, v43
	v_max_f32_e32 v37, v34, v35
	v_max_f32_e32 v32, v32, v33
	v_max_f32_e32 v33, v39, v40
	v_max_f32_e32 v47, v2, v6
	v_max_f32_e32 v0, v0, v1
	v_max_f32_e32 v1, v4, v5
	v_min_f32_e32 v38, v38, v43
	v_min_f32_e32 v34, v34, v35
	v_min_f32_e32 v43, v45, v49
	v_min_f32_e32 v2, v2, v6
	v_min_f32_e32 v39, v32, v33
	v_min_f32_e32 v4, v0, v1
	v_max_f32_e32 v35, v38, v34
	v_max_f32_e32 v6, v43, v2
	v_min_f32_e32 v34, v38, v34
	v_min_f32_e32 v2, v43, v2
	v_min_f32_e32 v40, v37, v39
	v_max_f32_e32 v50, v45, v49
	v_min_f32_e32 v5, v47, v4
	v_min_f32_e32 v38, v34, v2
	v_max_f32_e32 v2, v34, v2
; #define PG8_LAS __attribute__((address_space(3)))
; #define RT_BAR() do { asm volatile("s_waitcnt lgkmcnt(0)" ::: "memory"); __builtin_amdgcn_s_barrier(); asm volatile("" ::: "memory"); } while (0)
;     __device__ __forceinline__ void fused(f32x4 (&acc)[2][2][4][2], const Unit& u, int wr, int wc, int fr, int fq, PG8_LAS unsigned char* lds, int wid, int lane) const {
;     ...
;                 sort16_desc(nw);
;                 if (grp == 0) {
; #pragma unroll
;                     for (int q = 0; q < 16; ++q) run[q] = nw[q];
;                 } else merge_top16(run, nw);
;             }
;             RT_BAR();
;             if (half == 1) {
; #pragma unroll
;                 for (int i = 0; i < 4; ++i) *(PG8_LAS f32x4*)(tile + row * 16 + 4 * i) = (f32x4){run[4 * i], run[4 * i + 1], run[4 * i + 2], run[4 * i + 3]};
;             }
	v_max_f32_e32 v34, v36, v42
	v_max_f32_e32 v36, v37, v39
	v_max_f32_e32 v3, v3, v7
	v_max_f32_e32 v4, v47, v4
	v_max_f32_e32 v41, v44, v40
	v_max_f32_e32 v48, v50, v5
	v_min_f32_e32 v37, v34, v36
	v_min_f32_e32 v7, v3, v4
	v_max_f32_e32 v54, v46, v53
	v_min_f32_e32 v51, v41, v48
	v_min_f32_e32 v39, v37, v7
	v_min_f32_e32 v40, v44, v40
	v_min_f32_e32 v5, v50, v5
	v_min_f32_e32 v52, v54, v51
	v_min_f32_e32 v45, v35, v6
	v_min_f32_e32 v42, v2, v39
	v_min_f32_e32 v44, v40, v5
	v_max_f32_e32 v34, v34, v36
	v_max_f32_e32 v3, v3, v4
	v_max_f32_e32 v32, v32, v33
	v_max_f32_e32 v0, v0, v1
	v_min_f32_e32 v49, v52, v45
	v_max_f32_e32 v45, v52, v45
	v_min_f32_e32 v47, v42, v44
	v_max_f32_e32 v6, v35, v6
	v_min_f32_e32 v4, v34, v3
	v_max_f32_e32 v5, v40, v5
	v_min_f32_e32 v1, v32, v0
	v_min_f32_e32 v43, v49, v38
	v_max_f32_e32 v38, v49, v38
	v_min_f32_e32 v49, v45, v47
	v_max_f32_e32 v45, v45, v47
	v_max_f32_e32 v47, v54, v51
	v_min_f32_e32 v35, v6, v4
	v_max_f32_e32 v2, v2, v39
	v_min_f32_e32 v33, v5, v1
	v_min_f32_e32 v36, v47, v35
	v_max_f32_e32 v35, v47, v35
	v_min_f32_e32 v39, v2, v33
	v_min_f32_e32 v40, v35, v39
	v_max_f32_e32 v35, v35, v39
	v_max_f32_e32 v39, v41, v48
	v_max_f32_e32 v4, v6, v4
	v_min_f32_e32 v6, v39, v4
	v_max_f32_e32 v2, v2, v33
	v_min_f32_e32 v33, v6, v2
	v_max_f32_e32 v2, v6, v2
	v_max_f32_e32 v6, v37, v7
	v_max_f32_e32 v1, v5, v1
	v_max_f32_e32 v42, v42, v44
	v_max_f32_e32 v4, v39, v4
	v_min_f32_e32 v5, v6, v1
	v_max_f32_e32 v3, v34, v3
	v_max_f32_e32 v1, v6, v1
	v_min_f32_e32 v27, v9, v8
	v_min_f32_e32 v28, v10, v18
	v_min_f32_e32 v29, v11, v19
	v_min_f32_e32 v30, v20, v22
	v_min_f32_e32 v31, v21, v23
	v_min_f32_e32 v44, v36, v42
	v_max_f32_e32 v36, v36, v42
	v_min_f32_e32 v7, v4, v5
	v_max_f32_e32 v4, v4, v5
	v_min_f32_e32 v5, v3, v1
	v_max_f32_e32 v1, v3, v1
	v_min_f32_e32 v3, v46, v53
	v_max3_f32 v3, v17, v14, v3
	v_max_f32_e32 v6, v24, v43
	v_max3_f32 v12, v12, v13, v38
	v_max_f32_e32 v13, v25, v49
	v_max3_f32 v14, v16, v15, v45
	v_max_f32_e32 v15, v26, v44
	v_max3_f32 v8, v9, v8, v36
	v_max_f32_e32 v9, v27, v40
	v_max3_f32 v10, v10, v18, v35
	v_max_f32_e32 v16, v28, v33
	v_max3_f32 v2, v11, v19, v2
	v_max_f32_e32 v7, v29, v7
	v_max3_f32 v4, v20, v22, v4
	v_max_f32_e32 v5, v30, v5
	v_max3_f32 v1, v21, v23, v1
	v_max3_f32 v0, v31, v32, v0
	v_max_f32_e32 v11, v3, v10
	v_min_f32_e32 v3, v3, v10
	v_max_f32_e32 v10, v6, v16
	v_min_f32_e32 v6, v6, v16
	v_max_f32_e32 v16, v12, v2
	v_min_f32_e32 v2, v12, v2
	v_max_f32_e32 v12, v13, v7
	v_min_f32_e32 v7, v13, v7
	v_max_f32_e32 v13, v14, v4
	v_min_f32_e32 v4, v14, v4
	v_max_f32_e32 v14, v15, v5
	v_min_f32_e32 v5, v15, v5
	v_max_f32_e32 v15, v8, v1
	v_min_f32_e32 v1, v8, v1
	v_max_f32_e32 v8, v9, v0
	v_min_f32_e32 v0, v9, v0
	v_max_f32_e32 v9, v11, v13
	v_min_f32_e32 v11, v11, v13
	v_max_f32_e32 v13, v10, v14
	v_min_f32_e32 v10, v10, v14
	v_max_f32_e32 v14, v16, v15
	v_min_f32_e32 v15, v16, v15
	v_max_f32_e32 v16, v12, v8
	v_min_f32_e32 v8, v12, v8
	v_max_f32_e32 v12, v3, v4
	v_min_f32_e32 v3, v3, v4
	v_max_f32_e32 v4, v6, v5
	v_min_f32_e32 v5, v6, v5
	v_max_f32_e32 v6, v2, v1
	v_min_f32_e32 v1, v2, v1
	v_max_f32_e32 v2, v7, v0
	v_min_f32_e32 v0, v7, v0
	s_waitcnt lgkmcnt(0)
	s_barrier
	v_max_f32_e32 v7, v9, v14
	v_min_f32_e32 v9, v9, v14
	v_max_f32_e32 v14, v13, v16
	v_min_f32_e32 v16, v13, v16
	v_max_f32_e32 v17, v11, v15
	v_min_f32_e32 v11, v11, v15
	v_max_f32_e32 v18, v10, v8
	v_min_f32_e32 v19, v10, v8
	v_max_f32_e32 v20, v12, v6
	v_min_f32_e32 v21, v12, v6
	v_max_f32_e32 v6, v4, v2
	v_min_f32_e32 v2, v4, v2
	v_max_f32_e32 v22, v3, v1
	v_min_f32_e32 v3, v3, v1
	v_max_f32_e32 v1, v5, v0
	v_min_f32_e32 v23, v5, v0
	v_max_f32_e32 v12, v7, v14
	v_min_f32_e32 v13, v7, v14
	v_max_f32_e32 v14, v9, v16
	v_min_f32_e32 v15, v9, v16
	v_max_f32_e32 v8, v17, v18
	v_min_f32_e32 v9, v17, v18
	v_max_f32_e32 v10, v11, v19
	v_min_f32_e32 v11, v11, v19
	v_max_f32_e32 v4, v20, v6
	v_min_f32_e32 v5, v20, v6
	v_max_f32_e32 v6, v21, v2
	v_min_f32_e32 v7, v21, v2
	v_max_f32_e32 v0, v22, v1
	v_min_f32_e32 v1, v22, v1
	v_max_f32_e32 v2, v3, v23
	v_min_f32_e32 v3, v3, v23
	s_cbranch_vccnz .LBB0_604
	ds_write_b128 v97, v[12:15]
	ds_write_b128 v97, v[8:11] offset:16
	ds_write_b128 v97, v[4:7] offset:32
	ds_write_b128 v97, v[0:3] offset:48
; #define PG8_LAS __attribute__((address_space(3)))
;     __device__ __forceinline__ void fused(f32x4 (&acc)[2][2][4][2], const Unit& u, int wr, int wc, int fr, int fq, PG8_LAS unsigned char* lds, int wid, int lane) const {
;     ...
;             if (half == 0) {
;                 float nw[16];
; #pragma unroll
;                 for (int i = 0; i < 4; ++i) { const f32x4 v = *(const PG8_LAS f32x4*)(tile + row * 16 + 4 * i); nw[4 * i] = v[0]; nw[4 * i + 1] = v[1]; nw[4 * i + 2] = v[2]; nw[4 * i + 3] = v[3]; }
;                 merge_top16(run, nw);
;             }
; #pragma unroll
;             for (int q = 0; q < 16; ++q) { if (bj == 0) top0[q] = run[q]; else top1[q] = run[q]; }
;             RT_BAR();
;         }
;         if (half == 0) {
;             PG8_LAS int* idxl = (PG8_LAS int*)(lds + 65536) + row * 32;
;             float v0[16], v1[16];
; #pragma unroll
;             for (int q = 0; q < 16; ++q) { const unsigned b0 = __float_as_uint(top0[q]), b1 = __float_as_uint(top1[q]);
;                 v0[q] = __uint_as_float(b0 & ~127u); v1[q] = __uint_as_float(b1 & ~127u); idxl[q] = (int)(b0 & 127u); idxl[16 + q] = (int)(b1 & 127u); }
;             float best[16];
;             { float cv[16]; cv[0] = __uint_as_float((__float_as_uint(v0[0] + v1[0]) & ~255u) | 0u); cv[1] = __uint_as_float((__float_as_uint(v0[0] + v1[1]) & ~255u) | 1u); cv[2] = __uint_as_float((__float_as_uint(v0[0] + v1[2]) & ~255u) | 2u); cv[3] = __uint_as_float((__float_as_uint(v0[0] + v1[3]) & ~255u) | 3u); cv[4] = __uint_as_float((__float_as_uint(v0[0] + v1[4]) & ~255u) | 4u); cv[5] = __uint_as_float((__float_as_uint(v0[0] + v1[5]) & ~255u) | 5u); cv[6] = __uint_as_float((__float_as_uint(v0[0] + v1[6]) & ~255u) | 6u); cv[7] = __uint_as_float((__float_as_uint(v0[0] + v1[7]) & ~255u) | 7u); cv[8] = __uint_as_float((__float_as_uint(v0[0] + v1[8]) & ~255u) | 8u); cv[9] = __uint_as_float((__float_as_uint(v0[0] + v1[9]) & ~255u) | 9u); cv[10] = __uint_as_float((__float_as_uint(v0[0] + v1[10]) & ~255u) | 10u); cv[11] = __uint_as_float((__float_as_uint(v0[0] + v1[11]) & ~255u) | 11u); cv[12] = __uint_as_float((__float_as_uint(v0[0] + v1[12]) & ~255u) | 12u); cv[13] = __uint_as_float((__float_as_uint(v0[0] + v1[13]) & ~255u) | 13u); cv[14] = __uint_as_float((__float_as_uint(v0[0] + v1[14]) & ~255u) | 14u); cv[15] = __uint_as_float((__float_as_uint(v0[0] + v1[15]) & ~255u) | 15u); sort16_desc(cv);
.LBB0_604:
	s_waitcnt lgkmcnt(0)
	s_barrier
	v_cndmask_b32_e64 v16, 0, 1, s[14:15]
	v_cmp_ne_u32_e64 s[4:5], 1, v16
	s_andn2_b64 vcc, exec, s[14:15]
	s_cbranch_vccnz .LBB0_606
	ds_read_b128 v[16:19], v97 offset:48
	ds_read_b128 v[20:23], v97 offset:32
	ds_read_b128 v[24:27], v97
	ds_read_b128 v[28:31], v97 offset:16
	s_waitcnt lgkmcnt(0)
	v_max_f32_e32 v15, v15, v16
	v_max_f32_e32 v16, v23, v23
	v_max_f32_e32 v8, v8, v16
	v_max_f32_e32 v16, v22, v22
	v_max_f32_e32 v9, v9, v16
	v_max_f32_e32 v16, v21, v21
	v_max_f32_e32 v10, v10, v16
	v_max_f32_e32 v16, v20, v20
	v_max_f32_e32 v11, v11, v16
	v_max_f32_e32 v16, v31, v31
	v_max_f32_e32 v4, v4, v16
	v_max_f32_e32 v16, v30, v30
	v_max_f32_e32 v5, v5, v16
	v_max_f32_e32 v16, v29, v29
	v_max_f32_e32 v6, v6, v16
	v_max_f32_e32 v16, v28, v28
	v_max_f32_e32 v7, v7, v16
	v_max_f32_e32 v16, v27, v27
	v_max_f32_e32 v0, v0, v16
	v_max_f32_e32 v16, v26, v26
	v_max_f32_e32 v1, v1, v16
	v_max_f32_e32 v16, v25, v25
	v_max_f32_e32 v2, v2, v16
	v_max_f32_e32 v16, v24, v24
	v_max_f32_e32 v12, v12, v19
	v_max_f32_e32 v13, v13, v18
	v_max_f32_e32 v14, v14, v17
	v_max_f32_e32 v3, v3, v16
	v_max_f32_e32 v16, v12, v4
	v_min_f32_e32 v4, v12, v4
	v_max_f32_e32 v12, v13, v5
	v_min_f32_e32 v5, v13, v5
	v_max_f32_e32 v13, v14, v6
	v_min_f32_e32 v6, v14, v6
	v_max_f32_e32 v14, v15, v7
	v_min_f32_e32 v7, v15, v7
	v_max_f32_e32 v15, v8, v0
	v_min_f32_e32 v0, v8, v0
	v_max_f32_e32 v8, v9, v1
	v_min_f32_e32 v1, v9, v1
	v_max_f32_e32 v9, v10, v2
	v_min_f32_e32 v2, v10, v2
	v_max_f32_e32 v10, v11, v3
	v_min_f32_e32 v3, v11, v3
	v_max_f32_e32 v11, v16, v15
	v_min_f32_e32 v15, v16, v15
	v_max_f32_e32 v16, v12, v8
	v_min_f32_e32 v8, v12, v8
	v_max_f32_e32 v12, v13, v9
	v_min_f32_e32 v9, v13, v9
	v_max_f32_e32 v13, v14, v10
	v_min_f32_e32 v10, v14, v10
	v_max_f32_e32 v14, v4, v0
	v_min_f32_e32 v0, v4, v0
	v_max_f32_e32 v4, v5, v1
	v_min_f32_e32 v1, v5, v1
	v_max_f32_e32 v5, v6, v2
	v_min_f32_e32 v2, v6, v2
	v_max_f32_e32 v6, v7, v3
	v_min_f32_e32 v3, v7, v3
	v_max_f32_e32 v7, v11, v12
	v_min_f32_e32 v11, v11, v12
	v_max_f32_e32 v17, v16, v13
	v_min_f32_e32 v16, v16, v13
	v_max_f32_e32 v18, v15, v9
	v_min_f32_e32 v19, v15, v9
	v_max_f32_e32 v9, v8, v10
	v_min_f32_e32 v20, v8, v10
	v_max_f32_e32 v21, v14, v5
	v_min_f32_e32 v22, v14, v5
	v_max_f32_e32 v5, v4, v6
	v_min_f32_e32 v23, v4, v6
	v_max_f32_e32 v24, v0, v2
	v_min_f32_e32 v25, v0, v2
	v_max_f32_e32 v2, v1, v3
	v_min_f32_e32 v3, v1, v3
	v_max_f32_e32 v12, v7, v17
	v_min_f32_e32 v13, v7, v17
	v_max_f32_e32 v14, v11, v16
	v_min_f32_e32 v15, v11, v16
	v_max_f32_e32 v8, v18, v9
	v_min_f32_e32 v9, v18, v9
	v_max_f32_e32 v10, v19, v20
	v_min_f32_e32 v11, v19, v20
	v_max_f32_e32 v4, v21, v5
	v_min_f32_e32 v5, v21, v5
	v_max_f32_e32 v6, v22, v23
	v_min_f32_e32 v7, v22, v23
	v_max_f32_e32 v0, v24, v2
	v_min_f32_e32 v1, v24, v2
	v_max_f32_e32 v2, v25, v3
	v_min_f32_e32 v3, v25, v3
.LBB0_606:
	s_waitcnt lgkmcnt(0)
	s_barrier
	s_and_b64 vcc, exec, s[4:5]
	s_cbranch_vccnz .LBB0_608
	v_lshl_add_u32 v16, v128, 7, 0
	v_add_u32_e32 v16, 0x10000, v16
	v_and_b32_e32 v17, 0xffffff80, v12
	v_and_b32_e32 v18, 0xffffff80, v13
	v_and_b32_e32 v21, 0x7f, v77
	v_and_b32_e32 v20, 0x7f, v76
	v_and_b32_e32 v13, 0x7f, v13
	v_and_b32_e32 v12, 0x7f, v12
	v_and_b32_e32 v26, 0xffffff80, v14
	v_and_b32_e32 v28, 0xffffff80, v15
	v_and_b32_e32 v23, 0x7f, v79
	v_and_b32_e32 v22, 0x7f, v78
	v_and_b32_e32 v15, 0x7f, v15
	v_and_b32_e32 v14, 0x7f, v14
	ds_write_b128 v16, v[20:23]
	ds_write_b128 v16, v[12:15] offset:64
	v_and_b32_e32 v21, 0xffffff80, v8
	v_and_b32_e32 v23, 0xffffff80, v9
	v_and_b32_e32 v13, 0x7f, v73
	v_and_b32_e32 v12, 0x7f, v72
	v_and_b32_e32 v9, 0x7f, v9
	v_and_b32_e32 v8, 0x7f, v8
	v_and_b32_e32 v30, 0xffffff80, v10
	v_and_b32_e32 v32, 0xffffff80, v11
	v_and_b32_e32 v15, 0x7f, v75
	v_and_b32_e32 v14, 0x7f, v74
	v_and_b32_e32 v11, 0x7f, v11
	v_and_b32_e32 v10, 0x7f, v10
	v_and_b32_e32 v19, 0xffffff80, v76
	ds_write_b128 v16, v[12:15] offset:16
	ds_write_b128 v16, v[8:11] offset:80
	v_and_b32_e32 v13, 0xffffff80, v4
	v_and_b32_e32 v15, 0xffffff80, v5
	v_and_b32_e32 v9, 0x7f, v69
	v_and_b32_e32 v8, 0x7f, v68
	v_and_b32_e32 v5, 0x7f, v5
	v_and_b32_e32 v4, 0x7f, v4
	v_and_b32_e32 v34, 0xffffff80, v6
	v_and_b32_e32 v36, 0xffffff80, v7
	v_and_b32_e32 v11, 0x7f, v71
	v_and_b32_e32 v10, 0x7f, v70
	v_and_b32_e32 v7, 0x7f, v7
	v_and_b32_e32 v6, 0x7f, v6
	ds_write_b128 v16, v[8:11] offset:32
	ds_write_b128 v16, v[4:7] offset:96
	v_and_b32_e32 v5, 0x7f, v65
	v_and_b32_e32 v4, 0x7f, v64
	v_and_b32_e32 v41, 0xffffff80, v2
	v_and_b32_e32 v42, 0xffffff80, v3
	v_and_b32_e32 v7, 0x7f, v67
	v_and_b32_e32 v6, 0x7f, v66
	v_and_b32_e32 v11, 0x7f, v3
	v_and_b32_e32 v10, 0x7f, v2
	v_add_f32_e32 v2, v19, v17
	s_movk_i32 s3, 0xff00
	v_add_f32_e32 v3, v19, v18
	v_and_b32_e32 v24, 0xffffff80, v77
	ds_write_b128 v16, v[4:7] offset:48
	v_and_b32_e32 v2, 0xffffff00, v2
	v_and_or_b32 v3, v3, s3, 1
	v_add_f32_e32 v4, v19, v26
	v_add_f32_e32 v5, v19, v28
	v_and_b32_e32 v40, 0xffffff80, v1
	v_and_b32_e32 v9, 0x7f, v1
	v_and_b32_e32 v8, 0x7f, v0
	v_and_or_b32 v4, v4, s3, 2
	v_and_or_b32 v5, v5, s3, 3
	v_add_f32_e32 v48, v24, v17
	v_add_f32_e32 v49, v24, v18
	ds_write_b128 v16, v[8:11] offset:112
	v_add_f32_e32 v6, v19, v21
	v_add_f32_e32 v7, v19, v23
	v_add_f32_e32 v11, v19, v15
	v_add_f32_e32 v15, v19, v36
	v_add_f32_e32 v36, v19, v40
	v_max_f32_e32 v40, v2, v3
	v_min_f32_e32 v2, v2, v3
	v_max_f32_e32 v3, v5, v5
	v_and_or_b32 v48, v48, s3, 16
	v_and_or_b32 v49, v49, s3, 17
	v_add_f32_e32 v50, v24, v26
	v_add_f32_e32 v51, v24, v28
	v_and_or_b32 v6, v6, s3, 4
	v_and_or_b32 v7, v7, s3, 5
	v_add_f32_e32 v8, v19, v30
	v_add_f32_e32 v9, v19, v32
;     __device__ __forceinline__ void fused(f32x4 (&acc)[2][2][4][2], const Unit& u, int wr, int wc, int fr, int fq, PG8_LAS unsigned char* lds, int wid, int lane) const {
;     ...
;             { float cv[16]; cv[0] = __uint_as_float((__float_as_uint(v0[0] + v1[0]) & ~255u) | 0u); cv[1] = __uint_as_float((__float_as_uint(v0[0] + v1[1]) & ~255u) | 1u); cv[2] = __uint_as_float((__float_as_uint(v0[0] + v1[2]) & ~255u) | 2u); cv[3] = __uint_as_float((__float_as_uint(v0[0] + v1[3]) & ~255u) | 3u); cv[4] = __uint_as_float((__float_as_uint(v0[0] + v1[4]) & ~255u) | 4u); cv[5] = __uint_as_float((__float_as_uint(v0[0] + v1[5]) & ~255u) | 5u); cv[6] = __uint_as_float((__float_as_uint(v0[0] + v1[6]) & ~255u) | 6u); cv[7] = __uint_as_float((__float_as_uint(v0[0] + v1[7]) & ~255u) | 7u); cv[8] = __uint_as_float((__float_as_uint(v0[0] + v1[8]) & ~255u) | 8u); cv[9] = __uint_as_float((__float_as_uint(v0[0] + v1[9]) & ~255u) | 9u); cv[10] = __uint_as_float((__float_as_uint(v0[0] + v1[10]) & ~255u) | 10u); cv[11] = __uint_as_float((__float_as_uint(v0[0] + v1[11]) & ~255u) | 11u); cv[12] = __uint_as_float((__float_as_uint(v0[0] + v1[12]) & ~255u) | 12u); cv[13] = __uint_as_float((__float_as_uint(v0[0] + v1[13]) & ~255u) | 13u); cv[14] = __uint_as_float((__float_as_uint(v0[0] + v1[14]) & ~255u) | 14u); cv[15] = __uint_as_float((__float_as_uint(v0[0] + v1[15]) & ~255u) | 15u); sort16_desc(cv);
; #pragma unroll
;               for (int q = 0; q < 16; ++q) best[q] = cv[q]; }
	v_max_f32_e32 v5, v4, v3
	v_min_f32_e32 v3, v4, v3
	v_and_or_b32 v50, v50, s3, 18
	v_and_or_b32 v51, v51, s3, 19
	v_and_or_b32 v8, v8, s3, 6
	v_and_or_b32 v9, v9, s3, 7
	v_max_f32_e32 v4, v40, v5
	v_min_f32_e32 v5, v40, v5
	v_max_f32_e32 v40, v2, v3
	v_add_f32_e32 v52, v24, v21
	v_add_f32_e32 v23, v24, v23
	v_add_f32_e32 v30, v24, v30
	v_add_f32_e32 v24, v24, v32
	v_max_f32_e32 v58, v48, v49
	v_min_f32_e32 v48, v48, v49
	v_max_f32_e32 v49, v51, v51
	v_min_f32_e32 v2, v2, v3
	v_max_f32_e32 v3, v40, v5
	v_min_f32_e32 v5, v40, v5
	v_max_f32_e32 v40, v6, v7
	v_min_f32_e32 v6, v6, v7
	v_max_f32_e32 v7, v9, v9
	v_and_or_b32 v52, v52, s3, 20
	v_and_or_b32 v23, v23, s3, 21
	v_and_or_b32 v30, v30, s3, 22
	v_and_or_b32 v24, v24, s3, 23
	v_max_f32_e32 v51, v50, v49
	v_min_f32_e32 v49, v50, v49
	v_max_f32_e32 v9, v8, v7
	v_min_f32_e32 v7, v8, v7
	v_max_f32_e32 v50, v58, v51
	v_min_f32_e32 v51, v58, v51
	v_max_f32_e32 v58, v48, v49
	v_max_f32_e32 v8, v40, v9
	v_min_f32_e32 v9, v40, v9
	v_max_f32_e32 v40, v6, v7
	v_min_f32_e32 v48, v48, v49
	v_max_f32_e32 v49, v58, v51
	v_min_f32_e32 v51, v58, v51
	v_max_f32_e32 v58, v52, v23
	v_min_f32_e32 v23, v52, v23
	v_max_f32_e32 v52, v30, v24
	v_min_f32_e32 v24, v30, v24
	v_min_f32_e32 v6, v6, v7
	v_max_f32_e32 v7, v40, v9
	v_min_f32_e32 v9, v40, v9
	v_max_f32_e32 v30, v58, v52
	v_min_f32_e32 v52, v58, v52
	v_max_f32_e32 v58, v23, v24
	v_max_f32_e32 v40, v4, v8
	v_min_f32_e32 v4, v4, v8
	v_max_f32_e32 v8, v5, v9
	v_min_f32_e32 v23, v23, v24
	v_max_f32_e32 v24, v58, v52
	v_min_f32_e32 v52, v58, v52
	v_and_b32_e32 v25, 0xffffff80, v78
	v_add_f32_e32 v10, v19, v13
	v_min_f32_e32 v5, v5, v9
	v_max_f32_e32 v9, v8, v4
	v_min_f32_e32 v4, v8, v4
	v_max_f32_e32 v8, v3, v7
	v_min_f32_e32 v3, v3, v7
	v_max_f32_e32 v7, v2, v6
	v_max_f32_e32 v58, v50, v30
	v_min_f32_e32 v30, v50, v30
	v_max_f32_e32 v50, v51, v52
	v_and_or_b32 v10, v10, s3, 8
	v_and_or_b32 v11, v11, s3, 9
	v_add_f32_e32 v13, v19, v34
	v_min_f32_e32 v2, v2, v6
	v_max_f32_e32 v6, v7, v3
	v_min_f32_e32 v3, v7, v3
	v_add_f32_e32 v32, v25, v17
	v_add_f32_e32 v53, v25, v18
	v_min_f32_e32 v51, v51, v52
	v_max_f32_e32 v52, v50, v30
	v_min_f32_e32 v30, v50, v30
	v_max_f32_e32 v50, v49, v24
	v_min_f32_e32 v24, v49, v24
	v_max_f32_e32 v49, v48, v23
	v_and_or_b32 v13, v13, s3, 10
	v_and_or_b32 v15, v15, s3, 11
	v_max_f32_e32 v7, v8, v9
	v_min_f32_e32 v8, v8, v9
	v_max_f32_e32 v9, v6, v4
	v_min_f32_e32 v4, v6, v4
	v_max_f32_e32 v6, v3, v5
	v_min_f32_e32 v3, v3, v5
	v_max_f32_e32 v5, v11, v11
	v_and_or_b32 v32, v32, s3, 32
	v_and_or_b32 v53, v53, s3, 33
	v_add_f32_e32 v54, v25, v26
	v_add_f32_e32 v55, v25, v28
	v_min_f32_e32 v23, v48, v23
	v_max_f32_e32 v48, v49, v24
	v_min_f32_e32 v24, v49, v24
	v_and_b32_e32 v27, 0xffffff80, v79
	v_and_b32_e32 v38, 0xffffff80, v0
	v_max_f32_e32 v11, v10, v5
	v_min_f32_e32 v5, v10, v5
	v_max_f32_e32 v10, v15, v15
	v_and_or_b32 v54, v54, s3, 34
	v_and_or_b32 v55, v55, s3, 35
	v_max_f32_e32 v49, v50, v52
	v_min_f32_e32 v50, v50, v52
	v_max_f32_e32 v52, v48, v30
	v_min_f32_e32 v30, v48, v30
	v_max_f32_e32 v48, v24, v51
	v_min_f32_e32 v24, v24, v51
	v_max_f32_e32 v51, v53, v53
	v_add_f32_e32 v34, v19, v38
	v_max_f32_e32 v15, v13, v10
	v_min_f32_e32 v10, v13, v10
	v_add_f32_e32 v21, v25, v21
	v_add_f32_e32 v25, v27, v17
	v_max_f32_e32 v53, v32, v51
	v_min_f32_e32 v32, v32, v51
	v_max_f32_e32 v51, v55, v55
	v_and_or_b32 v34, v34, s3, 12
	v_and_or_b32 v36, v36, s3, 13
	v_add_f32_e32 v38, v19, v41
	v_add_f32_e32 v19, v19, v42
	v_max_f32_e32 v13, v11, v15
	v_min_f32_e32 v11, v11, v15
	v_max_f32_e32 v15, v5, v10
	v_and_or_b32 v21, v21, s3, 36
	v_and_or_b32 v25, v25, s3, 48
	v_add_f32_e32 v56, v27, v18
	v_add_f32_e32 v57, v27, v26
	v_max_f32_e32 v55, v54, v51
	v_min_f32_e32 v51, v54, v51
	v_and_or_b32 v38, v38, s3, 14
	v_and_or_b32 v19, v19, s3, 15
	v_min_f32_e32 v5, v5, v10
	v_max_f32_e32 v10, v15, v11
	v_min_f32_e32 v11, v15, v11
	v_max_f32_e32 v15, v36, v36
	v_and_or_b32 v56, v56, s3, 49
	v_and_or_b32 v57, v57, s3, 50
	v_max_f32_e32 v54, v53, v55
	v_min_f32_e32 v53, v53, v55
	v_max_f32_e32 v55, v32, v51
	v_max_f32_e32 v36, v34, v15
	v_min_f32_e32 v15, v34, v15
	v_max_f32_e32 v34, v38, v38
	v_min_f32_e32 v32, v32, v51
	v_max_f32_e32 v51, v55, v53
	v_min_f32_e32 v53, v55, v53
	v_max_f32_e32 v55, v21, v25
	v_min_f32_e32 v21, v21, v25
	v_max_f32_e32 v25, v57, v57
	v_max_f32_e32 v38, v34, v19
	v_min_f32_e32 v19, v34, v19
	v_max_f32_e32 v57, v56, v25
	v_min_f32_e32 v25, v56, v25
	v_max_f32_e32 v34, v36, v38
	v_min_f32_e32 v36, v36, v38
	v_max_f32_e32 v38, v15, v19
	v_max_f32_e32 v56, v55, v57
	v_min_f32_e32 v55, v55, v57
	v_max_f32_e32 v57, v21, v25
	v_min_f32_e32 v15, v15, v19
	v_max_f32_e32 v19, v38, v36
	v_min_f32_e32 v36, v38, v36
	v_min_f32_e32 v21, v21, v25
	v_max_f32_e32 v25, v57, v55
	v_min_f32_e32 v55, v57, v55
	v_max_f32_e32 v38, v13, v34
	v_min_f32_e32 v13, v13, v34
	v_max_f32_e32 v34, v11, v36
	v_max_f32_e32 v57, v54, v56
	v_min_f32_e32 v54, v54, v56
	v_max_f32_e32 v56, v53, v55
	v_min_f32_e32 v11, v11, v36
	v_max_f32_e32 v36, v34, v13
	v_min_f32_e32 v13, v34, v13
	v_max_f32_e32 v34, v10, v19
	v_min_f32_e32 v10, v10, v19
	v_max_f32_e32 v19, v5, v15
	v_min_f32_e32 v53, v53, v55
	v_max_f32_e32 v55, v56, v54
	v_min_f32_e32 v54, v56, v54
	v_max_f32_e32 v56, v51, v25
	v_min_f32_e32 v25, v51, v25
	v_max_f32_e32 v51, v32, v21
	v_min_f32_e32 v5, v5, v15
	v_max_f32_e32 v15, v19, v10
	v_min_f32_e32 v21, v32, v21
	v_max_f32_e32 v32, v51, v25
	v_min_f32_e32 v10, v19, v10
	v_max_f32_e32 v19, v34, v36
	v_min_f32_e32 v34, v34, v36
	v_max_f32_e32 v36, v15, v13
	v_min_f32_e32 v13, v15, v13
	v_min_f32_e32 v25, v51, v25
	v_max_f32_e32 v51, v56, v55
;     __device__ __forceinline__ void fused(f32x4 (&acc)[2][2][4][2], const Unit& u, int wr, int wc, int fr, int fq, PG8_LAS unsigned char* lds, int wid, int lane) const {
;     ...
;             { float cv[16]; cv[0] = __uint_as_float((__float_as_uint(v0[1] + v1[0]) & ~255u) | 16u); cv[1] = __uint_as_float((__float_as_uint(v0[1] + v1[1]) & ~255u) | 17u); cv[2] = __uint_as_float((__float_as_uint(v0[1] + v1[2]) & ~255u) | 18u); cv[3] = __uint_as_float((__float_as_uint(v0[1] + v1[3]) & ~255u) | 19u); cv[4] = __uint_as_float((__float_as_uint(v0[1] + v1[4]) & ~255u) | 20u); cv[5] = __uint_as_float((__float_as_uint(v0[1] + v1[5]) & ~255u) | 21u); cv[6] = __uint_as_float((__float_as_uint(v0[1] + v1[6]) & ~255u) | 22u); cv[7] = __uint_as_float((__float_as_uint(v0[1] + v1[7]) & ~255u) | 23u); cv[8] = __uint_as_float((__float_as_uint(v0[2] + v1[0]) & ~255u) | 32u); cv[9] = __uint_as_float((__float_as_uint(v0[2] + v1[1]) & ~255u) | 33u); cv[10] = __uint_as_float((__float_as_uint(v0[2] + v1[2]) & ~255u) | 34u); cv[11] = __uint_as_float((__float_as_uint(v0[2] + v1[3]) & ~255u) | 35u); cv[12] = __uint_as_float((__float_as_uint(v0[2] + v1[4]) & ~255u) | 36u); cv[13] = __uint_as_float((__float_as_uint(v0[3] + v1[0]) & ~255u) | 48u); cv[14] = __uint_as_float((__float_as_uint(v0[3] + v1[1]) & ~255u) | 49u); cv[15] = __uint_as_float((__float_as_uint(v0[3] + v1[2]) & ~255u) | 50u); sort16_desc(cv); merge_top16(best, cv); }
	v_min_f32_e32 v55, v56, v55
	v_max_f32_e32 v56, v32, v54
	v_min_f32_e32 v32, v32, v54
	v_max_f32_e32 v15, v10, v11
	v_min_f32_e32 v10, v10, v11
	v_min_f32_e32 v11, v40, v38
	v_max_f32_e32 v41, v4, v13
	v_max_f32_e32 v54, v25, v53
	v_min_f32_e32 v25, v25, v53
	v_min_f32_e32 v53, v58, v57
	v_max_f32_e32 v59, v30, v32
	v_min_f32_e32 v4, v4, v13
	v_max_f32_e32 v13, v41, v11
	v_min_f32_e32 v11, v41, v11
	v_max_f32_e32 v41, v8, v34
	v_min_f32_e32 v8, v8, v34
	v_max_f32_e32 v34, v3, v10
	v_min_f32_e32 v30, v30, v32
	v_max_f32_e32 v32, v59, v53
	v_min_f32_e32 v53, v59, v53
	v_max_f32_e32 v59, v50, v55
	v_min_f32_e32 v50, v50, v55
	v_max_f32_e32 v55, v24, v25
	v_min_f32_e32 v3, v3, v10
	v_max_f32_e32 v10, v34, v8
	v_min_f32_e32 v8, v34, v8
	v_min_f32_e32 v24, v24, v25
	v_max_f32_e32 v25, v55, v50
	v_min_f32_e32 v50, v55, v50
	v_max_f32_e32 v34, v41, v13
	v_min_f32_e32 v13, v41, v13
	v_max_f32_e32 v41, v10, v11
	v_min_f32_e32 v10, v10, v11
	v_max_f32_e32 v11, v8, v4
	v_min_f32_e32 v4, v8, v4
	v_max_f32_e32 v8, v7, v19
	v_min_f32_e32 v7, v7, v19
	v_max_f32_e32 v19, v6, v15
	v_max_f32_e32 v55, v59, v32
	v_min_f32_e32 v32, v59, v32
	v_max_f32_e32 v59, v25, v53
	v_min_f32_e32 v25, v25, v53
	v_max_f32_e32 v53, v50, v30
	v_min_f32_e32 v30, v50, v30
	v_max_f32_e32 v50, v49, v51
	v_min_f32_e32 v49, v49, v51
	v_max_f32_e32 v51, v48, v54
	v_min_f32_e32 v6, v6, v15
	v_max_f32_e32 v15, v19, v7
	v_min_f32_e32 v7, v19, v7
	v_max_f32_e32 v19, v9, v36
	v_min_f32_e32 v9, v9, v36
	v_max_f32_e32 v36, v2, v5
	v_min_f32_e32 v48, v48, v54
	v_max_f32_e32 v54, v51, v49
	v_min_f32_e32 v49, v51, v49
	v_max_f32_e32 v51, v52, v56
	v_min_f32_e32 v52, v52, v56
	v_max_f32_e32 v56, v23, v21
	v_min_f32_e32 v2, v2, v5
	v_max_f32_e32 v5, v36, v9
	v_min_f32_e32 v9, v36, v9
	v_max_f32_e32 v36, v19, v15
	v_min_f32_e32 v21, v23, v21
	v_max_f32_e32 v23, v56, v52
	v_min_f32_e32 v52, v56, v52
	v_and_b32_e32 v20, 0xffffff80, v72
	v_min_f32_e32 v15, v19, v15
	v_max_f32_e32 v19, v5, v7
	v_min_f32_e32 v5, v5, v7
	v_max_f32_e32 v7, v9, v6
	v_min_f32_e32 v6, v9, v6
	v_min_f32_e32 v9, v8, v34
	v_min_f32_e32 v42, v36, v13
	v_max_f32_e32 v56, v51, v54
	v_min_f32_e32 v51, v51, v54
	v_max_f32_e32 v54, v23, v49
	v_min_f32_e32 v23, v23, v49
	v_max_f32_e32 v49, v52, v48
	v_min_f32_e32 v48, v52, v48
	v_and_b32_e32 v39, 0xffffff80, v65
	v_min_f32_e32 v65, v48, v24
	v_max3_f32 v9, v9, v48, v24
	v_max3_f32 v24, v42, v49, v30
	v_add_f32_e32 v27, v27, v28
	v_add_f32_e32 v28, v20, v17
	v_add_f32_e32 v42, v20, v18
	v_add_f32_e32 v20, v20, v26
	v_and_b32_e32 v22, 0xffffff80, v73
	v_and_or_b32 v27, v27, s3, 51
	v_and_or_b32 v28, v28, s3, 64
	v_and_b32_e32 v42, 0xffffff00, v42
	v_and_b32_e32 v20, 0xffffff00, v20
	v_and_b32_e32 v29, 0xffffff80, v74
	v_and_b32_e32 v31, 0xffffff80, v75
	v_and_b32_e32 v33, 0xffffff80, v70
	v_and_b32_e32 v35, 0xffffff80, v71
	v_and_b32_e32 v37, 0xffffff80, v64
	v_min_f32_e32 v43, v15, v41
	v_min_f32_e32 v44, v19, v10
	v_min_f32_e32 v62, v54, v25
	v_or_b32_e32 v42, 0x41, v42
	v_or_b32_e32 v20, 0x42, v20
	v_add_f32_e32 v26, v22, v17
	v_add_f32_e32 v22, v22, v18
	v_min_f32_e32 v63, v23, v53
	v_max3_f32 v23, v43, v23, v53
	v_max3_f32 v10, v19, v10, v62
	v_max3_f32 v19, v44, v54, v25
	v_and_b32_e32 v26, 0xffffff00, v26
	v_and_b32_e32 v22, 0xffffff00, v22
	v_add_f32_e32 v43, v29, v17
	v_add_f32_e32 v29, v29, v18
	v_add_f32_e32 v44, v31, v17
	v_add_f32_e32 v18, v31, v18
	v_add_f32_e32 v31, v33, v17
	v_add_f32_e32 v33, v35, v17
	v_add_f32_e32 v35, v37, v17
	v_add_f32_e32 v37, v39, v17
	v_max_f32_e32 v39, v27, v28
	v_min_f32_e32 v27, v27, v28
	v_max_f32_e32 v28, v42, v42
	v_or_b32_e32 v26, 0x50, v26
	v_or_b32_e32 v22, 0x51, v22
	v_and_b32_e32 v43, 0xffffff00, v43
	v_and_b32_e32 v29, 0xffffff00, v29
	v_max_f32_e32 v42, v28, v20
	v_min_f32_e32 v20, v28, v20
	v_or_b32_e32 v43, 0x60, v43
	v_or_b32_e32 v29, 0x61, v29
	v_max_f32_e32 v28, v39, v42
	v_min_f32_e32 v39, v39, v42
	v_max_f32_e32 v42, v27, v20
	v_min_f32_e32 v20, v27, v20
	v_max_f32_e32 v27, v42, v39
	v_min_f32_e32 v39, v42, v39
	v_max_f32_e32 v42, v26, v22
	v_min_f32_e32 v22, v26, v22
	v_max_f32_e32 v26, v29, v29
	v_max_f32_e32 v29, v43, v43
	v_max_f32_e32 v43, v29, v26
	v_min_f32_e32 v26, v29, v26
	v_max_f32_e32 v29, v42, v43
	v_min_f32_e32 v42, v42, v43
	v_max_f32_e32 v43, v22, v26
	v_and_b32_e32 v12, 0xffffff80, v68
	v_and_b32_e32 v14, 0xffffff80, v69
	v_min_f32_e32 v22, v22, v26
	v_max_f32_e32 v26, v43, v42
	v_min_f32_e32 v42, v43, v42
	v_add_f32_e32 v12, v12, v17
	v_add_f32_e32 v14, v14, v17
	v_max_f32_e32 v43, v28, v29
	v_min_f32_e32 v28, v28, v29
	v_max_f32_e32 v29, v39, v42
	v_and_b32_e32 v44, 0xffffff00, v44
	v_and_b32_e32 v18, 0xffffff00, v18
	v_and_b32_e32 v12, 0xffffff00, v12
	v_and_b32_e32 v14, 0xffffff00, v14
	v_min_f32_e32 v39, v39, v42
	v_max_f32_e32 v42, v29, v28
	v_min_f32_e32 v28, v29, v28
	v_max_f32_e32 v29, v27, v26
	v_min_f32_e32 v26, v27, v26
	v_max_f32_e32 v27, v20, v22
	v_or_b32_e32 v44, 0x70, v44
	v_or_b32_e32 v18, 0x71, v18
	v_or_b32_e32 v12, 0x80, v12
	v_or_b32_e32 v14, 0x90, v14
	v_min_f32_e32 v20, v20, v22
	v_max_f32_e32 v22, v27, v26
	v_min_f32_e32 v26, v27, v26
	v_and_b32_e32 v31, 0xffffff00, v31
	v_and_b32_e32 v33, 0xffffff00, v33
	v_max_f32_e32 v27, v29, v42
	v_min_f32_e32 v29, v29, v42
	v_max_f32_e32 v42, v22, v28
	v_min_f32_e32 v22, v22, v28
	v_max_f32_e32 v28, v26, v39
	v_min_f32_e32 v26, v26, v39
	v_max_f32_e32 v39, v44, v44
	v_or_b32_e32 v31, 0xa0, v31
	v_or_b32_e32 v33, 0xb0, v33
	v_and_b32_e32 v35, 0xffffff00, v35
	v_and_b32_e32 v37, 0xffffff00, v37
	v_max_f32_e32 v44, v39, v18
	v_min_f32_e32 v18, v39, v18
	v_max_f32_e32 v39, v12, v14
	v_min_f32_e32 v12, v12, v14
	v_or_b32_e32 v35, 0xc0, v35
; __device__ __forceinline__ void merge_top16(float (&v)[16], const float (&nw)[16]) {
;     __device__ __forceinline__ void fused(f32x4 (&acc)[2][2][4][2], const Unit& u, int wr, int wc, int fr, int fq, PG8_LAS unsigned char* lds, int wid, int lane) const {
;     ...
;             { float cv[16]; cv[0] = __uint_as_float((__float_as_uint(v0[3] + v1[3]) & ~255u) | 51u); cv[1] = __uint_as_float((__float_as_uint(v0[4] + v1[0]) & ~255u) | 64u); cv[2] = __uint_as_float((__float_as_uint(v0[4] + v1[1]) & ~255u) | 65u); cv[3] = __uint_as_float((__float_as_uint(v0[4] + v1[2]) & ~255u) | 66u); cv[4] = __uint_as_float((__float_as_uint(v0[5] + v1[0]) & ~255u) | 80u); cv[5] = __uint_as_float((__float_as_uint(v0[5] + v1[1]) & ~255u) | 81u); cv[6] = __uint_as_float((__float_as_uint(v0[6] + v1[0]) & ~255u) | 96u); cv[7] = __uint_as_float((__float_as_uint(v0[6] + v1[1]) & ~255u) | 97u); cv[8] = __uint_as_float((__float_as_uint(v0[7] + v1[0]) & ~255u) | 112u); cv[9] = __uint_as_float((__float_as_uint(v0[7] + v1[1]) & ~255u) | 113u); cv[10] = __uint_as_float((__float_as_uint(v0[8] + v1[0]) & ~255u) | 128u); cv[11] = __uint_as_float((__float_as_uint(v0[9] + v1[0]) & ~255u) | 144u); cv[12] = __uint_as_float((__float_as_uint(v0[10] + v1[0]) & ~255u) | 160u); cv[13] = __uint_as_float((__float_as_uint(v0[11] + v1[0]) & ~255u) | 176u); cv[14] = __uint_as_float((__float_as_uint(v0[12] + v1[0]) & ~255u) | 192u); cv[15] = __uint_as_float((__float_as_uint(v0[13] + v1[0]) & ~255u) | 208u); sort16_desc(cv); merge_top16(best, cv); }
;             { float cv[16]; cv[0] = __uint_as_float((__float_as_uint(v0[14] + v1[0]) & ~255u) | 224u); cv[1] = __uint_as_float((__float_as_uint(v0[15] + v1[0]) & ~255u) | 240u); cv[2] = -INFINITY; cv[3] = -INFINITY; cv[4] = -INFINITY; cv[5] = -INFINITY; cv[6] = -INFINITY; cv[7] = -INFINITY; cv[8] = -INFINITY; cv[9] = -INFINITY; cv[10] = -INFINITY; cv[11] = -INFINITY; cv[12] = -INFINITY; cv[13] = -INFINITY; cv[14] = -INFINITY; cv[15] = -INFINITY; sort16_desc(cv); merge_top16(best, cv); }
	v_or_b32_e32 v37, 0xd0, v37
	v_max_f32_e32 v14, v44, v39
	v_min_f32_e32 v39, v44, v39
	v_max_f32_e32 v44, v18, v12
	v_min_f32_e32 v12, v18, v12
	v_max_f32_e32 v18, v44, v39
	v_min_f32_e32 v39, v44, v39
	v_max_f32_e32 v44, v31, v33
	v_min_f32_e32 v31, v31, v33
	v_max_f32_e32 v33, v37, v37
	v_max_f32_e32 v37, v35, v33
	v_min_f32_e32 v33, v35, v33
	v_max_f32_e32 v35, v44, v37
	v_min_f32_e32 v37, v44, v37
	v_max_f32_e32 v44, v31, v33
	v_min_f32_e32 v31, v31, v33
	v_max_f32_e32 v33, v44, v37
	v_min_f32_e32 v37, v44, v37
	v_max_f32_e32 v44, v14, v35
	v_min_f32_e32 v14, v14, v35
	v_max_f32_e32 v35, v39, v37
	v_min_f32_e32 v37, v39, v37
	v_max_f32_e32 v39, v35, v14
	v_min_f32_e32 v14, v35, v14
	v_max_f32_e32 v35, v18, v33
	v_min_f32_e32 v18, v18, v33
	v_max_f32_e32 v33, v12, v31
	v_min_f32_e32 v12, v12, v31
	v_max_f32_e32 v31, v33, v18
	v_min_f32_e32 v45, v5, v11
	v_min_f32_e32 v61, v51, v59
	v_min_f32_e32 v18, v33, v18
	v_max_f32_e32 v33, v35, v39
	v_min_f32_e32 v35, v35, v39
	v_max_f32_e32 v39, v31, v14
	v_min_f32_e32 v14, v31, v14
	v_max3_f32 v5, v5, v11, v61
	v_max3_f32 v11, v45, v51, v59
	v_max_f32_e32 v31, v18, v37
	v_min_f32_e32 v18, v18, v37
	v_min_f32_e32 v37, v43, v44
	v_max_f32_e32 v45, v22, v14
	v_min_f32_e32 v14, v22, v14
	v_max_f32_e32 v22, v45, v37
	v_min_f32_e32 v37, v45, v37
	v_max_f32_e32 v45, v29, v35
	v_min_f32_e32 v29, v29, v35
	v_max_f32_e32 v35, v26, v18
	v_min_f32_e32 v46, v7, v4
	v_min_f32_e32 v47, v6, v3
	v_min_f32_e32 v52, v50, v55
	v_min_f32_e32 v60, v56, v32
	v_min_f32_e32 v64, v49, v30
	v_min_f32_e32 v18, v26, v18
	v_max_f32_e32 v26, v35, v29
	v_min_f32_e32 v29, v35, v29
	v_max3_f32 v21, v40, v38, v21
	v_max3_f32 v8, v8, v34, v65
	v_max3_f32 v13, v36, v13, v64
	v_max3_f32 v15, v15, v41, v63
	v_max3_f32 v4, v7, v4, v60
	v_max3_f32 v7, v46, v56, v32
	v_max3_f32 v3, v6, v3, v52
	v_max3_f32 v6, v47, v50, v55
	v_max3_f32 v2, v2, v58, v57
	v_max_f32_e32 v35, v45, v22
	v_min_f32_e32 v22, v45, v22
	v_max_f32_e32 v45, v26, v37
	v_min_f32_e32 v26, v26, v37
	v_max_f32_e32 v37, v29, v14
	v_min_f32_e32 v14, v29, v14
	v_max_f32_e32 v29, v27, v33
	v_min_f32_e32 v27, v27, v33
	v_max_f32_e32 v33, v28, v31
	v_max_f32_e32 v25, v21, v19
	v_min_f32_e32 v19, v21, v19
	v_max_f32_e32 v21, v8, v5
	v_min_f32_e32 v5, v8, v5
	v_max_f32_e32 v8, v9, v11
	v_min_f32_e32 v9, v9, v11
	v_max_f32_e32 v11, v13, v4
	v_min_f32_e32 v4, v13, v4
	v_max_f32_e32 v13, v24, v7
	v_min_f32_e32 v7, v24, v7
	v_max_f32_e32 v24, v15, v3
	v_min_f32_e32 v3, v15, v3
	v_max_f32_e32 v15, v23, v6
	v_min_f32_e32 v6, v23, v6
	v_max_f32_e32 v23, v10, v2
	v_min_f32_e32 v2, v10, v2
	v_min_f32_e32 v28, v28, v31
	v_max_f32_e32 v31, v33, v27
	v_min_f32_e32 v27, v33, v27
	v_max_f32_e32 v33, v42, v39
	v_min_f32_e32 v39, v42, v39
	v_max_f32_e32 v42, v20, v12
	v_max_f32_e32 v10, v25, v13
	v_min_f32_e32 v13, v25, v13
	v_max_f32_e32 v25, v21, v24
	v_min_f32_e32 v21, v21, v24
	v_max_f32_e32 v24, v8, v15
	v_min_f32_e32 v8, v8, v15
	v_max_f32_e32 v15, v11, v23
	v_min_f32_e32 v11, v11, v23
	v_max_f32_e32 v23, v19, v7
	v_min_f32_e32 v7, v19, v7
	v_max_f32_e32 v19, v5, v3
	v_min_f32_e32 v3, v5, v3
	v_max_f32_e32 v5, v9, v6
	v_min_f32_e32 v6, v9, v6
	v_max_f32_e32 v9, v4, v2
	v_min_f32_e32 v2, v4, v2
	v_min_f32_e32 v12, v20, v12
	v_max_f32_e32 v20, v42, v39
	v_min_f32_e32 v39, v42, v39
	v_and_b32_e32 v1, 0xffffff80, v66
	v_and_b32_e32 v0, 0xffffff80, v67
	v_max_f32_e32 v4, v10, v24
	v_min_f32_e32 v10, v10, v24
	v_max_f32_e32 v24, v25, v15
	v_min_f32_e32 v15, v25, v15
	v_max_f32_e32 v25, v13, v8
	v_min_f32_e32 v8, v13, v8
	v_max_f32_e32 v13, v21, v11
	v_min_f32_e32 v11, v21, v11
	v_max_f32_e32 v21, v23, v5
	v_min_f32_e32 v5, v23, v5
	v_max_f32_e32 v23, v19, v9
	v_min_f32_e32 v9, v19, v9
	v_max_f32_e32 v19, v7, v6
	v_min_f32_e32 v6, v7, v6
	v_max_f32_e32 v7, v3, v2
	v_min_f32_e32 v2, v3, v2
	v_max_f32_e32 v42, v33, v31
	v_min_f32_e32 v31, v33, v31
	v_max_f32_e32 v33, v20, v27
	v_min_f32_e32 v20, v20, v27
	v_max_f32_e32 v27, v39, v28
	v_min_f32_e32 v28, v39, v28
	v_min_f32_e32 v3, v4, v24
	v_min_f32_e32 v30, v10, v15
	v_min_f32_e32 v32, v25, v13
	v_min_f32_e32 v34, v8, v11
	v_min_f32_e32 v36, v21, v23
	v_min_f32_e32 v38, v5, v9
	v_min_f32_e32 v40, v19, v7
	v_min_f32_e32 v41, v6, v2
	v_max_f32_e32 v39, v29, v35
	v_min_f32_e32 v29, v29, v35
	v_max_f32_e32 v35, v42, v22
	v_min_f32_e32 v22, v42, v22
	v_max_f32_e32 v42, v31, v45
	v_min_f32_e32 v31, v31, v45
	v_max_f32_e32 v45, v33, v26
	v_min_f32_e32 v26, v33, v26
	v_max_f32_e32 v33, v20, v37
	v_min_f32_e32 v20, v20, v37
	v_max_f32_e32 v37, v27, v14
	v_min_f32_e32 v14, v27, v14
	v_max_f32_e32 v27, v28, v18
	v_min_f32_e32 v18, v28, v18
	v_add_f32_e32 v1, v1, v17
	v_add_f32_e32 v0, v0, v17
	v_max3_f32 v4, v4, v24, v12
	v_max_f32_e32 v3, v3, v18
	v_max3_f32 v10, v10, v15, v27
	v_max_f32_e32 v12, v30, v14
	v_max3_f32 v13, v25, v13, v37
	v_max_f32_e32 v14, v32, v20
	v_max3_f32 v8, v8, v11, v33
	v_max_f32_e32 v11, v34, v26
	v_max3_f32 v15, v21, v23, v45
	v_max_f32_e32 v18, v36, v31
	v_max3_f32 v5, v5, v9, v42
	v_max_f32_e32 v9, v38, v22
	v_max3_f32 v7, v19, v7, v35
	v_max_f32_e32 v19, v40, v29
	v_max3_f32 v2, v6, v2, v39
	v_max3_f32 v6, v41, v43, v44
	v_and_b32_e32 v1, 0xffffff00, v1
	v_and_b32_e32 v0, 0xffffff00, v0
	v_max_f32_e32 v20, v4, v15
	v_min_f32_e32 v4, v4, v15
	v_max_f32_e32 v15, v3, v18
	v_min_f32_e32 v3, v3, v18
	v_max_f32_e32 v18, v10, v5
	v_min_f32_e32 v5, v10, v5
	v_max_f32_e32 v10, v12, v9
	v_min_f32_e32 v9, v12, v9
	v_max_f32_e32 v12, v13, v7
	v_min_f32_e32 v7, v13, v7
	v_max_f32_e32 v13, v14, v19
	v_min_f32_e32 v14, v14, v19
	v_max_f32_e32 v19, v8, v2
	v_min_f32_e32 v2, v8, v2
	v_max_f32_e32 v8, v11, v6
	v_min_f32_e32 v6, v11, v6
; #define RT_PK(q_) (ex[q_] | (int)((__float_as_uint(usc[ex[q_]]) >> 23) << 14))
;     __device__ __forceinline__ void fused(f32x4 (&acc)[2][2][4][2], const Unit& u, int wr, int wc, int fr, int fq, PG8_LAS unsigned char* lds, int wid, int lane) const {
;     ...
;             { float cv[16]; cv[0] = __uint_as_float((__float_as_uint(v0[14] + v1[0]) & ~255u) | 224u); cv[1] = __uint_as_float((__float_as_uint(v0[15] + v1[0]) & ~255u) | 240u); cv[2] = -INFINITY; cv[3] = -INFINITY; cv[4] = -INFINITY; cv[5] = -INFINITY; cv[6] = -INFINITY; cv[7] = -INFINITY; cv[8] = -INFINITY; cv[9] = -INFINITY; cv[10] = -INFINITY; cv[11] = -INFINITY; cv[12] = -INFINITY; cv[13] = -INFINITY; cv[14] = -INFINITY; cv[15] = -INFINITY; sort16_desc(cv); merge_top16(best, cv); }
;             float sc[16], sum = 0.f;
; #pragma unroll
;             for (int q = 0; q < 16; ++q) { sc[q] = __uint_as_float(__float_as_uint(best[q]) & ~255u); }
;             const float smax = sc[0];
; #pragma unroll
;             for (int q = 0; q < 16; ++q) { sc[q] = __builtin_amdgcn_exp2f((sc[q] - smax) * 1.4426950408889634f); }
; #pragma unroll
;             for (int q = 0; q < 16; ++q) sum += sc[q];
;             const float rs = 1.0f / sum;
;             asm volatile("s_waitcnt lgkmcnt(0)" ::: "memory");
;             int ex[16];
; #pragma unroll
;             for (int q = 0; q < 16; ++q) { const unsigned cid = __float_as_uint(best[q]) & 255u; ex[q] = idxl[cid >> 4] * 128 + idxl[16 + (cid & 15u)]; }
;             const size_t o = ((size_t)u.pn * 16384 + (size_t)(u.pm * BM + row)) * 16;
;             typedef int i32x4 __attribute__((ext_vector_type(4)));
; #pragma unroll
;             for (int i = 0; i < 4; ++i) {
;     ...
;                 *(i32x4*)(eidx + o + 4 * i) = (i32x4){RT_PK(4 * i), RT_PK(4 * i + 1), RT_PK(4 * i + 2), RT_PK(4 * i + 3)};
;                 *(f32x4*)(egate + o + 4 * i) = (f32x4){sc[4 * i] * rs * vsc[ex[4 * i]], sc[4 * i + 1] * rs * vsc[ex[4 * i + 1]], sc[4 * i + 2] * rs * vsc[ex[4 * i + 2]], sc[4 * i + 3] * rs * vsc[ex[4 * i + 3]]};
	v_or_b32_e32 v1, 0xe0, v1
	v_or_b32_e32 v0, 0xf0, v0
	v_max_f32_e32 v11, v20, v12
	v_min_f32_e32 v12, v20, v12
	v_max_f32_e32 v20, v15, v13
	v_min_f32_e32 v13, v15, v13
	v_max_f32_e32 v15, v18, v19
	v_min_f32_e32 v18, v18, v19
	v_max_f32_e32 v19, v10, v8
	v_min_f32_e32 v8, v10, v8
	v_max_f32_e32 v10, v4, v7
	v_min_f32_e32 v4, v4, v7
	v_max_f32_e32 v7, v3, v14
	v_min_f32_e32 v3, v3, v14
	v_max_f32_e32 v14, v5, v2
	v_min_f32_e32 v2, v5, v2
	v_max_f32_e32 v5, v9, v6
	v_min_f32_e32 v6, v9, v6
	v_max_f32_e32 v9, v11, v15
	v_min_f32_e32 v11, v11, v15
	v_max_f32_e32 v15, v20, v19
	v_min_f32_e32 v19, v20, v19
	v_max_f32_e32 v20, v12, v18
	v_min_f32_e32 v12, v12, v18
	v_max_f32_e32 v18, v13, v8
	v_min_f32_e32 v8, v13, v8
	v_max_f32_e32 v13, v10, v14
	v_min_f32_e32 v10, v10, v14
	v_max_f32_e32 v14, v7, v5
	v_min_f32_e32 v5, v7, v5
	v_max_f32_e32 v7, v4, v2
	v_min_f32_e32 v2, v4, v2
	v_max_f32_e32 v4, v3, v6
	v_min_f32_e32 v3, v3, v6
	v_max_f32_e32 v17, v1, v0
	v_min_f32_e32 v0, v1, v0
	v_min_f32_e32 v6, v9, v15
	v_min_f32_e32 v21, v11, v19
	v_min_f32_e32 v22, v20, v18
	v_min_f32_e32 v23, v12, v8
	v_min_f32_e32 v24, v13, v14
	v_min_f32_e32 v25, v10, v5
	v_min_f32_e32 v26, v7, v4
	v_min_f32_e32 v27, v2, v3
	s_mov_b32 s3, 0xff800000
	v_max_f32_e32 v0, 0xff800000, v0
	v_max3_f32 v1, v9, v15, s3
	v_max_f32_e32 v6, 0xff800000, v6
	v_max3_f32 v9, v11, v19, s3
	v_max_f32_e32 v11, 0xff800000, v21
	v_max3_f32 v15, v20, v18, s3
	v_max_f32_e32 v18, 0xff800000, v22
	v_max3_f32 v8, v12, v8, s3
	v_max_f32_e32 v12, 0xff800000, v23
	v_max3_f32 v13, v13, v14, s3
	v_max_f32_e32 v14, 0xff800000, v24
	v_max3_f32 v5, v10, v5, s3
	v_max_f32_e32 v10, 0xff800000, v25
	v_max3_f32 v4, v7, v4, s3
	v_max_f32_e32 v7, 0xff800000, v26
	v_max3_f32 v0, v2, v3, v0
	v_max3_f32 v2, v27, v17, s3
	v_max_f32_e32 v3, v1, v13
	v_min_f32_e32 v1, v1, v13
	v_max_f32_e32 v13, v6, v14
	v_min_f32_e32 v6, v6, v14
	v_max_f32_e32 v14, v9, v5
	v_min_f32_e32 v5, v9, v5
	v_max_f32_e32 v9, v11, v10
	v_min_f32_e32 v10, v11, v10
	v_max_f32_e32 v11, v15, v4
	v_min_f32_e32 v4, v15, v4
	v_max_f32_e32 v15, v18, v7
	v_max_f32_e32 v17, v8, v0
	v_min_f32_e32 v0, v8, v0
	v_max_f32_e32 v8, v12, v2
	v_min_f32_e32 v2, v12, v2
	v_max_f32_e32 v12, v3, v11
	v_min_f32_e32 v3, v3, v11
	v_max_f32_e32 v11, v13, v15
	v_min_f32_e32 v13, v13, v15
	v_max_f32_e32 v15, v14, v17
	v_min_f32_e32 v14, v14, v17
	v_max_f32_e32 v17, v9, v8
	v_min_f32_e32 v8, v9, v8
	v_max_f32_e32 v9, v1, v4
	v_min_f32_e32 v24, v1, v4
	v_max_f32_e32 v27, v5, v0
	v_min_f32_e32 v28, v5, v0
	v_max_f32_e32 v29, v10, v2
	v_min_f32_e32 v30, v10, v2
	v_max_f32_e32 v0, v12, v15
	v_min_f32_e32 v1, v12, v15
	v_max_f32_e32 v2, v11, v17
	v_min_f32_e32 v4, v11, v17
	v_min_f32_e32 v7, v18, v7
	v_max_f32_e32 v33, v0, v2
	v_min_f32_e32 v34, v0, v2
	v_min_f32_e32 v36, v1, v4
	v_max_f32_e32 v25, v6, v7
	v_min_f32_e32 v26, v6, v7
	v_max_f32_e32 v35, v1, v4
	v_lshrrev_b32_e32 v0, 2, v33
	v_lshrrev_b32_e32 v2, 2, v34
	v_lshrrev_b32_e32 v6, 2, v36
	v_max_f32_e32 v17, v3, v14
	v_min_f32_e32 v31, v3, v14
	v_and_b32_e32 v0, 60, v0
	v_and_b32_e32 v1, 15, v33
	v_and_b32_e32 v2, 60, v2
	v_and_b32_e32 v3, 15, v34
	v_lshrrev_b32_e32 v4, 2, v35
	v_and_b32_e32 v5, 15, v35
	v_and_b32_e32 v6, 60, v6
	v_and_b32_e32 v7, 15, v36
	s_waitcnt lgkmcnt(0)
	v_add_u32_e32 v0, v16, v0
	v_lshl_add_u32 v1, v1, 2, v16
	v_add_u32_e32 v2, v16, v2
	v_lshl_add_u32 v3, v3, 2, v16
	v_and_b32_e32 v4, 60, v4
	v_lshl_add_u32 v5, v5, 2, v16
	v_add_u32_e32 v6, v16, v6
	v_lshl_add_u32 v7, v7, 2, v16
	v_add_u32_e32 v4, v16, v4
	ds_read_b32 v0, v0
	ds_read_b32 v1, v1 offset:64
	ds_read_b32 v2, v2
	ds_read_b32 v3, v3 offset:64
	ds_read_b32 v10, v4
	ds_read_b32 v5, v5 offset:64
	ds_read_b32 v6, v6
	ds_read_b32 v7, v7 offset:64
	s_waitcnt lgkmcnt(0)
	v_lshl_add_u32 v0, v0, 7, v1
	v_ashrrev_i32_e32 v1, 31, v0
	v_lshl_add_u32 v4, v2, 7, v3
	v_lshlrev_b64 v[14:15], 2, v[0:1]
	v_lshl_add_u32 v10, v10, 7, v5
	v_lshl_add_u32 v12, v6, 7, v7
	v_lshl_add_u64 v[2:3], s[8:9], 0, v[14:15]
	v_ashrrev_i32_e32 v5, 31, v4
	v_max_f32_e32 v32, v13, v8
	v_min_f32_e32 v8, v13, v8
	global_load_dword v1, v[2:3], off
	v_lshlrev_b64 v[18:19], 2, v[4:5]
	v_ashrrev_i32_e32 v11, 31, v10
	v_ashrrev_i32_e32 v13, 31, v12
	v_lshl_add_u64 v[2:3], s[8:9], 0, v[18:19]
	v_lshlrev_b64 v[20:21], 2, v[10:11]
	v_lshlrev_b64 v[22:23], 2, v[12:13]
	v_lshl_add_u64 v[6:7], s[8:9], 0, v[20:21]
	global_load_dword v5, v[2:3], off
	global_load_dword v11, v[6:7], off
	v_lshl_add_u64 v[2:3], s[8:9], 0, v[22:23]
	global_load_dword v13, v[2:3], off
	v_min_f32_e32 v2, v9, v27
	v_min_f32_e32 v6, v25, v29
	v_max_f32_e32 v43, v2, v6
	v_min_f32_e32 v44, v2, v6
	v_and_b32_e32 v2, 0xffffff00, v34
	v_and_b32_e32 v51, 0xffffff00, v33
	v_max_f32_e32 v37, v9, v27
	v_max_f32_e32 v3, v25, v29
	v_sub_f32_e32 v2, v2, v51
	v_min_f32_e32 v9, v24, v28
	v_min_f32_e32 v25, v26, v30
	v_max_f32_e32 v41, v37, v3
	v_min_f32_e32 v42, v37, v3
	v_and_b32_e32 v3, 0xffffff00, v35
	v_mul_f32_e32 v2, 0x3fb8aa3b, v2
	v_max_f32_e32 v47, v9, v25
	v_min_f32_e32 v48, v9, v25
	v_exp_f32_e32 v25, v2
	v_sub_f32_e32 v2, v3, v51
	v_and_b32_e32 v6, 0xffffff00, v36
	v_mul_f32_e32 v2, 0x3fb8aa3b, v2
	v_max_f32_e32 v7, v24, v28
	v_max_f32_e32 v24, v26, v30
	v_max_f32_e32 v38, v17, v32
	v_exp_f32_e32 v26, v2
	v_sub_f32_e32 v2, v6, v51
	v_max_f32_e32 v45, v7, v24
	v_min_f32_e32 v46, v7, v24
	v_and_b32_e32 v7, 0xffffff00, v38
	v_mul_f32_e32 v2, 0x3fb8aa3b, v2
	v_min_f32_e32 v17, v17, v32
	v_exp_f32_e32 v27, v2
	v_sub_f32_e32 v2, v7, v51
	v_max_f32_e32 v39, v31, v8
	v_min_f32_e32 v40, v31, v8
	v_and_b32_e32 v8, 0xffffff00, v17
	v_mul_f32_e32 v2, 0x3fb8aa3b, v2
	v_exp_f32_e32 v28, v2
	v_sub_f32_e32 v2, v8, v51
	v_and_b32_e32 v9, 0xffffff00, v39
	v_mul_f32_e32 v2, 0x3fb8aa3b, v2
	v_exp_f32_e32 v29, v2
	v_sub_f32_e32 v2, v9, v51
	v_and_b32_e32 v31, 0xffffff00, v40
	v_mul_f32_e32 v2, 0x3fb8aa3b, v2
	v_exp_f32_e32 v30, v2
	v_sub_f32_e32 v2, v31, v51
	v_and_b32_e32 v32, 0xffffff00, v41
	v_mul_f32_e32 v2, 0x3fb8aa3b, v2
	v_exp_f32_e32 v31, v2
	v_sub_f32_e32 v2, v32, v51
	v_and_b32_e32 v34, 0xffffff00, v42
	v_mul_f32_e32 v2, 0x3fb8aa3b, v2
	v_exp_f32_e32 v6, v2
	v_sub_f32_e32 v2, v34, v51
	v_and_b32_e32 v35, 0xffffff00, v43
	v_mul_f32_e32 v2, 0x3fb8aa3b, v2
	v_exp_f32_e32 v7, v2
	v_sub_f32_e32 v2, v35, v51
	v_mul_f32_e32 v2, 0x3fb8aa3b, v2
	v_exp_f32_e32 v8, v2
	v_lshl_or_b32 v2, s18, 8, v128
	v_ashrrev_i32_e32 v3, 31, v2
	s_lshl_b64 s[4:5], s[16:17], 18
	s_mov_b32 s3, 0x7fc000
	v_lshl_add_u64 v[32:33], v[2:3], 4, s[4:5]
	v_sub_f32_e32 v24, v51, v51
	v_mul_f32_e32 v24, 0x3fb8aa3b, v24
	v_exp_f32_e32 v24, v24
	s_waitcnt vmcnt(0)
; #define RT_PK(q_) (ex[q_] | (int)((__float_as_uint(usc[ex[q_]]) >> 23) << 14))
;     __device__ __forceinline__ void fused(f32x4 (&acc)[2][2][4][2], const Unit& u, int wr, int wc, int fr, int fq, PG8_LAS unsigned char* lds, int wid, int lane) const {
;     ...
;             for (int q = 0; q < 16; ++q) { sc[q] = __builtin_amdgcn_exp2f((sc[q] - smax) * 1.4426950408889634f); }
; #pragma unroll
;             for (int q = 0; q < 16; ++q) sum += sc[q];
;             const float rs = 1.0f / sum;
;             asm volatile("s_waitcnt lgkmcnt(0)" ::: "memory");
;             int ex[16];
; #pragma unroll
;             for (int q = 0; q < 16; ++q) { const unsigned cid = __float_as_uint(best[q]) & 255u; ex[q] = idxl[cid >> 4] * 128 + idxl[16 + (cid & 15u)]; }
;             const size_t o = ((size_t)u.pn * 16384 + (size_t)(u.pm * BM + row)) * 16;
;             typedef int i32x4 __attribute__((ext_vector_type(4)));
; #pragma unroll
;             for (int i = 0; i < 4; ++i) {
;     ...
;                 *(i32x4*)(eidx + o + 4 * i) = (i32x4){RT_PK(4 * i), RT_PK(4 * i + 1), RT_PK(4 * i + 2), RT_PK(4 * i + 3)};
;                 *(f32x4*)(egate + o + 4 * i) = (f32x4){sc[4 * i] * rs * vsc[ex[4 * i]], sc[4 * i + 1] * rs * vsc[ex[4 * i + 1]], sc[4 * i + 2] * rs * vsc[ex[4 * i + 2]], sc[4 * i + 3] * rs * vsc[ex[4 * i + 3]]};
	v_lshrrev_b32_e32 v1, 9, v1
	v_and_or_b32 v2, v1, s3, v0
	v_and_b32_e32 v36, 0xffffff00, v44
	v_and_b32_e32 v37, 0xffffff00, v45
	v_and_b32_e32 v49, 0xffffff00, v46
	v_and_b32_e32 v50, 0xffffff00, v47
	v_and_b32_e32 v52, 0xffffff00, v48
	v_lshrrev_b32_e32 v0, 9, v5
	v_and_or_b32 v3, v0, s3, v4
	v_lshrrev_b32_e32 v0, 9, v11
	v_and_or_b32 v4, v0, s3, v10
	v_lshrrev_b32_e32 v0, 9, v13
	v_and_or_b32 v5, v0, s3, v12
	v_lshlrev_b64 v[12:13], 2, v[32:33]
	v_lshl_add_u64 v[0:1], s[12:13], 0, v[12:13]
	global_store_dwordx4 v[0:1], v[2:5], off
	v_lshl_add_u64 v[10:11], s[6:7], 0, v[20:21]
	v_lshrrev_b32_e32 v32, 2, v40
	v_lshl_add_u64 v[2:3], s[6:7], 0, v[14:15]
	v_lshl_add_u64 v[4:5], s[6:7], 0, v[18:19]
	v_lshl_add_u64 v[14:15], s[6:7], 0, v[22:23]
	global_load_dword v18, v[2:3], off
	global_load_dword v19, v[4:5], off
	global_load_dword v20, v[10:11], off
	global_load_dword v21, v[14:15], off
	v_add_f32_e32 v10, 0, v24
	v_add_f32_e32 v10, v25, v10
	v_add_f32_e32 v10, v26, v10
	v_add_f32_e32 v10, v27, v10
	v_sub_f32_e32 v2, v36, v51
	v_add_f32_e32 v10, v28, v10
	v_mul_f32_e32 v2, 0x3fb8aa3b, v2
	v_add_f32_e32 v10, v29, v10
	v_exp_f32_e32 v9, v2
	v_sub_f32_e32 v2, v37, v51
	v_add_f32_e32 v10, v30, v10
	v_mul_f32_e32 v2, 0x3fb8aa3b, v2
	v_sub_f32_e32 v3, v49, v51
	v_add_f32_e32 v10, v31, v10
	v_exp_f32_e32 v2, v2
	v_mul_f32_e32 v3, 0x3fb8aa3b, v3
	v_sub_f32_e32 v4, v50, v51
	v_add_f32_e32 v10, v6, v10
	v_exp_f32_e32 v3, v3
	v_mul_f32_e32 v4, 0x3fb8aa3b, v4
	v_sub_f32_e32 v5, v52, v51
	v_add_f32_e32 v10, v7, v10
	v_exp_f32_e32 v4, v4
	v_mul_f32_e32 v5, 0x3fb8aa3b, v5
	v_add_f32_e32 v10, v8, v10
	v_exp_f32_e32 v5, v5
	v_add_f32_e32 v10, v9, v10
	v_add_f32_e32 v10, v2, v10
	v_lshrrev_b32_e32 v11, 2, v38
	v_lshrrev_b32_e32 v15, 2, v17
	v_add_f32_e32 v10, v3, v10
	v_and_b32_e32 v11, 60, v11
	v_and_b32_e32 v14, 15, v38
	v_and_b32_e32 v15, 60, v15
	v_and_b32_e32 v17, 15, v17
	v_lshrrev_b32_e32 v22, 2, v39
	v_and_b32_e32 v23, 15, v39
	v_and_b32_e32 v33, 15, v40
	v_add_f32_e32 v10, v4, v10
	v_add_u32_e32 v11, v16, v11
	v_lshl_add_u32 v14, v14, 2, v16
	v_add_u32_e32 v15, v16, v15
	v_lshl_add_u32 v17, v17, 2, v16
	v_and_b32_e32 v22, 60, v22
	v_lshl_add_u32 v23, v23, 2, v16
	v_and_b32_e32 v32, 60, v32
	v_lshl_add_u32 v33, v33, 2, v16
	v_add_f32_e32 v10, v5, v10
	v_add_u32_e32 v22, v16, v22
	v_add_u32_e32 v32, v16, v32
	ds_read_b32 v11, v11
	ds_read_b32 v14, v14 offset:64
	ds_read_b32 v15, v15
	ds_read_b32 v17, v17 offset:64
	ds_read_b32 v34, v22
	ds_read_b32 v23, v23 offset:64
	ds_read_b32 v35, v32
	ds_read_b32 v33, v33 offset:64
	s_waitcnt lgkmcnt(6)
	v_lshl_add_u32 v14, v11, 7, v14
	v_div_scale_f32 v11, s[4:5], v10, v10, 1.0
	v_rcp_f32_e32 v36, v11
	s_waitcnt lgkmcnt(4)
	v_lshl_add_u32 v22, v15, 7, v17
	s_waitcnt lgkmcnt(2)
	v_lshl_add_u32 v32, v34, 7, v23
	s_waitcnt lgkmcnt(0)
	v_lshl_add_u32 v34, v35, 7, v33
	v_fma_f32 v15, -v11, v36, 1.0
	v_fmac_f32_e32 v36, v15, v36
	v_div_scale_f32 v15, vcc, 1.0, v10, 1.0
	v_mul_f32_e32 v17, v15, v36
	v_fma_f32 v23, -v11, v17, v15
	v_fmac_f32_e32 v17, v23, v36
	v_fma_f32 v11, -v11, v17, v15
	v_div_fmas_f32 v11, v11, v36, v17
	v_div_fixup_f32 v10, v11, v10, 1.0
	v_pk_mul_f32 v[24:25], v[24:25], v[10:11] op_sel_hi:[1,0]
	v_pk_mul_f32 v[26:27], v[26:27], v[10:11] op_sel_hi:[1,0]
	v_ashrrev_i32_e32 v15, 31, v14
	v_ashrrev_i32_e32 v33, 31, v32
	v_lshl_add_u64 v[12:13], s[10:11], 0, v[12:13]
	v_ashrrev_i32_e32 v23, 31, v22
	v_lshlrev_b64 v[36:37], 2, v[32:33]
	v_lshl_add_u64 v[38:39], s[8:9], 0, v[36:37]
	v_ashrrev_i32_e32 v35, 31, v34
	s_waitcnt vmcnt(2)
	v_pk_mul_f32 v[18:19], v[24:25], v[18:19]
	v_lshlrev_b64 v[24:25], 2, v[14:15]
	s_waitcnt vmcnt(0)
	v_pk_mul_f32 v[20:21], v[26:27], v[20:21]
	global_store_dwordx4 v[12:13], v[18:21], off
	v_lshlrev_b64 v[26:27], 2, v[22:23]
	s_nop 0
	v_lshl_add_u64 v[18:19], s[8:9], 0, v[24:25]
	v_lshl_add_u64 v[20:21], s[8:9], 0, v[26:27]
	global_load_dword v11, v[18:19], off
	global_load_dword v15, v[20:21], off
	global_load_dword v17, v[38:39], off
	v_lshlrev_b64 v[38:39], 2, v[34:35]
	v_lshl_add_u64 v[18:19], s[8:9], 0, v[38:39]
	global_load_dword v21, v[18:19], off
	s_waitcnt vmcnt(3)
	v_lshrrev_b32_e32 v11, 9, v11
	v_and_or_b32 v18, v11, s3, v14
	s_waitcnt vmcnt(2)
	v_lshrrev_b32_e32 v11, 9, v15
	v_and_or_b32 v19, v11, s3, v22
	s_waitcnt vmcnt(1)
	v_lshrrev_b32_e32 v11, 9, v17
	v_and_or_b32 v20, v11, s3, v32
	s_waitcnt vmcnt(0)
	v_lshrrev_b32_e32 v11, 9, v21
	v_and_or_b32 v21, v11, s3, v34
	global_store_dwordx4 v[0:1], v[18:21], off offset:16
	v_lshl_add_u64 v[14:15], s[6:7], 0, v[24:25]
	v_lshl_add_u64 v[22:23], s[6:7], 0, v[38:39]
	v_lshl_add_u64 v[18:19], s[6:7], 0, v[26:27]
	v_lshl_add_u64 v[20:21], s[6:7], 0, v[36:37]
	global_load_dword v24, v[14:15], off
	global_load_dword v26, v[20:21], off
	global_load_dword v27, v[22:23], off
	global_load_dword v25, v[18:19], off
	v_lshrrev_b32_e32 v11, 2, v41
	v_lshrrev_b32_e32 v15, 2, v42
	v_lshrrev_b32_e32 v18, 2, v43
	v_lshrrev_b32_e32 v20, 2, v44
	v_and_b32_e32 v11, 60, v11
	v_and_b32_e32 v14, 15, v41
	v_and_b32_e32 v15, 60, v15
	v_and_b32_e32 v17, 15, v42
	v_and_b32_e32 v18, 60, v18
	v_and_b32_e32 v19, 15, v43
	v_and_b32_e32 v20, 60, v20
	v_and_b32_e32 v21, 15, v44
	v_add_u32_e32 v11, v16, v11
	v_lshl_add_u32 v14, v14, 2, v16
	v_add_u32_e32 v15, v16, v15
	v_lshl_add_u32 v17, v17, 2, v16
	v_add_u32_e32 v18, v16, v18
	v_lshl_add_u32 v19, v19, 2, v16
	v_add_u32_e32 v20, v16, v20
	v_lshl_add_u32 v21, v21, 2, v16
	ds_read_b32 v11, v11
	ds_read_b32 v14, v14 offset:64
	ds_read_b32 v15, v15
	ds_read_b32 v17, v17 offset:64
	ds_read_b32 v18, v18
	ds_read_b32 v19, v19 offset:64
	ds_read_b32 v20, v20
	ds_read_b32 v21, v21 offset:64
	s_waitcnt lgkmcnt(6)
; #define RT_PK(q_) (ex[q_] | (int)((__float_as_uint(usc[ex[q_]]) >> 23) << 14))
;     __device__ __forceinline__ void fused(f32x4 (&acc)[2][2][4][2], const Unit& u, int wr, int wc, int fr, int fq, PG8_LAS unsigned char* lds, int wid, int lane) const {
;     ...
;             for (int q = 0; q < 16; ++q) { const unsigned cid = __float_as_uint(best[q]) & 255u; ex[q] = idxl[cid >> 4] * 128 + idxl[16 + (cid & 15u)]; }
;             const size_t o = ((size_t)u.pn * 16384 + (size_t)(u.pm * BM + row)) * 16;
;             typedef int i32x4 __attribute__((ext_vector_type(4)));
; #pragma unroll
;             for (int i = 0; i < 4; ++i) {
;     ...
;                 *(i32x4*)(eidx + o + 4 * i) = (i32x4){RT_PK(4 * i), RT_PK(4 * i + 1), RT_PK(4 * i + 2), RT_PK(4 * i + 3)};
;                 *(f32x4*)(egate + o + 4 * i) = (f32x4){sc[4 * i] * rs * vsc[ex[4 * i]], sc[4 * i + 1] * rs * vsc[ex[4 * i + 1]], sc[4 * i + 2] * rs * vsc[ex[4 * i + 2]], sc[4 * i + 3] * rs * vsc[ex[4 * i + 3]]};
	v_lshl_add_u32 v14, v11, 7, v14
	s_waitcnt lgkmcnt(4)
	v_lshl_add_u32 v22, v15, 7, v17
	s_waitcnt lgkmcnt(2)
	v_lshl_add_u32 v32, v18, 7, v19
	v_pk_mul_f32 v[18:19], v[28:29], v[10:11] op_sel_hi:[1,0]
	s_waitcnt lgkmcnt(0)
	v_lshl_add_u32 v34, v20, 7, v21
	v_pk_mul_f32 v[20:21], v[30:31], v[10:11] op_sel_hi:[1,0]
	v_ashrrev_i32_e32 v15, 31, v14
	v_ashrrev_i32_e32 v33, 31, v32
	v_ashrrev_i32_e32 v23, 31, v22
	v_lshlrev_b64 v[28:29], 2, v[32:33]
	v_lshl_add_u64 v[30:31], s[8:9], 0, v[28:29]
	v_ashrrev_i32_e32 v35, 31, v34
	s_waitcnt vmcnt(1)
	v_pk_mul_f32 v[20:21], v[20:21], v[26:27]
	s_waitcnt vmcnt(0)
	v_pk_mul_f32 v[18:19], v[18:19], v[24:25]
	v_lshlrev_b64 v[24:25], 2, v[14:15]
	global_store_dwordx4 v[12:13], v[18:21], off offset:16
	v_lshlrev_b64 v[26:27], 2, v[22:23]
	s_nop 0
	v_lshl_add_u64 v[18:19], s[8:9], 0, v[24:25]
	v_lshl_add_u64 v[20:21], s[8:9], 0, v[26:27]
	global_load_dword v11, v[18:19], off
	global_load_dword v15, v[20:21], off
	global_load_dword v17, v[30:31], off
	v_lshlrev_b64 v[30:31], 2, v[34:35]
	v_lshl_add_u64 v[18:19], s[8:9], 0, v[30:31]
	global_load_dword v21, v[18:19], off
	s_waitcnt vmcnt(3)
	v_lshrrev_b32_e32 v11, 9, v11
	v_and_or_b32 v18, v11, s3, v14
	s_waitcnt vmcnt(2)
	v_lshrrev_b32_e32 v11, 9, v15
	v_and_or_b32 v19, v11, s3, v22
	s_waitcnt vmcnt(1)
	v_lshrrev_b32_e32 v11, 9, v17
	v_and_or_b32 v20, v11, s3, v32
	s_waitcnt vmcnt(0)
	v_lshrrev_b32_e32 v11, 9, v21
	v_and_or_b32 v21, v11, s3, v34
	global_store_dwordx4 v[0:1], v[18:21], off offset:32
	v_lshl_add_u64 v[14:15], s[6:7], 0, v[24:25]
	v_lshl_add_u64 v[22:23], s[6:7], 0, v[30:31]
	v_lshl_add_u64 v[18:19], s[6:7], 0, v[26:27]
	v_lshl_add_u64 v[20:21], s[6:7], 0, v[28:29]
	global_load_dword v24, v[14:15], off
	global_load_dword v26, v[20:21], off
	global_load_dword v27, v[22:23], off
	global_load_dword v25, v[18:19], off
	v_lshrrev_b32_e32 v11, 2, v45
	v_lshrrev_b32_e32 v15, 2, v46
	v_lshrrev_b32_e32 v18, 2, v47
	v_lshrrev_b32_e32 v20, 2, v48
	v_and_b32_e32 v11, 60, v11
	v_and_b32_e32 v14, 15, v45
	v_and_b32_e32 v15, 60, v15
	v_and_b32_e32 v17, 15, v46
	v_and_b32_e32 v18, 60, v18
	v_and_b32_e32 v19, 15, v47
	v_and_b32_e32 v20, 60, v20
	v_add_u32_e32 v11, v16, v11
	v_lshl_add_u32 v14, v14, 2, v16
	v_add_u32_e32 v15, v16, v15
	v_lshl_add_u32 v17, v17, 2, v16
	v_add_u32_e32 v18, v16, v18
	v_lshl_add_u32 v19, v19, 2, v16
	v_add_u32_e32 v20, v16, v20
	v_and_b32_e32 v21, 15, v48
	v_lshl_add_u32 v16, v21, 2, v16
	ds_read_b32 v11, v11
	ds_read_b32 v14, v14 offset:64
	ds_read_b32 v15, v15
	ds_read_b32 v17, v17 offset:64
	ds_read_b32 v18, v18
	ds_read_b32 v19, v19 offset:64
	ds_read_b32 v20, v20
	ds_read_b32 v21, v16 offset:64
	s_waitcnt lgkmcnt(6)
	v_lshl_add_u32 v14, v11, 7, v14
	s_waitcnt lgkmcnt(4)
	v_lshl_add_u32 v16, v15, 7, v17
	s_waitcnt lgkmcnt(2)
	v_lshl_add_u32 v18, v18, 7, v19
	v_pk_mul_f32 v[6:7], v[6:7], v[10:11] op_sel_hi:[1,0]
	v_pk_mul_f32 v[8:9], v[8:9], v[10:11] op_sel_hi:[1,0]
	v_ashrrev_i32_e32 v15, 31, v14
	v_ashrrev_i32_e32 v19, 31, v18
	s_waitcnt lgkmcnt(0)
	v_lshl_add_u32 v20, v20, 7, v21
	v_lshlrev_b64 v[22:23], 2, v[14:15]
	v_ashrrev_i32_e32 v17, 31, v16
	v_ashrrev_i32_e32 v21, 31, v20
	s_waitcnt vmcnt(1)
	v_pk_mul_f32 v[8:9], v[8:9], v[26:27]
	s_waitcnt vmcnt(0)
	v_pk_mul_f32 v[6:7], v[6:7], v[24:25]
	v_lshlrev_b64 v[26:27], 2, v[18:19]
	global_store_dwordx4 v[12:13], v[6:9], off offset:32
	v_lshlrev_b64 v[24:25], 2, v[16:17]
	v_lshl_add_u64 v[28:29], s[8:9], 0, v[26:27]
	v_lshl_add_u64 v[6:7], s[8:9], 0, v[22:23]
	v_lshl_add_u64 v[8:9], s[8:9], 0, v[24:25]
	global_load_dword v11, v[6:7], off
	global_load_dword v15, v[8:9], off
	global_load_dword v17, v[28:29], off
	v_lshlrev_b64 v[28:29], 2, v[20:21]
	v_lshl_add_u64 v[6:7], s[8:9], 0, v[28:29]
	global_load_dword v9, v[6:7], off
	s_waitcnt vmcnt(3)
	v_lshrrev_b32_e32 v6, 9, v11
	s_waitcnt vmcnt(2)
	v_lshrrev_b32_e32 v7, 9, v15
	s_waitcnt vmcnt(1)
	v_lshrrev_b32_e32 v8, 9, v17
	v_and_or_b32 v6, v6, s3, v14
	v_and_or_b32 v7, v7, s3, v16
	s_waitcnt vmcnt(0)
	v_lshrrev_b32_e32 v9, 9, v9
	v_and_or_b32 v8, v8, s3, v18
	v_and_or_b32 v9, v9, s3, v20
	global_store_dwordx4 v[0:1], v[6:9], off offset:48
	v_lshl_add_u64 v[0:1], s[6:7], 0, v[22:23]
	v_lshl_add_u64 v[14:15], s[6:7], 0, v[28:29]
	v_lshl_add_u64 v[6:7], s[6:7], 0, v[24:25]
	v_lshl_add_u64 v[8:9], s[6:7], 0, v[26:27]
	global_load_dword v16, v[0:1], off
	global_load_dword v18, v[8:9], off
	global_load_dword v19, v[14:15], off
	global_load_dword v17, v[6:7], off
	v_pk_mul_f32 v[0:1], v[2:3], v[10:11] op_sel_hi:[1,0]
	v_pk_mul_f32 v[2:3], v[4:5], v[10:11] op_sel_hi:[1,0]
	s_waitcnt vmcnt(0)
	v_pk_mul_f32 v[0:1], v[0:1], v[16:17]
	v_pk_mul_f32 v[2:3], v[2:3], v[18:19]
	global_store_dwordx4 v[12:13], v[0:3], off offset:48
